# v9 plus: attention next-ticket atomic made asynchronous (result consumed at unit end); SwiGLU8 tiles zero their accumulators with 8 zero-operand bf16 MFMAs at the end of the epilogue (overlapping the
# baseline (speedup 1.0000x reference)
.LBB0_805:
	v_bfe_u32 v18, v16, 4, 2
	s_lshl_b32 s23, s23, 5
	v_and_b32_e32 v17, 15, v16
	v_lshlrev_b32_e32 v19, 4, v18
	v_lshlrev_b32_e32 v16, 2, v16
	s_and_b32 s42, s23, 0x60
	v_lshl_or_b32 v149, s24, 6, v17
	v_lshl_or_b32 v17, v17, 6, v19
	s_lshl_b32 s24, s24, 13
	v_and_b32_e32 v16, 32, v16
	s_lshl_b32 s23, s42, 7
	s_add_i32 m0, s16, 0x18000
	v_lshl_add_u64 v[8:9], v[8:9], 0, s[56:57]
	v_bitop3_b32 v19, v17, s24, v16 bitop3:0xde
	v_bitop3_b32 v151, v17, s23, v16 bitop3:0xde
	s_waitcnt vmcnt(2)
	s_barrier
	global_load_lds_dwordx4 v[8:9], off
	v_lshl_add_u64 v[6:7], v[6:7], 0, s[56:57]
	s_add_i32 m0, s16, 0x1a000
	s_add_i32 s23, s16, 0x8000
	s_add_i32 s24, s16, 0xa000
	s_sext_i32_i16 s63, s34
	global_load_lds_dwordx4 v[6:7], off
	v_lshl_add_u64 v[2:3], v[2:3], 0, s[56:57]
	s_mov_b32 m0, s23
	s_add_u32 s34, s58, 0x40080
	global_load_lds_dwordx4 v[2:3], off
	v_lshl_add_u64 v[2:3], v[4:5], 0, s[56:57]
	s_mov_b32 m0, s24
	s_addc_u32 s35, s59, 0
	global_load_lds_dwordx4 v[2:3], off
	s_add_i32 m0, s16, 0x1c000
	v_lshl_add_u64 v[2:3], s[34:35], 0, v[166:167]
	global_load_lds_dwordx4 v[2:3], off
	v_lshl_add_u64 v[2:3], s[34:35], 0, v[134:135]
	s_add_i32 m0, s16, 0x1e000
	s_cmp_gt_i32 s13, 0
	global_load_lds_dwordx4 v[2:3], off
	v_lshlrev_b32_e32 v2, 18, v18
	v_mov_b32_e32 v3, v167
	v_lshl_add_u64 v[136:137], s[28:29], 0, v[2:3]
	v_lshlrev_b32_e32 v2, 14, v10
	v_and_b32_e32 v2, 0xffff8000, v2
	v_lshl_add_u32 v2, v11, 11, v2
	v_and_b32_e32 v3, 1, v10
	s_cselect_b64 s[34:35], -1, 0
	s_add_i32 s53, s13, -2
	v_lshl_or_b32 v2, v3, 6, v2
	s_cmpk_lt_u32 s36, 0x100
	v_lshl_add_u32 v138, v12, 1, v2
	v_lshlrev_b32_e32 v2, 14, v13
	s_cselect_b64 s[36:37], -1, 0
	s_waitcnt lgkmcnt(0)
	s_ashr_i32 s62, s1, 31
	v_and_b32_e32 v2, 0xffff8000, v2
	s_waitcnt vmcnt(6)
	s_cmp_gt_i32 s0, -1
	s_mul_i32 s40, s1, 0x7fffffff
	v_lshl_add_u32 v2, v14, 11, v2
	v_and_b32_e32 v3, 1, v13
	s_cselect_b64 s[38:39], -1, 0
	s_mul_hi_i32 s41, s1, 0x7fffffff
	s_add_u32 s40, s40, s0
	v_lshl_or_b32 v2, v3, 6, v2
	s_mov_b32 s25, 0
	s_addc_u32 s41, s41, 0
	v_lshl_or_b32 v153, v18, 3, s42
	v_mov_b32_e32 v139, v167
	v_lshl_add_u32 v140, v15, 1, v2
	v_mov_b32_e32 v141, v167
	v_add_u32_e32 v154, 0, v19
	s_barrier
	v_mov_b32_e32 v2, 0
	v_mov_b32_e32 v3, 0
	v_mov_b32_e32 v4, 0
	v_mov_b32_e32 v5, 0
	v_mov_b32_e32 v6, 0
	v_mov_b32_e32 v7, 0
	v_mov_b32_e32 v8, 0
	v_mov_b32_e32 v9, 0
	v_mov_b32_e32 v10, 0
	v_mov_b32_e32 v11, 0
	v_mov_b32_e32 v12, 0
	v_mov_b32_e32 v13, 0
	v_mov_b32_e32 v14, 0
	v_mov_b32_e32 v15, 0
	v_mov_b32_e32 v16, 0
	v_mov_b32_e32 v17, 0
	v_mov_b32_e32 v18, 0
	v_mov_b32_e32 v19, 0
	v_mov_b32_e32 v20, 0
	v_mov_b32_e32 v21, 0
	v_mov_b32_e32 v22, 0
	v_mov_b32_e32 v23, 0
	v_mov_b32_e32 v24, 0
	v_mov_b32_e32 v25, 0
	v_mov_b32_e32 v26, 0
	v_mov_b32_e32 v27, 0
	v_mov_b32_e32 v28, 0
	v_mov_b32_e32 v29, 0
	v_mov_b32_e32 v30, 0
	v_mov_b32_e32 v31, 0
	v_mov_b32_e32 v32, 0
	v_mov_b32_e32 v33, 0
	v_mov_b32_e32 v34, 0
	v_mov_b32_e32 v35, 0
	v_mov_b32_e32 v36, 0
	v_mov_b32_e32 v37, 0
	v_mov_b32_e32 v38, 0
	v_mov_b32_e32 v39, 0
	v_mov_b32_e32 v40, 0
	v_mov_b32_e32 v41, 0
	v_mov_b32_e32 v42, 0
	v_mov_b32_e32 v43, 0
	v_mov_b32_e32 v44, 0
	v_mov_b32_e32 v45, 0
	v_mov_b32_e32 v46, 0
	v_mov_b32_e32 v47, 0
	v_mov_b32_e32 v48, 0
	v_mov_b32_e32 v49, 0
	v_mov_b32_e32 v50, 0
	v_mov_b32_e32 v51, 0
	v_mov_b32_e32 v52, 0
	v_mov_b32_e32 v53, 0
	v_mov_b32_e32 v54, 0
	v_mov_b32_e32 v55, 0
	v_mov_b32_e32 v56, 0
	v_mov_b32_e32 v57, 0
	v_mov_b32_e32 v58, 0
	v_mov_b32_e32 v59, 0
	v_mov_b32_e32 v60, 0
	v_mov_b32_e32 v61, 0
	v_mov_b32_e32 v62, 0
	v_mov_b32_e32 v63, 0
	v_mov_b32_e32 v64, 0
	v_mov_b32_e32 v65, 0
	v_mov_b32_e32 v66, 0
	v_mov_b32_e32 v67, 0
	v_mov_b32_e32 v68, 0
	v_mov_b32_e32 v69, 0
	v_mov_b32_e32 v70, 0
	v_mov_b32_e32 v71, 0
	v_mov_b32_e32 v72, 0
	v_mov_b32_e32 v73, 0
	v_mov_b32_e32 v74, 0
	v_mov_b32_e32 v75, 0
	v_mov_b32_e32 v76, 0
	v_mov_b32_e32 v77, 0
	v_mov_b32_e32 v78, 0
	v_mov_b32_e32 v79, 0
	v_mov_b32_e32 v80, 0
	v_mov_b32_e32 v81, 0
	v_mov_b32_e32 v82, 0
	v_mov_b32_e32 v83, 0
	v_mov_b32_e32 v84, 0
	v_mov_b32_e32 v85, 0
	v_mov_b32_e32 v86, 0
	v_mov_b32_e32 v87, 0
	v_mov_b32_e32 v88, 0
	v_mov_b32_e32 v89, 0
	v_mov_b32_e32 v90, 0
	v_mov_b32_e32 v91, 0
	v_mov_b32_e32 v92, 0
	v_mov_b32_e32 v93, 0
	v_mov_b32_e32 v94, 0
	v_mov_b32_e32 v95, 0
	v_mov_b32_e32 v96, 0
	v_mov_b32_e32 v97, 0
	v_mov_b32_e32 v98, 0
	v_mov_b32_e32 v99, 0
	v_mov_b32_e32 v100, 0
	v_mov_b32_e32 v101, 0
	v_mov_b32_e32 v102, 0
	v_mov_b32_e32 v103, 0
	v_mov_b32_e32 v104, 0
	v_mov_b32_e32 v105, 0
	v_mov_b32_e32 v106, 0
	v_mov_b32_e32 v107, 0
	v_mov_b32_e32 v108, 0
	v_mov_b32_e32 v109, 0
	v_mov_b32_e32 v110, 0
	v_mov_b32_e32 v111, 0
	v_mov_b32_e32 v112, 0
	v_mov_b32_e32 v113, 0
	v_mov_b32_e32 v114, 0
	v_mov_b32_e32 v115, 0
	v_mov_b32_e32 v116, 0
	v_mov_b32_e32 v117, 0
	v_mov_b32_e32 v118, 0
	v_mov_b32_e32 v119, 0
	v_mov_b32_e32 v120, 0
	v_mov_b32_e32 v121, 0
	v_mov_b32_e32 v122, 0
	v_mov_b32_e32 v123, 0
	v_mov_b32_e32 v124, 0
	v_mov_b32_e32 v125, 0
	v_mov_b32_e32 v126, 0
	v_mov_b32_e32 v127, 0
	v_mov_b32_e32 v128, 0
	v_mov_b32_e32 v129, 0
	s_branch .LBB0_808

.LBB0_815:
	s_ashr_i32 s45, s44, 31
	s_lshl_b64 s[48:49], s[44:45], 19
	s_add_u32 s48, s8, s48
	s_addc_u32 s49, s10, s49
	s_ashr_i32 s43, s42, 31
	s_lshl_b64 s[50:51], s[42:43], 19
	s_add_u32 s50, s11, s50
	s_addc_u32 s51, s12, s51
	s_andn2_b64 vcc, exec, s[34:35]
	s_cbranch_vccnz .LBB0_823
	v_lshl_add_u32 v156, s52, 8, v149
	v_ashrrev_i32_e32 v157, 31, v156
	v_lshl_add_u64 v[158:159], v[156:157], 2, v[136:137]
	global_load_dword v244, v[158:159], off
	global_load_dword v245, v[158:159], off offset:64
	global_load_dword v246, v[158:159], off offset:128
	global_load_dword v247, v[158:159], off offset:192
	global_load_dword v248, v[158:159], off offset:512
	global_load_dword v249, v[158:159], off offset:576
	global_load_dword v250, v[158:159], off offset:640
	global_load_dword v251, v[158:159], off offset:704
	s_and_b64 s[60:61], s[46:47], exec
	s_cselect_b32 s43, s49, s55
	s_cselect_b32 s45, s48, s54
	s_cselect_b32 s64, s51, s59
	s_cselect_b32 s65, s50, s58
	s_add_u32 s66, s58, 0x100
	s_addc_u32 s68, s59, 0
	s_add_u32 s54, s54, 0x40080
	v_mov_b32_e32 v1, 0x3ecc95a3
	s_addc_u32 s55, s55, 0
	s_mov_b32 s58, 0
	v_mov_b32_e32 v2, 0
	v_mov_b32_e32 v3, 0

.LBB0_820:
	v_xor_b32_e32 v218, 16, v231
	v_and_b32_e32 v216, 64, v231
	v_add_u32_e32 v216, 64, v216
	v_xor_b32_e32 v217, 32, v231
	v_cmp_lt_i32_e32 vcc, v218, v216
	v_mov_b32_e32 v142, 0xbfb8aa3b
	v_mov_b32_e32 v143, 1.0
	v_cndmask_b32_e32 v218, v231, v218, vcc
	v_cmp_lt_i32_e32 vcc, v217, v216
	v_lshlrev_b32_e32 v218, 2, v218
	v_mov_b32_e32 v144, 0x41000000
	v_cndmask_b32_e32 v217, v231, v217, vcc
	v_lshlrev_b32_e32 v217, 2, v217
	ds_bpermute_b32 v160, v218, v244
	ds_bpermute_b32 v161, v218, v245
	ds_bpermute_b32 v162, v218, v246
	ds_bpermute_b32 v163, v218, v247
	ds_bpermute_b32 v170, v218, v248
	ds_bpermute_b32 v171, v218, v249
	ds_bpermute_b32 v172, v218, v250
	ds_bpermute_b32 v173, v218, v251
	v_lshl_add_u32 v221, s52, 8, v149
	v_lshl_or_b32 v220, s63, 7, v153
	v_mad_u32_u24 v219, v221, s33, v220
	s_waitcnt lgkmcnt(7)
	v_add_f32_e32 v244, v244, v160
	ds_bpermute_b32 v160, v217, v244
	s_waitcnt lgkmcnt(7)
	v_add_f32_e32 v245, v245, v161
	ds_bpermute_b32 v161, v217, v245
	s_waitcnt lgkmcnt(7)
	v_add_f32_e32 v246, v246, v162
	ds_bpermute_b32 v162, v217, v246
	s_waitcnt lgkmcnt(7)
	v_add_f32_e32 v247, v247, v163
	ds_bpermute_b32 v163, v217, v247
	s_waitcnt lgkmcnt(7)
	v_add_f32_e32 v248, v248, v170
	ds_bpermute_b32 v170, v217, v248
	s_waitcnt lgkmcnt(7)
	v_add_f32_e32 v249, v249, v171
	ds_bpermute_b32 v171, v217, v249
	s_waitcnt lgkmcnt(7)
	v_add_f32_e32 v250, v250, v172
	ds_bpermute_b32 v172, v217, v250
	s_waitcnt lgkmcnt(7)
	v_add_f32_e32 v251, v251, v173
	ds_bpermute_b32 v173, v217, v251
	s_waitcnt lgkmcnt(7)
	v_add_f32_e32 v244, v244, v160
	v_fmamk_f32 v244, v244, 0x3a800000, v224
	s_waitcnt lgkmcnt(6)
	v_add_f32_e32 v245, v245, v161
	v_fmamk_f32 v245, v245, 0x3a800000, v224
	s_waitcnt lgkmcnt(5)
	v_add_f32_e32 v246, v246, v162
	v_fmamk_f32 v246, v246, 0x3a800000, v224
	s_waitcnt lgkmcnt(4)
	v_add_f32_e32 v247, v247, v163
	v_fmamk_f32 v247, v247, 0x3a800000, v224
	s_waitcnt lgkmcnt(3)
	v_add_f32_e32 v248, v248, v170
	v_fmamk_f32 v248, v248, 0x3a800000, v224
	s_waitcnt lgkmcnt(2)
	v_add_f32_e32 v249, v249, v171
	v_fmamk_f32 v249, v249, 0x3a800000, v224
	s_waitcnt lgkmcnt(1)
	v_add_f32_e32 v250, v250, v172
	v_fmamk_f32 v250, v250, 0x3a800000, v224
	s_waitcnt lgkmcnt(0)
	v_add_f32_e32 v251, v251, v173
	v_fmamk_f32 v251, v251, 0x3a800000, v224
	v_rsq_f32_e32 v244, v244
	v_rsq_f32_e32 v245, v245
	v_rsq_f32_e32 v246, v246
	v_rsq_f32_e32 v247, v247
	v_rsq_f32_e32 v248, v248
	v_rsq_f32_e32 v249, v249
	v_rsq_f32_e32 v250, v250
	v_rsq_f32_e32 v251, v251
	v_mov_b32_e32 v156, 0
	v_mov_b32_e32 v157, 0
	v_mov_b32_e32 v158, 0
	v_mov_b32_e32 v159, 0
	v_pk_mul_f32 v[160:161], v[126:127], v[244:245] op_sel_hi:[1,0]
	v_pk_mul_f32 v[162:163], v[128:129], v[244:245] op_sel_hi:[1,0]
	v_pk_mul_f32 v[170:171], v[118:119], v[244:245] op_sel_hi:[1,0]
	v_pk_mul_f32 v[172:173], v[160:161], v[142:143] op_sel_hi:[1,0]
	v_pk_mul_f32 v[174:175], v[162:163], v[142:143] op_sel_hi:[1,0]
	v_pk_mul_f32 v[176:177], v[170:171], v[142:143] op_sel_hi:[1,0]
	v_exp_f32_e32 v172, v172
	v_pk_mul_f32 v[178:179], v[120:121], v[244:245] op_sel_hi:[1,0]
	v_exp_f32_e32 v174, v174
	v_pk_mul_f32 v[180:181], v[110:111], v[244:245] op_sel:[0,1] op_sel_hi:[1,1]
	v_exp_f32_e32 v176, v176
	v_pk_mul_f32 v[182:183], v[178:179], v[142:143] op_sel_hi:[1,0]
	v_pk_mul_f32 v[184:185], v[180:181], v[142:143] op_sel_hi:[1,0]
	v_pk_mul_f32 v[186:187], v[112:113], v[244:245] op_sel:[0,1] op_sel_hi:[1,1]
	v_exp_f32_e32 v182, v182
	v_pk_mul_f32 v[188:189], v[102:103], v[244:245] op_sel:[0,1] op_sel_hi:[1,1]
	v_exp_f32_e32 v173, v173
	v_pk_mul_f32 v[190:191], v[186:187], v[142:143] op_sel_hi:[1,0]
	v_exp_f32_e32 v175, v175
	v_pk_mul_f32 v[192:193], v[188:189], v[142:143] op_sel_hi:[1,0]
	v_exp_f32_e32 v177, v177
	v_pk_mul_f32 v[194:195], v[104:105], v[244:245] op_sel:[0,1] op_sel_hi:[1,1]
	v_exp_f32_e32 v183, v183
	v_pk_mul_f32 v[196:197], v[122:123], v[244:245] op_sel_hi:[1,0]
	v_pk_add_f32 v[172:173], v[172:173], v[142:143] op_sel:[0,1] op_sel_hi:[1,1]
	v_exp_f32_e32 v184, v184
	v_pk_add_f32 v[174:175], v[174:175], v[142:143] op_sel:[0,1] op_sel_hi:[1,1]
	v_rcp_f32_e32 v172, v172
	v_pk_add_f32 v[176:177], v[176:177], v[142:143] op_sel:[0,1] op_sel_hi:[1,1]
	v_rcp_f32_e32 v174, v174
	v_pk_add_f32 v[182:183], v[182:183], v[142:143] op_sel:[0,1] op_sel_hi:[1,1]
	v_rcp_f32_e32 v176, v176
	v_pk_mul_f32 v[198:199], v[194:195], v[142:143] op_sel_hi:[1,0]
	v_rcp_f32_e32 v182, v182
	v_pk_mul_f32 v[196:197], v[196:197], v[160:161]
	v_exp_f32_e32 v190, v190
	v_pk_mul_f32 v[160:161], v[124:125], v[244:245] op_sel_hi:[1,0]
	v_exp_f32_e32 v192, v192
	v_pk_mul_f32 v[200:201], v[114:115], v[244:245] op_sel_hi:[1,0]
	v_rcp_f32_e32 v173, v173
	v_pk_mul_f32 v[202:203], v[94:95], v[246:247] op_sel_hi:[1,0]
	v_exp_f32_e32 v198, v198
	v_pk_mul_f32 v[160:161], v[160:161], v[162:163]
	v_rcp_f32_e32 v175, v175
	v_pk_mul_f32 v[200:201], v[200:201], v[170:171]
	v_rcp_f32_e32 v177, v177
	v_pk_mul_f32 v[162:163], v[116:117], v[244:245] op_sel_hi:[1,0]
	v_exp_f32_e32 v185, v185
	v_pk_mul_f32 v[196:197], v[196:197], v[172:173]
	v_rcp_f32_e32 v183, v183
	v_pk_mul_f32 v[170:171], v[202:203], v[142:143] op_sel_hi:[1,0]
	v_exp_f32_e32 v191, v191
	v_pk_mul_f32 v[196:197], v[196:197], v[144:145] op_sel_hi:[1,0]
	v_exp_f32_e32 v193, v193
	v_pk_mul_f32 v[160:161], v[160:161], v[174:175]
	v_exp_f32_e32 v199, v199
	v_pk_mul_f32 v[200:201], v[200:201], v[176:177]
	v_pk_add_f32 v[184:185], v[184:185], v[142:143] op_sel:[0,1] op_sel_hi:[1,1]
	v_med3_f32 v196, v196, s87, v227
	v_pk_mul_f32 v[160:161], v[160:161], v[144:145] op_sel_hi:[1,0]
	v_pk_mul_f32 v[200:201], v[200:201], v[144:145] op_sel_hi:[1,0]
	v_rcp_f32_e32 v184, v184
	v_pk_add_f32 v[190:191], v[190:191], v[142:143] op_sel:[0,1] op_sel_hi:[1,1]
	v_pk_add_f32 v[192:193], v[192:193], v[142:143] op_sel:[0,1] op_sel_hi:[1,1]
	v_pk_mul_f32 v[172:173], v[96:97], v[246:247] op_sel_hi:[1,0]
	v_pk_mul_f32 v[174:175], v[86:87], v[246:247] op_sel_hi:[1,0]
	v_med3_f32 v197, v197, s87, v227
	v_med3_f32 v160, v160, s87, v227
	v_med3_f32 v200, v200, s87, v227
	v_pk_mul_f32 v[162:163], v[162:163], v[178:179]
	v_rcp_f32_e32 v190, v190
	v_pk_add_f32 v[198:199], v[198:199], v[142:143] op_sel:[0,1] op_sel_hi:[1,1]
	v_pk_mul_f32 v[162:163], v[162:163], v[182:183]
	v_rcp_f32_e32 v192, v192
	v_pk_mul_f32 v[176:177], v[172:173], v[142:143] op_sel_hi:[1,0]
	v_pk_mul_f32 v[162:163], v[162:163], v[144:145] op_sel_hi:[1,0]
	v_exp_f32_e32 v170, v170
	v_pk_mul_f32 v[178:179], v[174:175], v[142:143] op_sel_hi:[1,0]
	v_pk_mul_f32 v[182:183], v[88:89], v[246:247] op_sel_hi:[1,0]
	v_cvt_pk_fp8_f32 v196, v196, v197
	v_med3_f32 v161, v161, s87, v227
	v_med3_f32 v201, v201, s87, v227
	v_med3_f32 v162, v162, s87, v227
	v_rcp_f32_e32 v198, v198
	v_pk_mul_f32 v[204:205], v[182:183], v[142:143] op_sel_hi:[1,0]
	v_exp_f32_e32 v176, v176
	v_cvt_pk_fp8_f32 v196, v160, v161 op_sel:[0,0,1]
	v_exp_f32_e32 v178, v178
	v_cvt_pk_fp8_f32 v197, v200, v201
	v_rcp_f32_e32 v185, v185
	v_med3_f32 v163, v163, s87, v227
	v_exp_f32_e32 v204, v204
	v_pk_mul_f32 v[160:161], v[106:107], v[244:245] op_sel:[0,1] op_sel_hi:[1,1]
	v_rcp_f32_e32 v191, v191
	v_cvt_pk_fp8_f32 v197, v162, v163 op_sel:[0,0,1]
	v_rcp_f32_e32 v193, v193
	v_pk_mul_f32 v[160:161], v[160:161], v[180:181]
	v_exp_f32_e32 v171, v171
	global_store_dwordx2 v219, v[196:197], s[26:27]
	v_rcp_f32_e32 v199, v199
	v_pk_mul_f32 v[160:161], v[160:161], v[184:185]
	v_exp_f32_e32 v177, v177
	v_pk_mul_f32 v[162:163], v[108:109], v[244:245] op_sel:[0,1] op_sel_hi:[1,1]
	v_exp_f32_e32 v179, v179
	v_pk_mul_f32 v[160:161], v[160:161], v[144:145] op_sel_hi:[1,0]
	v_exp_f32_e32 v205, v205
	v_pk_mul_f32 v[180:181], v[98:99], v[244:245] op_sel:[0,1] op_sel_hi:[1,1]
	v_pk_add_f32 v[170:171], v[170:171], v[142:143] op_sel:[0,1] op_sel_hi:[1,1]
	v_pk_mul_f32 v[184:185], v[78:79], v[246:247] op_sel:[0,1] op_sel_hi:[1,1]
	v_med3_f32 v160, v160, s87, v227
	v_pk_mul_f32 v[162:163], v[162:163], v[186:187]
	v_pk_mul_f32 v[180:181], v[180:181], v[188:189]
	v_pk_mul_f32 v[186:187], v[100:101], v[244:245] op_sel:[0,1] op_sel_hi:[1,1]
	v_pk_mul_f32 v[162:163], v[162:163], v[190:191]
	v_pk_mul_f32 v[180:181], v[180:181], v[192:193]
	v_rcp_f32_e32 v170, v170
	v_pk_mul_f32 v[162:163], v[162:163], v[144:145] op_sel_hi:[1,0]
	v_pk_mul_f32 v[180:181], v[180:181], v[144:145] op_sel_hi:[1,0]
	v_pk_add_f32 v[176:177], v[176:177], v[142:143] op_sel:[0,1] op_sel_hi:[1,1]
	v_pk_add_f32 v[178:179], v[178:179], v[142:143] op_sel:[0,1] op_sel_hi:[1,1]
	v_pk_mul_f32 v[188:189], v[184:185], v[142:143] op_sel_hi:[1,0]
	v_pk_mul_f32 v[190:191], v[80:81], v[246:247] op_sel:[0,1] op_sel_hi:[1,1]
	v_pk_mul_f32 v[192:193], v[70:71], v[246:247] op_sel:[0,1] op_sel_hi:[1,1]
	v_med3_f32 v161, v161, s87, v227
	v_med3_f32 v162, v162, s87, v227
	v_med3_f32 v180, v180, s87, v227
	v_pk_mul_f32 v[186:187], v[186:187], v[194:195]
	v_rcp_f32_e32 v176, v176
	v_pk_add_f32 v[204:205], v[204:205], v[142:143] op_sel:[0,1] op_sel_hi:[1,1]
	v_pk_mul_f32 v[186:187], v[186:187], v[198:199]
	v_rcp_f32_e32 v178, v178
	v_pk_mul_f32 v[194:195], v[190:191], v[142:143] op_sel_hi:[1,0]
	v_pk_mul_f32 v[186:187], v[186:187], v[144:145] op_sel_hi:[1,0]
	v_exp_f32_e32 v188, v188
	v_pk_mul_f32 v[196:197], v[192:193], v[142:143] op_sel_hi:[1,0]
	v_pk_mul_f32 v[198:199], v[72:73], v[246:247] op_sel:[0,1] op_sel_hi:[1,1]
	v_cvt_pk_fp8_f32 v160, v160, v161
	v_med3_f32 v163, v163, s87, v227
	v_med3_f32 v181, v181, s87, v227
	v_med3_f32 v186, v186, s87, v227
	v_rcp_f32_e32 v204, v204
	v_pk_mul_f32 v[200:201], v[198:199], v[142:143] op_sel_hi:[1,0]
	v_exp_f32_e32 v194, v194
	v_cvt_pk_fp8_f32 v160, v162, v163 op_sel:[0,0,1]
	v_exp_f32_e32 v196, v196
	v_cvt_pk_fp8_f32 v161, v180, v181
	v_rcp_f32_e32 v171, v171
	v_med3_f32 v187, v187, s87, v227
	v_exp_f32_e32 v200, v200
	v_pk_mul_f32 v[162:163], v[90:91], v[246:247] op_sel_hi:[1,0]
	v_rcp_f32_e32 v177, v177
	v_cvt_pk_fp8_f32 v161, v186, v187 op_sel:[0,0,1]
	v_rcp_f32_e32 v179, v179
	v_pk_mul_f32 v[162:163], v[162:163], v[202:203]
	v_exp_f32_e32 v189, v189
	v_pk_mul_f32 v[180:181], v[92:93], v[246:247] op_sel_hi:[1,0]
	v_rcp_f32_e32 v205, v205
	v_pk_mul_f32 v[162:163], v[162:163], v[170:171]
	v_exp_f32_e32 v195, v195
	v_pk_mul_f32 v[170:171], v[82:83], v[246:247] op_sel_hi:[1,0]
	v_exp_f32_e32 v197, v197
	v_pk_mul_f32 v[162:163], v[162:163], v[144:145] op_sel_hi:[1,0]
	v_exp_f32_e32 v201, v201
	v_pk_add_f32 v[188:189], v[188:189], v[142:143] op_sel:[0,1] op_sel_hi:[1,1]
	v_pk_mul_f32 v[186:187], v[62:63], v[248:249] op_sel_hi:[1,0]
	v_med3_f32 v162, v162, s87, v227
	v_pk_mul_f32 v[180:181], v[180:181], v[172:173]
	v_pk_mul_f32 v[170:171], v[170:171], v[174:175]
	v_pk_mul_f32 v[172:173], v[84:85], v[246:247] op_sel_hi:[1,0]
	v_pk_mul_f32 v[180:181], v[180:181], v[176:177]
	v_pk_mul_f32 v[170:171], v[170:171], v[178:179]
	v_rcp_f32_e32 v188, v188
	v_pk_mul_f32 v[180:181], v[180:181], v[144:145] op_sel_hi:[1,0]
	v_pk_mul_f32 v[170:171], v[170:171], v[144:145] op_sel_hi:[1,0]
	v_pk_add_f32 v[194:195], v[194:195], v[142:143] op_sel:[0,1] op_sel_hi:[1,1]
	v_pk_add_f32 v[196:197], v[196:197], v[142:143] op_sel:[0,1] op_sel_hi:[1,1]
	v_pk_mul_f32 v[174:175], v[186:187], v[142:143] op_sel_hi:[1,0]
	v_pk_mul_f32 v[176:177], v[64:65], v[248:249] op_sel_hi:[1,0]
	v_pk_mul_f32 v[178:179], v[54:55], v[248:249] op_sel_hi:[1,0]
	v_med3_f32 v163, v163, s87, v227
	v_med3_f32 v180, v180, s87, v227
	v_med3_f32 v170, v170, s87, v227
	v_pk_mul_f32 v[172:173], v[172:173], v[182:183]
	v_rcp_f32_e32 v194, v194
	v_pk_add_f32 v[200:201], v[200:201], v[142:143] op_sel:[0,1] op_sel_hi:[1,1]
	v_pk_mul_f32 v[172:173], v[172:173], v[204:205]
	v_rcp_f32_e32 v196, v196
	v_pk_mul_f32 v[182:183], v[176:177], v[142:143] op_sel_hi:[1,0]
	v_pk_mul_f32 v[172:173], v[172:173], v[144:145] op_sel_hi:[1,0]
	v_exp_f32_e32 v174, v174
	v_pk_mul_f32 v[202:203], v[178:179], v[142:143] op_sel_hi:[1,0]
	v_pk_mul_f32 v[204:205], v[56:57], v[248:249] op_sel_hi:[1,0]
	v_cvt_pk_fp8_f32 v162, v162, v163
	v_med3_f32 v181, v181, s87, v227
	v_med3_f32 v171, v171, s87, v227
	v_med3_f32 v172, v172, s87, v227
	v_rcp_f32_e32 v200, v200
	v_pk_mul_f32 v[206:207], v[204:205], v[142:143] op_sel_hi:[1,0]
	v_exp_f32_e32 v182, v182
	v_cvt_pk_fp8_f32 v162, v180, v181 op_sel:[0,0,1]
	v_exp_f32_e32 v202, v202
	v_cvt_pk_fp8_f32 v163, v170, v171
	v_rcp_f32_e32 v189, v189
	v_med3_f32 v173, v173, s87, v227
	v_exp_f32_e32 v206, v206
	v_add_u32_e32 v170, 0xe000, v219
	v_rcp_f32_e32 v195, v195
	v_cvt_pk_fp8_f32 v163, v172, v173 op_sel:[0,0,1]
	global_store_dwordx2 v170, v[160:161], s[26:27]
	v_rcp_f32_e32 v197, v197
	v_pk_mul_f32 v[160:161], v[74:75], v[246:247] op_sel:[0,1] op_sel_hi:[1,1]
	v_exp_f32_e32 v175, v175
	v_pk_mul_f32 v[170:171], v[76:77], v[246:247] op_sel:[0,1] op_sel_hi:[1,1]
	v_rcp_f32_e32 v201, v201
	v_pk_mul_f32 v[160:161], v[160:161], v[184:185]
	v_exp_f32_e32 v183, v183
	v_pk_mul_f32 v[172:173], v[66:67], v[246:247] op_sel:[0,1] op_sel_hi:[1,1]
	v_exp_f32_e32 v203, v203
	v_pk_mul_f32 v[160:161], v[160:161], v[188:189]
	v_exp_f32_e32 v207, v207
	v_pk_add_f32 v[174:175], v[174:175], v[142:143] op_sel:[0,1] op_sel_hi:[1,1]
	v_pk_mul_f32 v[160:161], v[160:161], v[144:145] op_sel_hi:[1,0]
	v_pk_mul_f32 v[180:181], v[46:47], v[248:249] op_sel:[0,1] op_sel_hi:[1,1]
	v_pk_mul_f32 v[170:171], v[170:171], v[190:191]
	v_med3_f32 v160, v160, s87, v227
	v_pk_mul_f32 v[172:173], v[172:173], v[192:193]
	v_pk_mul_f32 v[170:171], v[170:171], v[194:195]
	v_pk_mul_f32 v[184:185], v[68:69], v[246:247] op_sel:[0,1] op_sel_hi:[1,1]
	v_pk_mul_f32 v[172:173], v[172:173], v[196:197]
	v_pk_mul_f32 v[170:171], v[170:171], v[144:145] op_sel_hi:[1,0]
	v_rcp_f32_e32 v174, v174
	v_pk_mul_f32 v[172:173], v[172:173], v[144:145] op_sel_hi:[1,0]
	v_pk_add_f32 v[182:183], v[182:183], v[142:143] op_sel:[0,1] op_sel_hi:[1,1]
	v_pk_add_f32 v[202:203], v[202:203], v[142:143] op_sel:[0,1] op_sel_hi:[1,1]
	v_pk_mul_f32 v[188:189], v[180:181], v[142:143] op_sel_hi:[1,0]
	v_pk_mul_f32 v[190:191], v[48:49], v[248:249] op_sel:[0,1] op_sel_hi:[1,1]
	v_pk_mul_f32 v[192:193], v[38:39], v[248:249] op_sel:[0,1] op_sel_hi:[1,1]
	v_med3_f32 v161, v161, s87, v227
	v_med3_f32 v170, v170, s87, v227
	v_med3_f32 v172, v172, s87, v227
	v_pk_mul_f32 v[184:185], v[184:185], v[198:199]
	v_rcp_f32_e32 v182, v182
	v_pk_add_f32 v[206:207], v[206:207], v[142:143] op_sel:[0,1] op_sel_hi:[1,1]
	v_pk_mul_f32 v[184:185], v[184:185], v[200:201]
	v_rcp_f32_e32 v202, v202
	v_pk_mul_f32 v[194:195], v[190:191], v[142:143] op_sel_hi:[1,0]
	v_pk_mul_f32 v[184:185], v[184:185], v[144:145] op_sel_hi:[1,0]
	v_exp_f32_e32 v188, v188
	v_pk_mul_f32 v[196:197], v[192:193], v[142:143] op_sel_hi:[1,0]
	v_pk_mul_f32 v[198:199], v[40:41], v[248:249] op_sel:[0,1] op_sel_hi:[1,1]
	v_cvt_pk_fp8_f32 v160, v160, v161
	v_med3_f32 v171, v171, s87, v227
	v_med3_f32 v173, v173, s87, v227
	v_med3_f32 v184, v184, s87, v227
	v_rcp_f32_e32 v206, v206
	v_pk_mul_f32 v[200:201], v[198:199], v[142:143] op_sel_hi:[1,0]
	v_exp_f32_e32 v194, v194
	v_cvt_pk_fp8_f32 v160, v170, v171 op_sel:[0,0,1]
	v_exp_f32_e32 v196, v196
	v_cvt_pk_fp8_f32 v161, v172, v173
	v_rcp_f32_e32 v175, v175
	v_med3_f32 v185, v185, s87, v227
	v_exp_f32_e32 v200, v200
	v_add_u32_e32 v170, 0x1c000, v219
	v_rcp_f32_e32 v183, v183
	v_cvt_pk_fp8_f32 v161, v184, v185 op_sel:[0,0,1]
	global_store_dwordx2 v170, v[162:163], s[26:27]
	v_rcp_f32_e32 v203, v203
	v_pk_mul_f32 v[162:163], v[58:59], v[248:249] op_sel_hi:[1,0]
	v_exp_f32_e32 v189, v189
	v_pk_mul_f32 v[170:171], v[60:61], v[248:249] op_sel_hi:[1,0]
	v_rcp_f32_e32 v207, v207
	v_pk_mul_f32 v[162:163], v[162:163], v[186:187]
	v_exp_f32_e32 v195, v195
	v_pk_mul_f32 v[172:173], v[50:51], v[248:249] op_sel_hi:[1,0]
	v_exp_f32_e32 v197, v197
	v_pk_mul_f32 v[162:163], v[162:163], v[174:175]
	v_exp_f32_e32 v201, v201
	v_pk_add_f32 v[188:189], v[188:189], v[142:143] op_sel:[0,1] op_sel_hi:[1,1]
	v_pk_mul_f32 v[162:163], v[162:163], v[144:145] op_sel_hi:[1,0]
	v_pk_mul_f32 v[174:175], v[30:31], v[250:251] op_sel_hi:[1,0]
	v_pk_mul_f32 v[170:171], v[170:171], v[176:177]
	v_med3_f32 v162, v162, s87, v227
	v_pk_mul_f32 v[172:173], v[172:173], v[178:179]
	v_pk_mul_f32 v[170:171], v[170:171], v[182:183]
	v_pk_mul_f32 v[176:177], v[52:53], v[248:249] op_sel_hi:[1,0]
	v_pk_mul_f32 v[172:173], v[172:173], v[202:203]
	v_pk_mul_f32 v[170:171], v[170:171], v[144:145] op_sel_hi:[1,0]
	v_rcp_f32_e32 v188, v188
	v_pk_mul_f32 v[172:173], v[172:173], v[144:145] op_sel_hi:[1,0]
	v_pk_add_f32 v[194:195], v[194:195], v[142:143] op_sel:[0,1] op_sel_hi:[1,1]
	v_pk_add_f32 v[196:197], v[196:197], v[142:143] op_sel:[0,1] op_sel_hi:[1,1]
	v_pk_mul_f32 v[178:179], v[174:175], v[142:143] op_sel_hi:[1,0]
	v_pk_mul_f32 v[182:183], v[32:33], v[250:251] op_sel_hi:[1,0]
	v_pk_mul_f32 v[184:185], v[22:23], v[250:251] op_sel_hi:[1,0]
	v_med3_f32 v163, v163, s87, v227
	v_med3_f32 v170, v170, s87, v227
	v_med3_f32 v172, v172, s87, v227
	v_pk_mul_f32 v[176:177], v[176:177], v[204:205]
	v_rcp_f32_e32 v194, v194
	v_pk_add_f32 v[200:201], v[200:201], v[142:143] op_sel:[0,1] op_sel_hi:[1,1]
	v_pk_mul_f32 v[176:177], v[176:177], v[206:207]
	v_rcp_f32_e32 v196, v196
	v_pk_mul_f32 v[186:187], v[182:183], v[142:143] op_sel_hi:[1,0]
	v_pk_mul_f32 v[176:177], v[176:177], v[144:145] op_sel_hi:[1,0]
	v_exp_f32_e32 v178, v178
	v_pk_mul_f32 v[202:203], v[184:185], v[142:143] op_sel_hi:[1,0]
	v_pk_mul_f32 v[204:205], v[24:25], v[250:251] op_sel_hi:[1,0]
	v_cvt_pk_fp8_f32 v162, v162, v163
	v_med3_f32 v171, v171, s87, v227
	v_med3_f32 v173, v173, s87, v227
	v_med3_f32 v176, v176, s87, v227
	v_rcp_f32_e32 v200, v200
	v_pk_mul_f32 v[206:207], v[204:205], v[142:143] op_sel_hi:[1,0]
	v_exp_f32_e32 v186, v186
	v_cvt_pk_fp8_f32 v162, v170, v171 op_sel:[0,0,1]
	v_exp_f32_e32 v202, v202
	v_cvt_pk_fp8_f32 v163, v172, v173
	v_rcp_f32_e32 v189, v189
	v_med3_f32 v177, v177, s87, v227
	v_exp_f32_e32 v206, v206
	v_add_u32_e32 v170, 0x2a000, v219
	v_rcp_f32_e32 v195, v195
	v_cvt_pk_fp8_f32 v163, v176, v177 op_sel:[0,0,1]
	global_store_dwordx2 v170, v[160:161], s[26:27]
	v_rcp_f32_e32 v197, v197
	v_pk_mul_f32 v[160:161], v[42:43], v[248:249] op_sel:[0,1] op_sel_hi:[1,1]
	v_exp_f32_e32 v179, v179
	v_pk_mul_f32 v[170:171], v[44:45], v[248:249] op_sel:[0,1] op_sel_hi:[1,1]
	v_rcp_f32_e32 v201, v201
	v_pk_mul_f32 v[160:161], v[160:161], v[180:181]
	v_exp_f32_e32 v187, v187
	v_pk_mul_f32 v[172:173], v[34:35], v[248:249] op_sel:[0,1] op_sel_hi:[1,1]
	v_exp_f32_e32 v203, v203
	v_pk_mul_f32 v[160:161], v[160:161], v[188:189]
	v_exp_f32_e32 v207, v207
	v_pk_add_f32 v[178:179], v[178:179], v[142:143] op_sel:[0,1] op_sel_hi:[1,1]
	v_pk_mul_f32 v[160:161], v[160:161], v[144:145] op_sel_hi:[1,0]
	v_pk_mul_f32 v[176:177], v[14:15], v[250:251] op_sel:[0,1] op_sel_hi:[1,1]
	v_pk_mul_f32 v[170:171], v[170:171], v[190:191]
	v_med3_f32 v160, v160, s87, v227
	v_pk_mul_f32 v[172:173], v[172:173], v[192:193]
	v_pk_mul_f32 v[170:171], v[170:171], v[194:195]
	v_pk_mul_f32 v[180:181], v[36:37], v[248:249] op_sel:[0,1] op_sel_hi:[1,1]
	v_pk_mul_f32 v[172:173], v[172:173], v[196:197]
	v_pk_mul_f32 v[170:171], v[170:171], v[144:145] op_sel_hi:[1,0]
	v_rcp_f32_e32 v178, v178
	v_pk_mul_f32 v[172:173], v[172:173], v[144:145] op_sel_hi:[1,0]
	v_pk_add_f32 v[186:187], v[186:187], v[142:143] op_sel:[0,1] op_sel_hi:[1,1]
	v_pk_add_f32 v[202:203], v[202:203], v[142:143] op_sel:[0,1] op_sel_hi:[1,1]
	v_pk_mul_f32 v[188:189], v[176:177], v[142:143] op_sel_hi:[1,0]
	v_pk_mul_f32 v[190:191], v[16:17], v[250:251] op_sel:[0,1] op_sel_hi:[1,1]
	v_pk_mul_f32 v[192:193], v[6:7], v[250:251] op_sel:[0,1] op_sel_hi:[1,1]
	v_med3_f32 v161, v161, s87, v227
	v_med3_f32 v170, v170, s87, v227
	v_med3_f32 v172, v172, s87, v227
	v_pk_mul_f32 v[180:181], v[180:181], v[198:199]
	v_rcp_f32_e32 v186, v186
	v_pk_add_f32 v[206:207], v[206:207], v[142:143] op_sel:[0,1] op_sel_hi:[1,1]
	v_pk_mul_f32 v[180:181], v[180:181], v[200:201]
	v_rcp_f32_e32 v202, v202
	v_pk_mul_f32 v[194:195], v[190:191], v[142:143] op_sel_hi:[1,0]
	v_pk_mul_f32 v[180:181], v[180:181], v[144:145] op_sel_hi:[1,0]
	v_exp_f32_e32 v188, v188
	v_pk_mul_f32 v[196:197], v[192:193], v[142:143] op_sel_hi:[1,0]
	v_pk_mul_f32 v[198:199], v[8:9], v[250:251] op_sel:[0,1] op_sel_hi:[1,1]
	v_cvt_pk_fp8_f32 v160, v160, v161
	v_med3_f32 v171, v171, s87, v227
	v_med3_f32 v173, v173, s87, v227
	v_med3_f32 v180, v180, s87, v227
	v_rcp_f32_e32 v206, v206
	v_pk_mul_f32 v[200:201], v[198:199], v[142:143] op_sel_hi:[1,0]
	v_exp_f32_e32 v194, v194
	v_cvt_pk_fp8_f32 v160, v170, v171 op_sel:[0,0,1]
	v_exp_f32_e32 v196, v196
	v_cvt_pk_fp8_f32 v161, v172, v173
	v_rcp_f32_e32 v179, v179
	v_med3_f32 v181, v181, s87, v227
	v_exp_f32_e32 v200, v200
	v_add_u32_e32 v170, 0x70000, v219
	v_rcp_f32_e32 v187, v187
	v_cvt_pk_fp8_f32 v161, v180, v181 op_sel:[0,0,1]
	global_store_dwordx2 v170, v[162:163], s[26:27]
	v_rcp_f32_e32 v203, v203
	v_pk_mul_f32 v[162:163], v[26:27], v[250:251] op_sel_hi:[1,0]
	v_exp_f32_e32 v189, v189
	v_pk_mul_f32 v[170:171], v[28:29], v[250:251] op_sel_hi:[1,0]
	v_rcp_f32_e32 v207, v207
	v_pk_mul_f32 v[162:163], v[162:163], v[174:175]
	v_exp_f32_e32 v195, v195
	v_pk_mul_f32 v[172:173], v[18:19], v[250:251] op_sel_hi:[1,0]
	v_exp_f32_e32 v197, v197
	v_pk_mul_f32 v[162:163], v[162:163], v[178:179]
	v_exp_f32_e32 v201, v201
	v_pk_add_f32 v[188:189], v[188:189], v[142:143] op_sel:[0,1] op_sel_hi:[1,1]
	v_pk_mul_f32 v[162:163], v[162:163], v[144:145] op_sel_hi:[1,0]
	v_pk_mul_f32 v[170:171], v[170:171], v[182:183]
	v_pk_mul_f32 v[172:173], v[172:173], v[184:185]
	v_med3_f32 v162, v162, s87, v227
	v_pk_mul_f32 v[170:171], v[170:171], v[186:187]
	v_pk_mul_f32 v[172:173], v[172:173], v[202:203]
	v_pk_mul_f32 v[174:175], v[20:21], v[250:251] op_sel_hi:[1,0]
	v_pk_mul_f32 v[170:171], v[170:171], v[144:145] op_sel_hi:[1,0]
	v_pk_mul_f32 v[172:173], v[172:173], v[144:145] op_sel_hi:[1,0]
	v_rcp_f32_e32 v188, v188
	v_pk_add_f32 v[194:195], v[194:195], v[142:143] op_sel:[0,1] op_sel_hi:[1,1]
	v_pk_add_f32 v[196:197], v[196:197], v[142:143] op_sel:[0,1] op_sel_hi:[1,1]
	v_med3_f32 v163, v163, s87, v227
	v_med3_f32 v170, v170, s87, v227
	v_med3_f32 v172, v172, s87, v227
	v_pk_mul_f32 v[174:175], v[174:175], v[204:205]
	v_rcp_f32_e32 v194, v194
	v_pk_add_f32 v[200:201], v[200:201], v[142:143] op_sel:[0,1] op_sel_hi:[1,1]
	v_pk_mul_f32 v[174:175], v[174:175], v[206:207]
	v_rcp_f32_e32 v196, v196
	v_cvt_pk_fp8_f32 v162, v162, v163
	v_pk_mul_f32 v[174:175], v[174:175], v[144:145] op_sel_hi:[1,0]
	v_med3_f32 v171, v171, s87, v227
	v_med3_f32 v173, v173, s87, v227
	v_med3_f32 v174, v174, s87, v227
	v_rcp_f32_e32 v200, v200
	v_cvt_pk_fp8_f32 v162, v170, v171 op_sel:[0,0,1]
	v_rcp_f32_e32 v189, v189
	v_cvt_pk_fp8_f32 v163, v172, v173
	v_med3_f32 v175, v175, s87, v227
	v_add_u32_e32 v170, 0x7e000, v219
	v_rcp_f32_e32 v195, v195
	v_cvt_pk_fp8_f32 v163, v174, v175 op_sel:[0,0,1]
	global_store_dwordx2 v170, v[160:161], s[26:27]
	v_rcp_f32_e32 v197, v197
	v_pk_mul_f32 v[160:161], v[10:11], v[250:251] op_sel:[0,1] op_sel_hi:[1,1]
	v_rcp_f32_e32 v201, v201
	v_pk_mul_f32 v[170:171], v[12:13], v[250:251] op_sel:[0,1] op_sel_hi:[1,1]
	v_pk_mul_f32 v[160:161], v[160:161], v[176:177]
	v_pk_mul_f32 v[172:173], v[2:3], v[250:251] op_sel:[0,1] op_sel_hi:[1,1]
	v_pk_mul_f32 v[170:171], v[170:171], v[190:191]
	v_pk_mul_f32 v[160:161], v[160:161], v[188:189]
	v_pk_mul_f32 v[172:173], v[172:173], v[192:193]
	v_pk_mul_f32 v[170:171], v[170:171], v[194:195]
	v_pk_mul_f32 v[160:161], v[160:161], v[144:145] op_sel_hi:[1,0]
	v_pk_mul_f32 v[172:173], v[172:173], v[196:197]
	v_pk_mul_f32 v[170:171], v[170:171], v[144:145] op_sel_hi:[1,0]
	v_med3_f32 v160, v160, s87, v227
	v_pk_mul_f32 v[172:173], v[172:173], v[144:145] op_sel_hi:[1,0]
	v_pk_mul_f32 v[174:175], v[4:5], v[250:251] op_sel:[0,1] op_sel_hi:[1,1]
	v_med3_f32 v161, v161, s87, v227
	v_med3_f32 v170, v170, s87, v227
	v_med3_f32 v172, v172, s87, v227
	v_pk_mul_f32 v[174:175], v[174:175], v[198:199]
	v_cvt_pk_fp8_f32 v160, v160, v161
	v_med3_f32 v171, v171, s87, v227
	v_pk_mul_f32 v[174:175], v[174:175], v[200:201]
	v_med3_f32 v173, v173, s87, v227
	v_cvt_pk_fp8_f32 v160, v170, v171 op_sel:[0,0,1]
	v_pk_mul_f32 v[174:175], v[174:175], v[144:145] op_sel_hi:[1,0]
	v_cvt_pk_fp8_f32 v161, v172, v173
	v_add_u32_e32 v170, 0x8c000, v219
	v_med3_f32 v174, v174, s87, v227
	v_add_u32_e32 v171, 0x9a000, v219
	global_store_dwordx2 v170, v[162:163], s[26:27]
	v_med3_f32 v175, v175, s87, v227
	v_mfma_f32_32x32x16_bf16 v[2:17], v[156:159], v[156:159], 0
	v_mfma_f32_32x32x16_bf16 v[18:33], v[156:159], v[156:159], 0
	v_cvt_pk_fp8_f32 v161, v174, v175 op_sel:[0,0,1]
	v_mfma_f32_32x32x16_bf16 v[34:49], v[156:159], v[156:159], 0
	v_mfma_f32_32x32x16_bf16 v[50:65], v[156:159], v[156:159], 0
	global_store_dwordx2 v171, v[160:161], s[26:27]
	v_mfma_f32_32x32x16_bf16 v[66:81], v[156:159], v[156:159], 0
	v_mfma_f32_32x32x16_bf16 v[82:97], v[156:159], v[156:159], 0
	v_mfma_f32_32x32x16_bf16 v[98:113], v[156:159], v[156:159], 0
	v_mfma_f32_32x32x16_bf16 v[114:129], v[156:159], v[156:159], 0
	s_nop 15
	s_andn2_b64 vcc, exec, s[46:47]
	s_mov_b64 s[46:47], -1
	s_cbranch_vccnz .LBB0_807
	s_andn2_b64 vcc, exec, s[30:31]
	s_cbranch_vccnz .LBB0_806
	s_barrier
	s_branch .LBB0_806

.LBB0_830:
	v_bfe_u32 v18, v16, 4, 2
	s_lshl_b32 s23, s23, 5
	v_and_b32_e32 v17, 15, v16
	v_lshlrev_b32_e32 v19, 4, v18
	v_lshlrev_b32_e32 v16, 2, v16
	s_and_b32 s40, s23, 0x60
	v_lshl_or_b32 v195, s24, 6, v17
	v_lshl_or_b32 v17, v17, 6, v19
	s_lshl_b32 s24, s24, 13
	v_and_b32_e32 v16, 32, v16
	s_lshl_b32 s23, s40, 7
	s_add_i32 m0, s16, 0x18000
	v_lshl_add_u64 v[8:9], v[8:9], 0, s[56:57]
	v_bitop3_b32 v19, v17, s24, v16 bitop3:0xde
	v_bitop3_b32 v196, v17, s23, v16 bitop3:0xde
	s_waitcnt vmcnt(2)
	s_barrier
	global_load_lds_dwordx4 v[8:9], off
	v_lshl_add_u64 v[6:7], v[6:7], 0, s[56:57]
	s_add_i32 m0, s16, 0x1a000
	s_add_i32 s23, s16, 0x8000
	s_add_i32 s24, s16, 0xa000
	s_sext_i32_i16 s61, s34
	global_load_lds_dwordx4 v[6:7], off
	v_lshl_add_u64 v[2:3], v[2:3], 0, s[56:57]
	s_mov_b32 m0, s23
	s_add_u32 s34, s54, 0x20080
	global_load_lds_dwordx4 v[2:3], off
	v_lshl_add_u64 v[2:3], v[4:5], 0, s[56:57]
	s_mov_b32 m0, s24
	s_addc_u32 s35, s55, 0
	global_load_lds_dwordx4 v[2:3], off
	s_add_i32 m0, s16, 0x1c000
	v_lshl_add_u64 v[2:3], s[34:35], 0, v[166:167]
	global_load_lds_dwordx4 v[2:3], off
	v_lshl_add_u64 v[2:3], s[34:35], 0, v[178:179]
	s_add_i32 m0, s16, 0x1e000
	s_cmp_gt_i32 s13, 0
	global_load_lds_dwordx4 v[2:3], off
	v_lshlrev_b32_e32 v2, 18, v18
	v_mov_b32_e32 v3, v167
	v_lshl_add_u64 v[180:181], s[28:29], 0, v[2:3]
	v_lshlrev_b32_e32 v2, 13, v10
	v_and_b32_e32 v2, 0xffffc000, v2
	v_lshl_add_u32 v2, v11, 10, v2
	v_and_b32_e32 v3, 1, v10
	s_cselect_b64 s[34:35], -1, 0
	s_add_i32 s51, s13, -2
	v_lshl_or_b32 v2, v3, 6, v2
	s_cmpk_lt_u32 s36, 0x100
	v_lshl_add_u32 v182, v12, 1, v2
	v_lshlrev_b32_e32 v2, 13, v13
	s_cselect_b64 s[36:37], -1, 0
	s_waitcnt lgkmcnt(0)
	s_ashr_i32 s60, s1, 31
	v_and_b32_e32 v2, 0xffffc000, v2
	s_waitcnt vmcnt(6)
	s_cmp_gt_i32 s0, -1
	s_mul_i32 s28, s1, 0x7fffffff
	v_lshl_add_u32 v2, v14, 10, v2
	v_and_b32_e32 v3, 1, v13
	s_cselect_b64 s[38:39], -1, 0
	s_mul_hi_i32 s29, s1, 0x7fffffff
	s_add_u32 s28, s28, s0
	v_lshl_or_b32 v2, v3, 6, v2
	s_mov_b32 s25, 0
	s_addc_u32 s29, s29, 0
	v_lshl_or_b32 v197, v18, 3, s40
	v_mov_b32_e32 v183, v167
	v_lshl_add_u32 v184, v15, 1, v2
	v_mov_b32_e32 v185, v167
	v_add_u32_e32 v198, 0, v19
	s_barrier
	v_mov_b32_e32 v34, 0
	v_mov_b32_e32 v35, 0
	v_mov_b32_e32 v36, 0
	v_mov_b32_e32 v37, 0
	v_mov_b32_e32 v38, 0
	v_mov_b32_e32 v39, 0
	v_mov_b32_e32 v40, 0
	v_mov_b32_e32 v41, 0
	v_mov_b32_e32 v42, 0
	v_mov_b32_e32 v43, 0
	v_mov_b32_e32 v44, 0
	v_mov_b32_e32 v45, 0
	v_mov_b32_e32 v46, 0
	v_mov_b32_e32 v47, 0
	v_mov_b32_e32 v48, 0
	v_mov_b32_e32 v49, 0
	v_mov_b32_e32 v50, 0
	v_mov_b32_e32 v51, 0
	v_mov_b32_e32 v52, 0
	v_mov_b32_e32 v53, 0
	v_mov_b32_e32 v54, 0
	v_mov_b32_e32 v55, 0
	v_mov_b32_e32 v56, 0
	v_mov_b32_e32 v57, 0
	v_mov_b32_e32 v58, 0
	v_mov_b32_e32 v59, 0
	v_mov_b32_e32 v60, 0
	v_mov_b32_e32 v61, 0
	v_mov_b32_e32 v62, 0
	v_mov_b32_e32 v63, 0
	v_mov_b32_e32 v64, 0
	v_mov_b32_e32 v65, 0
	v_mov_b32_e32 v66, 0
	v_mov_b32_e32 v67, 0
	v_mov_b32_e32 v68, 0
	v_mov_b32_e32 v69, 0
	v_mov_b32_e32 v70, 0
	v_mov_b32_e32 v71, 0
	v_mov_b32_e32 v72, 0
	v_mov_b32_e32 v73, 0
	v_mov_b32_e32 v74, 0
	v_mov_b32_e32 v75, 0
	v_mov_b32_e32 v76, 0
	v_mov_b32_e32 v77, 0
	v_mov_b32_e32 v78, 0
	v_mov_b32_e32 v79, 0
	v_mov_b32_e32 v80, 0
	v_mov_b32_e32 v81, 0
	v_mov_b32_e32 v82, 0
	v_mov_b32_e32 v83, 0
	v_mov_b32_e32 v84, 0
	v_mov_b32_e32 v85, 0
	v_mov_b32_e32 v86, 0
	v_mov_b32_e32 v87, 0
	v_mov_b32_e32 v88, 0
	v_mov_b32_e32 v89, 0
	v_mov_b32_e32 v90, 0
	v_mov_b32_e32 v91, 0
	v_mov_b32_e32 v92, 0
	v_mov_b32_e32 v93, 0
	v_mov_b32_e32 v94, 0
	v_mov_b32_e32 v95, 0
	v_mov_b32_e32 v96, 0
	v_mov_b32_e32 v97, 0
	v_mov_b32_e32 v98, 0
	v_mov_b32_e32 v99, 0
	v_mov_b32_e32 v100, 0
	v_mov_b32_e32 v101, 0
	v_mov_b32_e32 v102, 0
	v_mov_b32_e32 v103, 0
	v_mov_b32_e32 v104, 0
	v_mov_b32_e32 v105, 0
	v_mov_b32_e32 v106, 0
	v_mov_b32_e32 v107, 0
	v_mov_b32_e32 v108, 0
	v_mov_b32_e32 v109, 0
	v_mov_b32_e32 v110, 0
	v_mov_b32_e32 v111, 0
	v_mov_b32_e32 v112, 0
	v_mov_b32_e32 v113, 0
	v_mov_b32_e32 v114, 0
	v_mov_b32_e32 v115, 0
	v_mov_b32_e32 v116, 0
	v_mov_b32_e32 v117, 0
	v_mov_b32_e32 v118, 0
	v_mov_b32_e32 v119, 0
	v_mov_b32_e32 v120, 0
	v_mov_b32_e32 v121, 0
	v_mov_b32_e32 v122, 0
	v_mov_b32_e32 v123, 0
	v_mov_b32_e32 v124, 0
	v_mov_b32_e32 v125, 0
	v_mov_b32_e32 v126, 0
	v_mov_b32_e32 v127, 0
	v_mov_b32_e32 v128, 0
	v_mov_b32_e32 v129, 0
	v_mov_b32_e32 v130, 0
	v_mov_b32_e32 v131, 0
	v_mov_b32_e32 v132, 0
	v_mov_b32_e32 v133, 0
	v_mov_b32_e32 v134, 0
	v_mov_b32_e32 v135, 0
	v_mov_b32_e32 v136, 0
	v_mov_b32_e32 v137, 0
	v_mov_b32_e32 v138, 0
	v_mov_b32_e32 v139, 0
	v_mov_b32_e32 v140, 0
	v_mov_b32_e32 v141, 0
	v_mov_b32_e32 v142, 0
	v_mov_b32_e32 v143, 0
	v_mov_b32_e32 v144, 0
	v_mov_b32_e32 v145, 0
	v_mov_b32_e32 v146, 0
	v_mov_b32_e32 v147, 0
	v_mov_b32_e32 v148, 0
	v_mov_b32_e32 v149, 0
	v_mov_b32_e32 v150, 0
	v_mov_b32_e32 v151, 0
	v_mov_b32_e32 v152, 0
	v_mov_b32_e32 v153, 0
	v_mov_b32_e32 v154, 0
	v_mov_b32_e32 v155, 0
	v_mov_b32_e32 v156, 0
	v_mov_b32_e32 v157, 0
	v_mov_b32_e32 v158, 0
	v_mov_b32_e32 v159, 0
	v_mov_b32_e32 v160, 0
	v_mov_b32_e32 v161, 0
	s_branch .LBB0_833

.LBB0_840:
	s_ashr_i32 s43, s42, 31
	s_lshl_b64 s[46:47], s[42:43], 18
	s_add_u32 s46, s8, s46
	s_addc_u32 s47, s10, s47
	s_ashr_i32 s41, s40, 31
	s_lshl_b64 s[48:49], s[40:41], 18
	s_add_u32 s48, s11, s48
	s_addc_u32 s49, s12, s49
	s_andn2_b64 vcc, exec, s[34:35]
	s_cbranch_vccnz .LBB0_848
	v_lshl_add_u32 v2, s50, 8, v195
	v_ashrrev_i32_e32 v3, 31, v2
	v_lshl_add_u64 v[4:5], v[2:3], 2, v[180:181]
	global_load_dword v244, v[4:5], off
	global_load_dword v245, v[4:5], off offset:64
	global_load_dword v246, v[4:5], off offset:128
	global_load_dword v247, v[4:5], off offset:192
	global_load_dword v248, v[4:5], off offset:512
	global_load_dword v249, v[4:5], off offset:576
	global_load_dword v250, v[4:5], off offset:640
	global_load_dword v251, v[4:5], off offset:704
	s_and_b64 s[58:59], s[44:45], exec
	s_cselect_b32 s41, s47, s53
	s_cselect_b32 s43, s46, s52
	s_cselect_b32 s62, s49, s55
	s_cselect_b32 s63, s48, s54
	s_add_u32 s64, s54, 0x100
	s_addc_u32 s65, s55, 0
	s_add_u32 s52, s52, 0x20080
	v_mov_b32_e32 v1, 0x3ecc95a3
	s_addc_u32 s53, s53, 0
	s_mov_b32 s54, 0

.LBB0_845:
	v_xor_b32_e32 v240, 16, v231
	v_and_b32_e32 v238, 64, v231
	v_add_u32_e32 v238, 64, v238
	v_xor_b32_e32 v239, 32, v231
	v_cmp_lt_i32_e32 vcc, v240, v238
	v_mov_b32_e32 v2, 0xbfb8aa3b
	v_mov_b32_e32 v3, 1.0
	v_cndmask_b32_e32 v240, v231, v240, vcc
	v_cmp_lt_i32_e32 vcc, v239, v238
	v_lshlrev_b32_e32 v240, 2, v240
	v_mov_b32_e32 v4, 0x41000000
	v_cndmask_b32_e32 v239, v231, v239, vcc
	v_lshlrev_b32_e32 v239, 2, v239
	ds_bpermute_b32 v6, v240, v244
	ds_bpermute_b32 v7, v240, v245
	ds_bpermute_b32 v12, v240, v246
	ds_bpermute_b32 v13, v240, v247
	ds_bpermute_b32 v14, v240, v248
	ds_bpermute_b32 v15, v240, v249
	ds_bpermute_b32 v16, v240, v250
	ds_bpermute_b32 v17, v240, v251
	v_lshl_add_u32 v243, s50, 8, v195
	v_lshl_or_b32 v242, s61, 7, v197
	v_mad_u32_u24 v241, v243, s33, v242
	s_waitcnt lgkmcnt(7)
	v_add_f32_e32 v244, v244, v6
	ds_bpermute_b32 v6, v239, v244
	s_waitcnt lgkmcnt(7)
	v_add_f32_e32 v245, v245, v7
	ds_bpermute_b32 v7, v239, v245
	s_waitcnt lgkmcnt(7)
	v_add_f32_e32 v246, v246, v12
	ds_bpermute_b32 v12, v239, v246
	s_waitcnt lgkmcnt(7)
	v_add_f32_e32 v247, v247, v13
	ds_bpermute_b32 v13, v239, v247
	s_waitcnt lgkmcnt(7)
	v_add_f32_e32 v248, v248, v14
	ds_bpermute_b32 v14, v239, v248
	s_waitcnt lgkmcnt(7)
	v_add_f32_e32 v249, v249, v15
	ds_bpermute_b32 v15, v239, v249
	s_waitcnt lgkmcnt(7)
	v_add_f32_e32 v250, v250, v16
	ds_bpermute_b32 v16, v239, v250
	s_waitcnt lgkmcnt(7)
	v_add_f32_e32 v251, v251, v17
	ds_bpermute_b32 v17, v239, v251
	s_waitcnt lgkmcnt(7)
	v_add_f32_e32 v244, v244, v6
	v_fmamk_f32 v244, v244, 0x3a800000, v224
	s_waitcnt lgkmcnt(6)
	v_add_f32_e32 v245, v245, v7
	v_fmamk_f32 v245, v245, 0x3a800000, v224
	s_waitcnt lgkmcnt(5)
	v_add_f32_e32 v246, v246, v12
	v_fmamk_f32 v246, v246, 0x3a800000, v224
	s_waitcnt lgkmcnt(4)
	v_add_f32_e32 v247, v247, v13
	v_fmamk_f32 v247, v247, 0x3a800000, v224
	s_waitcnt lgkmcnt(3)
	v_add_f32_e32 v248, v248, v14
	v_fmamk_f32 v248, v248, 0x3a800000, v224
	s_waitcnt lgkmcnt(2)
	v_add_f32_e32 v249, v249, v15
	v_fmamk_f32 v249, v249, 0x3a800000, v224
	s_waitcnt lgkmcnt(1)
	v_add_f32_e32 v250, v250, v16
	v_fmamk_f32 v250, v250, 0x3a800000, v224
	s_waitcnt lgkmcnt(0)
	v_add_f32_e32 v251, v251, v17
	v_fmamk_f32 v251, v251, 0x3a800000, v224
	v_rsq_f32_e32 v244, v244
	v_rsq_f32_e32 v245, v245
	v_rsq_f32_e32 v246, v246
	v_rsq_f32_e32 v247, v247
	v_rsq_f32_e32 v248, v248
	v_rsq_f32_e32 v249, v249
	v_rsq_f32_e32 v250, v250
	v_rsq_f32_e32 v251, v251
	v_mov_b32_e32 v8, 0
	v_mov_b32_e32 v9, 0
	v_mov_b32_e32 v10, 0
	v_mov_b32_e32 v11, 0
	v_pk_mul_f32 v[6:7], v[158:159], v[244:245] op_sel_hi:[1,0]
	v_pk_mul_f32 v[12:13], v[160:161], v[244:245] op_sel_hi:[1,0]
	v_pk_mul_f32 v[14:15], v[150:151], v[244:245] op_sel_hi:[1,0]
	v_pk_mul_f32 v[16:17], v[6:7], v[2:3] op_sel_hi:[1,0]
	v_pk_mul_f32 v[18:19], v[12:13], v[2:3] op_sel_hi:[1,0]
	v_pk_mul_f32 v[20:21], v[14:15], v[2:3] op_sel_hi:[1,0]
	v_exp_f32_e32 v16, v16
	v_pk_mul_f32 v[22:23], v[152:153], v[244:245] op_sel_hi:[1,0]
	v_exp_f32_e32 v18, v18
	v_pk_mul_f32 v[24:25], v[142:143], v[244:245] op_sel:[0,1] op_sel_hi:[1,1]
	v_exp_f32_e32 v20, v20
	v_pk_mul_f32 v[26:27], v[22:23], v[2:3] op_sel_hi:[1,0]
	v_pk_mul_f32 v[28:29], v[24:25], v[2:3] op_sel_hi:[1,0]
	v_pk_mul_f32 v[30:31], v[144:145], v[244:245] op_sel:[0,1] op_sel_hi:[1,1]
	v_exp_f32_e32 v26, v26
	v_pk_mul_f32 v[32:33], v[134:135], v[244:245] op_sel:[0,1] op_sel_hi:[1,1]
	v_exp_f32_e32 v17, v17
	v_pk_mul_f32 v[186:187], v[30:31], v[2:3] op_sel_hi:[1,0]
	v_exp_f32_e32 v19, v19
	v_pk_mul_f32 v[188:189], v[32:33], v[2:3] op_sel_hi:[1,0]
	v_exp_f32_e32 v21, v21
	v_pk_mul_f32 v[190:191], v[136:137], v[244:245] op_sel:[0,1] op_sel_hi:[1,1]
	v_exp_f32_e32 v27, v27
	v_pk_mul_f32 v[192:193], v[154:155], v[244:245] op_sel_hi:[1,0]
	v_pk_add_f32 v[16:17], v[16:17], v[2:3] op_sel:[0,1] op_sel_hi:[1,1]
	v_exp_f32_e32 v28, v28
	v_pk_add_f32 v[18:19], v[18:19], v[2:3] op_sel:[0,1] op_sel_hi:[1,1]
	v_rcp_f32_e32 v16, v16
	v_pk_add_f32 v[20:21], v[20:21], v[2:3] op_sel:[0,1] op_sel_hi:[1,1]
	v_rcp_f32_e32 v18, v18
	v_pk_add_f32 v[26:27], v[26:27], v[2:3] op_sel:[0,1] op_sel_hi:[1,1]
	v_rcp_f32_e32 v20, v20
	v_pk_mul_f32 v[200:201], v[190:191], v[2:3] op_sel_hi:[1,0]
	v_rcp_f32_e32 v26, v26
	v_pk_mul_f32 v[192:193], v[192:193], v[6:7]
	v_exp_f32_e32 v186, v186
	v_pk_mul_f32 v[6:7], v[156:157], v[244:245] op_sel_hi:[1,0]
	v_exp_f32_e32 v188, v188
	v_pk_mul_f32 v[202:203], v[146:147], v[244:245] op_sel_hi:[1,0]
	v_rcp_f32_e32 v17, v17
	v_pk_mul_f32 v[204:205], v[126:127], v[246:247] op_sel_hi:[1,0]
	v_exp_f32_e32 v200, v200
	v_pk_mul_f32 v[6:7], v[6:7], v[12:13]
	v_rcp_f32_e32 v19, v19
	v_pk_mul_f32 v[202:203], v[202:203], v[14:15]
	v_rcp_f32_e32 v21, v21
	v_pk_mul_f32 v[12:13], v[148:149], v[244:245] op_sel_hi:[1,0]
	v_exp_f32_e32 v29, v29
	v_pk_mul_f32 v[192:193], v[192:193], v[16:17]
	v_rcp_f32_e32 v27, v27
	v_pk_mul_f32 v[14:15], v[204:205], v[2:3] op_sel_hi:[1,0]
	v_exp_f32_e32 v187, v187
	v_pk_mul_f32 v[192:193], v[192:193], v[4:5] op_sel_hi:[1,0]
	v_exp_f32_e32 v189, v189
	v_pk_mul_f32 v[6:7], v[6:7], v[18:19]
	v_exp_f32_e32 v201, v201
	v_pk_mul_f32 v[202:203], v[202:203], v[20:21]
	v_pk_add_f32 v[28:29], v[28:29], v[2:3] op_sel:[0,1] op_sel_hi:[1,1]
	v_med3_f32 v192, v192, s87, v227
	v_pk_mul_f32 v[6:7], v[6:7], v[4:5] op_sel_hi:[1,0]
	v_pk_mul_f32 v[202:203], v[202:203], v[4:5] op_sel_hi:[1,0]
	v_rcp_f32_e32 v28, v28
	v_pk_add_f32 v[186:187], v[186:187], v[2:3] op_sel:[0,1] op_sel_hi:[1,1]
	v_pk_add_f32 v[188:189], v[188:189], v[2:3] op_sel:[0,1] op_sel_hi:[1,1]
	v_pk_mul_f32 v[16:17], v[128:129], v[246:247] op_sel_hi:[1,0]
	v_pk_mul_f32 v[18:19], v[118:119], v[246:247] op_sel_hi:[1,0]
	v_med3_f32 v193, v193, s87, v227
	v_med3_f32 v6, v6, s87, v227
	v_med3_f32 v202, v202, s87, v227
	v_pk_mul_f32 v[12:13], v[12:13], v[22:23]
	v_rcp_f32_e32 v186, v186
	v_pk_add_f32 v[200:201], v[200:201], v[2:3] op_sel:[0,1] op_sel_hi:[1,1]
	v_pk_mul_f32 v[12:13], v[12:13], v[26:27]
	v_rcp_f32_e32 v188, v188
	v_pk_mul_f32 v[20:21], v[16:17], v[2:3] op_sel_hi:[1,0]
	v_pk_mul_f32 v[12:13], v[12:13], v[4:5] op_sel_hi:[1,0]
	v_exp_f32_e32 v14, v14
	v_pk_mul_f32 v[22:23], v[18:19], v[2:3] op_sel_hi:[1,0]
	v_pk_mul_f32 v[26:27], v[120:121], v[246:247] op_sel_hi:[1,0]
	v_cvt_pk_fp8_f32 v192, v192, v193
	v_med3_f32 v7, v7, s87, v227
	v_med3_f32 v203, v203, s87, v227
	v_med3_f32 v12, v12, s87, v227
	v_rcp_f32_e32 v200, v200
	v_pk_mul_f32 v[206:207], v[26:27], v[2:3] op_sel_hi:[1,0]
	v_exp_f32_e32 v20, v20
	v_cvt_pk_fp8_f32 v192, v6, v7 op_sel:[0,0,1]
	v_exp_f32_e32 v22, v22
	v_cvt_pk_fp8_f32 v193, v202, v203
	v_rcp_f32_e32 v29, v29
	v_med3_f32 v13, v13, s87, v227
	v_exp_f32_e32 v206, v206
	v_pk_mul_f32 v[6:7], v[138:139], v[244:245] op_sel:[0,1] op_sel_hi:[1,1]
	v_rcp_f32_e32 v187, v187
	v_cvt_pk_fp8_f32 v193, v12, v13 op_sel:[0,0,1]
	v_rcp_f32_e32 v189, v189
	v_pk_mul_f32 v[6:7], v[6:7], v[24:25]
	v_exp_f32_e32 v15, v15
	global_store_dwordx2 v241, v[192:193], s[26:27]
	v_rcp_f32_e32 v201, v201
	v_pk_mul_f32 v[6:7], v[6:7], v[28:29]
	v_exp_f32_e32 v21, v21
	v_pk_mul_f32 v[12:13], v[140:141], v[244:245] op_sel:[0,1] op_sel_hi:[1,1]
	v_exp_f32_e32 v23, v23
	v_pk_mul_f32 v[6:7], v[6:7], v[4:5] op_sel_hi:[1,0]
	v_exp_f32_e32 v207, v207
	v_pk_mul_f32 v[24:25], v[130:131], v[244:245] op_sel:[0,1] op_sel_hi:[1,1]
	v_pk_add_f32 v[14:15], v[14:15], v[2:3] op_sel:[0,1] op_sel_hi:[1,1]
	v_pk_mul_f32 v[28:29], v[110:111], v[246:247] op_sel:[0,1] op_sel_hi:[1,1]
	v_med3_f32 v6, v6, s87, v227
	v_pk_mul_f32 v[12:13], v[12:13], v[30:31]
	v_pk_mul_f32 v[24:25], v[24:25], v[32:33]
	v_pk_mul_f32 v[30:31], v[132:133], v[244:245] op_sel:[0,1] op_sel_hi:[1,1]
	v_pk_mul_f32 v[12:13], v[12:13], v[186:187]
	v_pk_mul_f32 v[24:25], v[24:25], v[188:189]
	v_rcp_f32_e32 v14, v14
	v_pk_mul_f32 v[12:13], v[12:13], v[4:5] op_sel_hi:[1,0]
	v_pk_mul_f32 v[24:25], v[24:25], v[4:5] op_sel_hi:[1,0]
	v_pk_add_f32 v[20:21], v[20:21], v[2:3] op_sel:[0,1] op_sel_hi:[1,1]
	v_pk_add_f32 v[22:23], v[22:23], v[2:3] op_sel:[0,1] op_sel_hi:[1,1]
	v_pk_mul_f32 v[32:33], v[28:29], v[2:3] op_sel_hi:[1,0]
	v_pk_mul_f32 v[186:187], v[112:113], v[246:247] op_sel:[0,1] op_sel_hi:[1,1]
	v_pk_mul_f32 v[188:189], v[102:103], v[246:247] op_sel:[0,1] op_sel_hi:[1,1]
	v_med3_f32 v7, v7, s87, v227
	v_med3_f32 v12, v12, s87, v227
	v_med3_f32 v24, v24, s87, v227
	v_pk_mul_f32 v[30:31], v[30:31], v[190:191]
	v_rcp_f32_e32 v20, v20
	v_pk_add_f32 v[206:207], v[206:207], v[2:3] op_sel:[0,1] op_sel_hi:[1,1]
	v_pk_mul_f32 v[30:31], v[30:31], v[200:201]
	v_rcp_f32_e32 v22, v22
	v_pk_mul_f32 v[190:191], v[186:187], v[2:3] op_sel_hi:[1,0]
	v_pk_mul_f32 v[30:31], v[30:31], v[4:5] op_sel_hi:[1,0]
	v_exp_f32_e32 v32, v32
	v_pk_mul_f32 v[192:193], v[188:189], v[2:3] op_sel_hi:[1,0]
	v_pk_mul_f32 v[200:201], v[104:105], v[246:247] op_sel:[0,1] op_sel_hi:[1,1]
	v_cvt_pk_fp8_f32 v6, v6, v7
	v_med3_f32 v13, v13, s87, v227
	v_med3_f32 v25, v25, s87, v227
	v_med3_f32 v30, v30, s87, v227
	v_rcp_f32_e32 v206, v206
	v_pk_mul_f32 v[202:203], v[200:201], v[2:3] op_sel_hi:[1,0]
	v_exp_f32_e32 v190, v190
	v_cvt_pk_fp8_f32 v6, v12, v13 op_sel:[0,0,1]
	v_exp_f32_e32 v192, v192
	v_cvt_pk_fp8_f32 v7, v24, v25
	v_rcp_f32_e32 v15, v15
	v_med3_f32 v31, v31, s87, v227
	v_exp_f32_e32 v202, v202
	v_pk_mul_f32 v[12:13], v[122:123], v[246:247] op_sel_hi:[1,0]
	v_rcp_f32_e32 v21, v21
	v_cvt_pk_fp8_f32 v7, v30, v31 op_sel:[0,0,1]
	v_rcp_f32_e32 v23, v23
	v_pk_mul_f32 v[12:13], v[12:13], v[204:205]
	v_exp_f32_e32 v33, v33
	v_pk_mul_f32 v[24:25], v[124:125], v[246:247] op_sel_hi:[1,0]
	v_rcp_f32_e32 v207, v207
	v_pk_mul_f32 v[12:13], v[12:13], v[14:15]
	v_exp_f32_e32 v191, v191
	v_pk_mul_f32 v[14:15], v[114:115], v[246:247] op_sel_hi:[1,0]
	v_exp_f32_e32 v193, v193
	v_pk_mul_f32 v[12:13], v[12:13], v[4:5] op_sel_hi:[1,0]
	v_exp_f32_e32 v203, v203
	v_pk_add_f32 v[32:33], v[32:33], v[2:3] op_sel:[0,1] op_sel_hi:[1,1]
	v_pk_mul_f32 v[30:31], v[94:95], v[248:249] op_sel_hi:[1,0]
	v_med3_f32 v12, v12, s87, v227
	v_pk_mul_f32 v[24:25], v[24:25], v[16:17]
	v_pk_mul_f32 v[14:15], v[14:15], v[18:19]
	v_pk_mul_f32 v[16:17], v[116:117], v[246:247] op_sel_hi:[1,0]
	v_pk_mul_f32 v[24:25], v[24:25], v[20:21]
	v_pk_mul_f32 v[14:15], v[14:15], v[22:23]
	v_rcp_f32_e32 v32, v32
	v_pk_mul_f32 v[24:25], v[24:25], v[4:5] op_sel_hi:[1,0]
	v_pk_mul_f32 v[14:15], v[14:15], v[4:5] op_sel_hi:[1,0]
	v_pk_add_f32 v[190:191], v[190:191], v[2:3] op_sel:[0,1] op_sel_hi:[1,1]
	v_pk_add_f32 v[192:193], v[192:193], v[2:3] op_sel:[0,1] op_sel_hi:[1,1]
	v_pk_mul_f32 v[18:19], v[30:31], v[2:3] op_sel_hi:[1,0]
	v_pk_mul_f32 v[20:21], v[96:97], v[248:249] op_sel_hi:[1,0]
	v_pk_mul_f32 v[22:23], v[86:87], v[248:249] op_sel_hi:[1,0]
	v_med3_f32 v13, v13, s87, v227
	v_med3_f32 v24, v24, s87, v227
	v_med3_f32 v14, v14, s87, v227
	v_pk_mul_f32 v[16:17], v[16:17], v[26:27]
	v_rcp_f32_e32 v190, v190
	v_pk_add_f32 v[202:203], v[202:203], v[2:3] op_sel:[0,1] op_sel_hi:[1,1]
	v_pk_mul_f32 v[16:17], v[16:17], v[206:207]
	v_rcp_f32_e32 v192, v192
	v_pk_mul_f32 v[26:27], v[20:21], v[2:3] op_sel_hi:[1,0]
	v_pk_mul_f32 v[16:17], v[16:17], v[4:5] op_sel_hi:[1,0]
	v_exp_f32_e32 v18, v18
	v_pk_mul_f32 v[204:205], v[22:23], v[2:3] op_sel_hi:[1,0]
	v_pk_mul_f32 v[206:207], v[88:89], v[248:249] op_sel_hi:[1,0]
	v_cvt_pk_fp8_f32 v12, v12, v13
	v_med3_f32 v25, v25, s87, v227
	v_med3_f32 v15, v15, s87, v227
	v_med3_f32 v16, v16, s87, v227
	v_rcp_f32_e32 v202, v202
	v_pk_mul_f32 v[208:209], v[206:207], v[2:3] op_sel_hi:[1,0]
	v_exp_f32_e32 v26, v26
	v_cvt_pk_fp8_f32 v12, v24, v25 op_sel:[0,0,1]
	v_exp_f32_e32 v204, v204
	v_cvt_pk_fp8_f32 v13, v14, v15
	v_rcp_f32_e32 v33, v33
	v_med3_f32 v17, v17, s87, v227
	v_exp_f32_e32 v208, v208
	v_add_u32_e32 v14, 0xe000, v241
	v_rcp_f32_e32 v191, v191
	v_cvt_pk_fp8_f32 v13, v16, v17 op_sel:[0,0,1]
	global_store_dwordx2 v14, v[6:7], s[26:27]
	v_rcp_f32_e32 v193, v193
	v_pk_mul_f32 v[6:7], v[106:107], v[246:247] op_sel:[0,1] op_sel_hi:[1,1]
	v_exp_f32_e32 v19, v19
	v_pk_mul_f32 v[14:15], v[108:109], v[246:247] op_sel:[0,1] op_sel_hi:[1,1]
	v_rcp_f32_e32 v203, v203
	v_pk_mul_f32 v[6:7], v[6:7], v[28:29]
	v_exp_f32_e32 v27, v27
	v_pk_mul_f32 v[16:17], v[98:99], v[246:247] op_sel:[0,1] op_sel_hi:[1,1]
	v_exp_f32_e32 v205, v205
	v_pk_mul_f32 v[6:7], v[6:7], v[32:33]
	v_exp_f32_e32 v209, v209
	v_pk_add_f32 v[18:19], v[18:19], v[2:3] op_sel:[0,1] op_sel_hi:[1,1]
	v_pk_mul_f32 v[6:7], v[6:7], v[4:5] op_sel_hi:[1,0]
	v_pk_mul_f32 v[24:25], v[78:79], v[248:249] op_sel:[0,1] op_sel_hi:[1,1]
	v_pk_mul_f32 v[14:15], v[14:15], v[186:187]
	v_med3_f32 v6, v6, s87, v227
	v_pk_mul_f32 v[16:17], v[16:17], v[188:189]
	v_pk_mul_f32 v[14:15], v[14:15], v[190:191]
	v_pk_mul_f32 v[28:29], v[100:101], v[246:247] op_sel:[0,1] op_sel_hi:[1,1]
	v_pk_mul_f32 v[16:17], v[16:17], v[192:193]
	v_pk_mul_f32 v[14:15], v[14:15], v[4:5] op_sel_hi:[1,0]
	v_rcp_f32_e32 v18, v18
	v_pk_mul_f32 v[16:17], v[16:17], v[4:5] op_sel_hi:[1,0]
	v_pk_add_f32 v[26:27], v[26:27], v[2:3] op_sel:[0,1] op_sel_hi:[1,1]
	v_pk_add_f32 v[204:205], v[204:205], v[2:3] op_sel:[0,1] op_sel_hi:[1,1]
	v_pk_mul_f32 v[32:33], v[24:25], v[2:3] op_sel_hi:[1,0]
	v_pk_mul_f32 v[186:187], v[80:81], v[248:249] op_sel:[0,1] op_sel_hi:[1,1]
	v_pk_mul_f32 v[188:189], v[70:71], v[248:249] op_sel:[0,1] op_sel_hi:[1,1]
	v_med3_f32 v7, v7, s87, v227
	v_med3_f32 v14, v14, s87, v227
	v_med3_f32 v16, v16, s87, v227
	v_pk_mul_f32 v[28:29], v[28:29], v[200:201]
	v_rcp_f32_e32 v26, v26
	v_pk_add_f32 v[208:209], v[208:209], v[2:3] op_sel:[0,1] op_sel_hi:[1,1]
	v_pk_mul_f32 v[28:29], v[28:29], v[202:203]
	v_rcp_f32_e32 v204, v204
	v_pk_mul_f32 v[190:191], v[186:187], v[2:3] op_sel_hi:[1,0]
	v_pk_mul_f32 v[28:29], v[28:29], v[4:5] op_sel_hi:[1,0]
	v_exp_f32_e32 v32, v32
	v_pk_mul_f32 v[192:193], v[188:189], v[2:3] op_sel_hi:[1,0]
	v_pk_mul_f32 v[200:201], v[72:73], v[248:249] op_sel:[0,1] op_sel_hi:[1,1]
	v_cvt_pk_fp8_f32 v6, v6, v7
	v_med3_f32 v15, v15, s87, v227
	v_med3_f32 v17, v17, s87, v227
	v_med3_f32 v28, v28, s87, v227
	v_rcp_f32_e32 v208, v208
	v_pk_mul_f32 v[202:203], v[200:201], v[2:3] op_sel_hi:[1,0]
	v_exp_f32_e32 v190, v190
	v_cvt_pk_fp8_f32 v6, v14, v15 op_sel:[0,0,1]
	v_exp_f32_e32 v192, v192
	v_cvt_pk_fp8_f32 v7, v16, v17
	v_rcp_f32_e32 v19, v19
	v_med3_f32 v29, v29, s87, v227
	v_exp_f32_e32 v202, v202
	v_add_u32_e32 v14, 0x1c000, v241
	v_rcp_f32_e32 v27, v27
	v_cvt_pk_fp8_f32 v7, v28, v29 op_sel:[0,0,1]
	global_store_dwordx2 v14, v[12:13], s[26:27]
	v_rcp_f32_e32 v205, v205
	v_pk_mul_f32 v[12:13], v[90:91], v[248:249] op_sel_hi:[1,0]
	v_exp_f32_e32 v33, v33
	v_pk_mul_f32 v[14:15], v[92:93], v[248:249] op_sel_hi:[1,0]
	v_rcp_f32_e32 v209, v209
	v_pk_mul_f32 v[12:13], v[12:13], v[30:31]
	v_exp_f32_e32 v191, v191
	v_pk_mul_f32 v[16:17], v[82:83], v[248:249] op_sel_hi:[1,0]
	v_exp_f32_e32 v193, v193
	v_pk_mul_f32 v[12:13], v[12:13], v[18:19]
	v_exp_f32_e32 v203, v203
	v_pk_add_f32 v[32:33], v[32:33], v[2:3] op_sel:[0,1] op_sel_hi:[1,1]
	v_pk_mul_f32 v[12:13], v[12:13], v[4:5] op_sel_hi:[1,0]
	v_pk_mul_f32 v[18:19], v[62:63], v[250:251] op_sel_hi:[1,0]
	v_pk_mul_f32 v[14:15], v[14:15], v[20:21]
	v_med3_f32 v12, v12, s87, v227
	v_pk_mul_f32 v[16:17], v[16:17], v[22:23]
	v_pk_mul_f32 v[14:15], v[14:15], v[26:27]
	v_pk_mul_f32 v[20:21], v[84:85], v[248:249] op_sel_hi:[1,0]
	v_pk_mul_f32 v[16:17], v[16:17], v[204:205]
	v_pk_mul_f32 v[14:15], v[14:15], v[4:5] op_sel_hi:[1,0]
	v_rcp_f32_e32 v32, v32
	v_pk_mul_f32 v[16:17], v[16:17], v[4:5] op_sel_hi:[1,0]
	v_pk_add_f32 v[190:191], v[190:191], v[2:3] op_sel:[0,1] op_sel_hi:[1,1]
	v_pk_add_f32 v[192:193], v[192:193], v[2:3] op_sel:[0,1] op_sel_hi:[1,1]
	v_pk_mul_f32 v[22:23], v[18:19], v[2:3] op_sel_hi:[1,0]
	v_pk_mul_f32 v[26:27], v[64:65], v[250:251] op_sel_hi:[1,0]
	v_pk_mul_f32 v[28:29], v[54:55], v[250:251] op_sel_hi:[1,0]
	v_med3_f32 v13, v13, s87, v227
	v_med3_f32 v14, v14, s87, v227
	v_med3_f32 v16, v16, s87, v227
	v_pk_mul_f32 v[20:21], v[20:21], v[206:207]
	v_rcp_f32_e32 v190, v190
	v_pk_add_f32 v[202:203], v[202:203], v[2:3] op_sel:[0,1] op_sel_hi:[1,1]
	v_pk_mul_f32 v[20:21], v[20:21], v[208:209]
	v_rcp_f32_e32 v192, v192
	v_pk_mul_f32 v[30:31], v[26:27], v[2:3] op_sel_hi:[1,0]
	v_pk_mul_f32 v[20:21], v[20:21], v[4:5] op_sel_hi:[1,0]
	v_exp_f32_e32 v22, v22
	v_pk_mul_f32 v[204:205], v[28:29], v[2:3] op_sel_hi:[1,0]
	v_pk_mul_f32 v[206:207], v[56:57], v[250:251] op_sel_hi:[1,0]
	v_cvt_pk_fp8_f32 v12, v12, v13
	v_med3_f32 v15, v15, s87, v227
	v_med3_f32 v17, v17, s87, v227
	v_med3_f32 v20, v20, s87, v227
	v_rcp_f32_e32 v202, v202
	v_pk_mul_f32 v[208:209], v[206:207], v[2:3] op_sel_hi:[1,0]
	v_exp_f32_e32 v30, v30
	v_cvt_pk_fp8_f32 v12, v14, v15 op_sel:[0,0,1]
	v_exp_f32_e32 v204, v204
	v_cvt_pk_fp8_f32 v13, v16, v17
	v_rcp_f32_e32 v33, v33
	v_med3_f32 v21, v21, s87, v227
	v_exp_f32_e32 v208, v208
	v_add_u32_e32 v14, 0x2a000, v241
	v_rcp_f32_e32 v191, v191
	v_cvt_pk_fp8_f32 v13, v20, v21 op_sel:[0,0,1]
	global_store_dwordx2 v14, v[6:7], s[26:27]
	v_rcp_f32_e32 v193, v193
	v_pk_mul_f32 v[6:7], v[74:75], v[248:249] op_sel:[0,1] op_sel_hi:[1,1]
	v_exp_f32_e32 v23, v23
	v_pk_mul_f32 v[14:15], v[76:77], v[248:249] op_sel:[0,1] op_sel_hi:[1,1]
	v_rcp_f32_e32 v203, v203
	v_pk_mul_f32 v[6:7], v[6:7], v[24:25]
	v_exp_f32_e32 v31, v31
	v_pk_mul_f32 v[16:17], v[66:67], v[248:249] op_sel:[0,1] op_sel_hi:[1,1]
	v_exp_f32_e32 v205, v205
	v_pk_mul_f32 v[6:7], v[6:7], v[32:33]
	v_exp_f32_e32 v209, v209
	v_pk_add_f32 v[22:23], v[22:23], v[2:3] op_sel:[0,1] op_sel_hi:[1,1]
	v_pk_mul_f32 v[6:7], v[6:7], v[4:5] op_sel_hi:[1,0]
	v_pk_mul_f32 v[20:21], v[46:47], v[250:251] op_sel:[0,1] op_sel_hi:[1,1]
	v_pk_mul_f32 v[14:15], v[14:15], v[186:187]
	v_med3_f32 v6, v6, s87, v227
	v_pk_mul_f32 v[16:17], v[16:17], v[188:189]
	v_pk_mul_f32 v[14:15], v[14:15], v[190:191]
	v_pk_mul_f32 v[24:25], v[68:69], v[248:249] op_sel:[0,1] op_sel_hi:[1,1]
	v_pk_mul_f32 v[16:17], v[16:17], v[192:193]
	v_pk_mul_f32 v[14:15], v[14:15], v[4:5] op_sel_hi:[1,0]
	v_rcp_f32_e32 v22, v22
	v_pk_mul_f32 v[16:17], v[16:17], v[4:5] op_sel_hi:[1,0]
	v_pk_add_f32 v[30:31], v[30:31], v[2:3] op_sel:[0,1] op_sel_hi:[1,1]
	v_pk_add_f32 v[204:205], v[204:205], v[2:3] op_sel:[0,1] op_sel_hi:[1,1]
	v_pk_mul_f32 v[32:33], v[20:21], v[2:3] op_sel_hi:[1,0]
	v_pk_mul_f32 v[186:187], v[48:49], v[250:251] op_sel:[0,1] op_sel_hi:[1,1]
	v_pk_mul_f32 v[188:189], v[38:39], v[250:251] op_sel:[0,1] op_sel_hi:[1,1]
	v_med3_f32 v7, v7, s87, v227
	v_med3_f32 v14, v14, s87, v227
	v_med3_f32 v16, v16, s87, v227
	v_pk_mul_f32 v[24:25], v[24:25], v[200:201]
	v_rcp_f32_e32 v30, v30
	v_pk_add_f32 v[208:209], v[208:209], v[2:3] op_sel:[0,1] op_sel_hi:[1,1]
	v_pk_mul_f32 v[24:25], v[24:25], v[202:203]
	v_rcp_f32_e32 v204, v204
	v_pk_mul_f32 v[190:191], v[186:187], v[2:3] op_sel_hi:[1,0]
	v_pk_mul_f32 v[24:25], v[24:25], v[4:5] op_sel_hi:[1,0]
	v_exp_f32_e32 v32, v32
	v_pk_mul_f32 v[192:193], v[188:189], v[2:3] op_sel_hi:[1,0]
	v_pk_mul_f32 v[200:201], v[40:41], v[250:251] op_sel:[0,1] op_sel_hi:[1,1]
	v_cvt_pk_fp8_f32 v6, v6, v7
	v_med3_f32 v15, v15, s87, v227
	v_med3_f32 v17, v17, s87, v227
	v_med3_f32 v24, v24, s87, v227
	v_rcp_f32_e32 v208, v208
	v_pk_mul_f32 v[202:203], v[200:201], v[2:3] op_sel_hi:[1,0]
	v_exp_f32_e32 v190, v190
	v_cvt_pk_fp8_f32 v6, v14, v15 op_sel:[0,0,1]
	v_exp_f32_e32 v192, v192
	v_cvt_pk_fp8_f32 v7, v16, v17
	v_rcp_f32_e32 v23, v23
	v_med3_f32 v25, v25, s87, v227
	v_exp_f32_e32 v202, v202
	v_add_u32_e32 v14, 0x70000, v241
	v_rcp_f32_e32 v31, v31
	v_cvt_pk_fp8_f32 v7, v24, v25 op_sel:[0,0,1]
	global_store_dwordx2 v14, v[12:13], s[26:27]
	v_rcp_f32_e32 v205, v205
	v_pk_mul_f32 v[12:13], v[58:59], v[250:251] op_sel_hi:[1,0]
	v_exp_f32_e32 v33, v33
	v_pk_mul_f32 v[14:15], v[60:61], v[250:251] op_sel_hi:[1,0]
	v_rcp_f32_e32 v209, v209
	v_pk_mul_f32 v[12:13], v[12:13], v[18:19]
	v_exp_f32_e32 v191, v191
	v_pk_mul_f32 v[16:17], v[50:51], v[250:251] op_sel_hi:[1,0]
	v_exp_f32_e32 v193, v193
	v_pk_mul_f32 v[12:13], v[12:13], v[22:23]
	v_exp_f32_e32 v203, v203
	v_pk_add_f32 v[32:33], v[32:33], v[2:3] op_sel:[0,1] op_sel_hi:[1,1]
	v_pk_mul_f32 v[12:13], v[12:13], v[4:5] op_sel_hi:[1,0]
	v_pk_mul_f32 v[14:15], v[14:15], v[26:27]
	v_pk_mul_f32 v[16:17], v[16:17], v[28:29]
	v_med3_f32 v12, v12, s87, v227
	v_pk_mul_f32 v[14:15], v[14:15], v[30:31]
	v_pk_mul_f32 v[16:17], v[16:17], v[204:205]
	v_pk_mul_f32 v[18:19], v[52:53], v[250:251] op_sel_hi:[1,0]
	v_pk_mul_f32 v[14:15], v[14:15], v[4:5] op_sel_hi:[1,0]
	v_pk_mul_f32 v[16:17], v[16:17], v[4:5] op_sel_hi:[1,0]
	v_rcp_f32_e32 v32, v32
	v_pk_add_f32 v[190:191], v[190:191], v[2:3] op_sel:[0,1] op_sel_hi:[1,1]
	v_pk_add_f32 v[192:193], v[192:193], v[2:3] op_sel:[0,1] op_sel_hi:[1,1]
	v_med3_f32 v13, v13, s87, v227
	v_med3_f32 v14, v14, s87, v227
	v_med3_f32 v16, v16, s87, v227
	v_pk_mul_f32 v[18:19], v[18:19], v[206:207]
	v_rcp_f32_e32 v190, v190
	v_pk_add_f32 v[202:203], v[202:203], v[2:3] op_sel:[0,1] op_sel_hi:[1,1]
	v_pk_mul_f32 v[18:19], v[18:19], v[208:209]
	v_rcp_f32_e32 v192, v192
	v_cvt_pk_fp8_f32 v12, v12, v13
	v_pk_mul_f32 v[18:19], v[18:19], v[4:5] op_sel_hi:[1,0]
	v_med3_f32 v15, v15, s87, v227
	v_med3_f32 v17, v17, s87, v227
	v_med3_f32 v18, v18, s87, v227
	v_rcp_f32_e32 v202, v202
	v_cvt_pk_fp8_f32 v12, v14, v15 op_sel:[0,0,1]
	v_rcp_f32_e32 v33, v33
	v_cvt_pk_fp8_f32 v13, v16, v17
	v_med3_f32 v19, v19, s87, v227
	v_add_u32_e32 v14, 0x7e000, v241
	v_rcp_f32_e32 v191, v191
	v_cvt_pk_fp8_f32 v13, v18, v19 op_sel:[0,0,1]
	global_store_dwordx2 v14, v[6:7], s[26:27]
	v_rcp_f32_e32 v193, v193
	v_pk_mul_f32 v[6:7], v[42:43], v[250:251] op_sel:[0,1] op_sel_hi:[1,1]
	v_rcp_f32_e32 v203, v203
	v_pk_mul_f32 v[14:15], v[44:45], v[250:251] op_sel:[0,1] op_sel_hi:[1,1]
	v_pk_mul_f32 v[6:7], v[6:7], v[20:21]
	v_pk_mul_f32 v[16:17], v[34:35], v[250:251] op_sel:[0,1] op_sel_hi:[1,1]
	v_pk_mul_f32 v[14:15], v[14:15], v[186:187]
	v_pk_mul_f32 v[6:7], v[6:7], v[32:33]
	v_pk_mul_f32 v[16:17], v[16:17], v[188:189]
	v_pk_mul_f32 v[14:15], v[14:15], v[190:191]
	v_pk_mul_f32 v[6:7], v[6:7], v[4:5] op_sel_hi:[1,0]
	v_pk_mul_f32 v[16:17], v[16:17], v[192:193]
	v_pk_mul_f32 v[14:15], v[14:15], v[4:5] op_sel_hi:[1,0]
	v_med3_f32 v6, v6, s87, v227
	v_pk_mul_f32 v[16:17], v[16:17], v[4:5] op_sel_hi:[1,0]
	v_pk_mul_f32 v[18:19], v[36:37], v[250:251] op_sel:[0,1] op_sel_hi:[1,1]
	v_med3_f32 v7, v7, s87, v227
	v_med3_f32 v14, v14, s87, v227
	v_med3_f32 v16, v16, s87, v227
	v_pk_mul_f32 v[18:19], v[18:19], v[200:201]
	v_cvt_pk_fp8_f32 v6, v6, v7
	v_med3_f32 v15, v15, s87, v227
	v_pk_mul_f32 v[18:19], v[18:19], v[202:203]
	v_med3_f32 v17, v17, s87, v227
	v_cvt_pk_fp8_f32 v6, v14, v15 op_sel:[0,0,1]
	v_pk_mul_f32 v[18:19], v[18:19], v[4:5] op_sel_hi:[1,0]
	v_cvt_pk_fp8_f32 v7, v16, v17
	v_add_u32_e32 v14, 0x8c000, v241
	v_med3_f32 v18, v18, s87, v227
	v_add_u32_e32 v15, 0x9a000, v241
	global_store_dwordx2 v14, v[12:13], s[26:27]
	v_med3_f32 v19, v19, s87, v227
	v_mfma_f32_32x32x16_bf16 v[34:49], v[8:11], v[8:11], 0
	v_mfma_f32_32x32x16_bf16 v[50:65], v[8:11], v[8:11], 0
	v_cvt_pk_fp8_f32 v7, v18, v19 op_sel:[0,0,1]
	v_mfma_f32_32x32x16_bf16 v[66:81], v[8:11], v[8:11], 0
	v_mfma_f32_32x32x16_bf16 v[82:97], v[8:11], v[8:11], 0
	global_store_dwordx2 v15, v[6:7], s[26:27]
	v_mfma_f32_32x32x16_bf16 v[98:113], v[8:11], v[8:11], 0
	v_mfma_f32_32x32x16_bf16 v[114:129], v[8:11], v[8:11], 0
	v_mfma_f32_32x32x16_bf16 v[130:145], v[8:11], v[8:11], 0
	v_mfma_f32_32x32x16_bf16 v[146:161], v[8:11], v[8:11], 0
	s_nop 15
	s_andn2_b64 vcc, exec, s[44:45]
	s_mov_b64 s[44:45], -1
	s_cbranch_vccnz .LBB0_832
	s_andn2_b64 vcc, exec, s[30:31]
	s_cbranch_vccnz .LBB0_831
	s_barrier
	s_branch .LBB0_831

.LBB0_1360:
	s_mov_b32 m0, s100
	s_add_i32 s71, s71, -1
	s_mul_hi_u32 s42, s71, 0xaaaaaaab
	s_lshr_b32 s42, s42, 1
	s_mul_i32 s42, s42, 3
	s_sub_i32 s42, s71, s42
	v_lshl_add_u32 v66, s42, 13, v240
	ds_read_b64_tr_b16 v[68:69], v66 offset:40960
	ds_read_b64_tr_b16 v[70:71], v66 offset:41472
	ds_read_b64_tr_b16 v[72:73], v66 offset:41984
	ds_read_b64_tr_b16 v[74:75], v66 offset:42496
	ds_read_b64_tr_b16 v[76:77], v66 offset:43008
	ds_read_b64_tr_b16 v[78:79], v66 offset:43520
	ds_read_b64_tr_b16 v[80:81], v66 offset:44032
	ds_read_b64_tr_b16 v[82:83], v66 offset:44544
	ds_read_b64_tr_b16 v[84:85], v66 offset:45056
	ds_read_b64_tr_b16 v[86:87], v66 offset:45568
	ds_read_b64_tr_b16 v[88:89], v66 offset:46080
	ds_read_b64_tr_b16 v[90:91], v66 offset:46592
	ds_read_b64_tr_b16 v[92:93], v66 offset:47104
	ds_read_b64_tr_b16 v[94:95], v66 offset:47616
	ds_read_b64_tr_b16 v[96:97], v66 offset:48128
	ds_read_b64_tr_b16 v[98:99], v66 offset:48640
	v_add_f32_e32 v66, v50, v51
	v_add_f32_e32 v67, v52, v53
	v_add_f32_e32 v66, v66, v67
	v_add_f32_e32 v66, 0, v66
	v_add_f32_e32 v67, v54, v55
	v_add_f32_e32 v100, v56, v57
	v_add_f32_e32 v67, v67, v100
	v_add_f32_e32 v66, v67, v66
	v_add_f32_e32 v67, v58, v59
	v_add_f32_e32 v100, v60, v61
	v_add_f32_e32 v67, v67, v100
	v_add_f32_e32 v66, v67, v66
	v_add_f32_e32 v67, v62, v63
	v_add_f32_e32 v100, v64, v65
	v_add_f32_e32 v67, v67, v100
	v_add_f32_e32 v66, v67, v66
	v_add_f32_e32 v67, v34, v35
	v_add_f32_e32 v100, v36, v37
	v_add_f32_e32 v67, v67, v100
	v_add_f32_e32 v66, v67, v66
	v_add_f32_e32 v67, v38, v39
	v_add_f32_e32 v100, v40, v41
	v_add_f32_e32 v67, v67, v100
	v_add_f32_e32 v66, v67, v66
	v_add_f32_e32 v67, v42, v43
	v_add_f32_e32 v100, v44, v45
	v_add_f32_e32 v67, v67, v100
	v_add_f32_e32 v66, v67, v66
	v_add_f32_e32 v67, v46, v47
	v_add_f32_e32 v100, v48, v49
	v_add_f32_e32 v67, v67, v100
	s_mov_b64 s[72:73], 0xe800000
	v_add_f32_e32 v66, v67, v66
	v_cvt_pk_bf16_f32 v50, v50, v51
	v_cvt_pk_bf16_f32 v51, v52, v53
	v_cvt_pk_bf16_f32 v52, v54, v55
	v_cvt_pk_bf16_f32 v53, v56, v57
	v_cvt_pk_bf16_f32 v54, v58, v59
	v_cvt_pk_bf16_f32 v55, v60, v61
	v_cvt_pk_bf16_f32 v56, v62, v63
	v_cvt_pk_bf16_f32 v57, v64, v65
	v_cvt_pk_bf16_f32 v34, v34, v35
	v_cvt_pk_bf16_f32 v35, v36, v37
	v_cvt_pk_bf16_f32 v36, v38, v39
	v_cvt_pk_bf16_f32 v37, v40, v41
	v_cvt_pk_bf16_f32 v38, v42, v43
	v_cvt_pk_bf16_f32 v39, v44, v45
	v_cvt_pk_bf16_f32 v40, v46, v47
	v_cvt_pk_bf16_f32 v41, v48, v49
	s_waitcnt lgkmcnt(14)
	v_mfma_f32_32x32x16_bf16 v[2:17], v[50:53], v[68:71], v[2:17]
	s_waitcnt lgkmcnt(6)
	v_mfma_f32_32x32x16_bf16 v[18:33], v[50:53], v[84:87], v[18:33]
	v_mfma_f32_32x32x16_bf16 v[2:17], v[54:57], v[72:75], v[2:17]
	s_waitcnt lgkmcnt(4)
	v_mfma_f32_32x32x16_bf16 v[18:33], v[54:57], v[88:91], v[18:33]
	v_mfma_f32_32x32x16_bf16 v[2:17], v[34:37], v[76:79], v[2:17]
	s_waitcnt lgkmcnt(2)
	v_mfma_f32_32x32x16_bf16 v[18:33], v[34:37], v[92:95], v[18:33]
	v_mfma_f32_32x32x16_bf16 v[2:17], v[38:41], v[80:83], v[2:17]
	s_waitcnt lgkmcnt(0)
	v_mfma_f32_32x32x16_bf16 v[18:33], v[38:41], v[96:99], v[18:33]
	v_mov_b32_e32 v50, 0
	s_and_saveexec_b64 s[42:43], s[38:39]
	s_mov_b64 s[70:71], 0xe800800
	s_cbranch_execz .LBB0_1364
	s_mov_b64 s[50:51], exec
	v_mbcnt_lo_u32_b32 v34, s50, 0
	v_mbcnt_hi_u32_b32 v34, s51, v34
	v_cmp_eq_u32_e32 vcc, 0, v34
	s_and_saveexec_b64 s[44:45], vcc
	s_cbranch_execz .LBB0_1363
	s_bcnt1_i32_b64 s50, s[50:51]
	v_mov_b32_e32 v35, s50
	global_atomic_add v50, v167, v35, s[36:37] sc0
.LBB0_1363:
	s_or_b64 exec, exec, s[44:45]
.LBB0_1364:
	s_or_b64 exec, exec, s[42:43]
	s_lshl_b64 s[42:43], s[48:49], 1
	s_add_u32 s44, s11, s42
	s_addc_u32 s45, s12, s43
	s_add_u32 s44, s44, s46
	s_addc_u32 s45, s45, s47
	v_lshlrev_b32_e32 v166, 1, v184
	v_lshl_add_u64 v[34:35], s[44:45], 0, v[166:167]
	v_mov_b32_e32 v197, v167
	v_lshl_add_u64 v[34:35], v[34:35], 0, v[196:197]
	s_movk_i32 s44, 0x4000
	v_add_co_u32_e32 v36, vcc, s44, v34
	flat_load_dwordx4 v[46:49], v[34:35]
	s_nop 0
	v_addc_co_u32_e32 v37, vcc, 0, v35, vcc
	flat_load_dwordx4 v[42:45], v[36:37]
	v_add_co_u32_e32 v36, vcc, 0x8000, v34
	s_and_b32 s25, s25, 0x3fffffc0
	s_nop 0
	v_addc_co_u32_e32 v37, vcc, 0, v35, vcc
	v_add_co_u32_e32 v34, vcc, 0xc000, v34
	flat_load_dwordx4 v[38:41], v[36:37]
	s_nop 0
	v_addc_co_u32_e32 v35, vcc, 0, v35, vcc
	flat_load_dwordx4 v[34:37], v[34:35]
	v_add_f32_e32 v51, v193, v66
	s_lshl_b32 s25, s25, 2
	v_mov_b32_e32 v52, v51
	s_add_i32 s25, s25, 0
	s_nop 0
	v_permlane32_swap_b32_e32 v51, v52
	s_add_i32 s25, s25, 0x10000
	s_and_saveexec_b64 s[44:45], s[40:41]
	v_lshl_add_u32 v53, v236, 2, s25
	v_add_f32_e32 v51, v51, v52
	ds_write_b32 v53, v51
	s_or_b64 exec, exec, s[44:45]
	s_waitcnt lgkmcnt(0)
	v_lshl_add_u32 v51, v239, 2, s25
	ds_read_b128 v[52:55], v51
	ds_read_b128 v[56:59], v51 offset:32
	s_add_u32 s42, s8, s42
	s_addc_u32 s25, s10, s43
	s_add_u32 s42, s42, s46
	s_waitcnt lgkmcnt(0)
	v_rcp_f32_e32 v60, v52
	v_rcp_f32_e32 v61, v53
	v_rcp_f32_e32 v62, v54
	v_rcp_f32_e32 v63, v55
	v_rcp_f32_e32 v64, v56
	ds_read_b128 v[52:55], v51 offset:64
	v_rcp_f32_e32 v65, v57
	v_rcp_f32_e32 v66, v58
	v_rcp_f32_e32 v67, v59
	ds_read_b128 v[56:59], v51 offset:96
	s_addc_u32 s43, s25, s47
	s_lshl_b32 s24, s24, 12
	s_add_i32 s24, s24, 0
	v_mul_f32_e32 v2, v2, v60
	s_waitcnt lgkmcnt(0)
	v_rcp_f32_e32 v51, v52
	v_rcp_f32_e32 v52, v53
	v_rcp_f32_e32 v53, v54
	v_rcp_f32_e32 v54, v55
	v_rcp_f32_e32 v55, v56
	v_rcp_f32_e32 v56, v57
	v_rcp_f32_e32 v57, v58
	v_rcp_f32_e32 v58, v59
	s_add_i32 s24, s24, 0x10800
	v_lshlrev_b32_e32 v59, 1, v236
	v_bfe_u32 v68, v2, 16, 1
	v_add3_u32 v59, s24, v59, v241
	v_add3_u32 v2, v2, v68, s9
	ds_write_b16_d16_hi v59, v2
	v_mul_f32_e32 v2, v18, v60
	v_bfe_u32 v18, v2, 16, 1
	v_add3_u32 v2, v2, v18, s9
	ds_write_b16_d16_hi v59, v2 offset:64
	v_mul_f32_e32 v2, v3, v61
	v_bfe_u32 v3, v2, 16, 1
	v_add3_u32 v2, v2, v3, s9
	ds_write_b16_d16_hi v59, v2 offset:128
	v_mul_f32_e32 v2, v19, v61
	v_bfe_u32 v3, v2, 16, 1
	v_add3_u32 v2, v2, v3, s9
	ds_write_b16_d16_hi v59, v2 offset:192
	v_mul_f32_e32 v2, v4, v62
	v_bfe_u32 v3, v2, 16, 1
	v_add3_u32 v2, v2, v3, s9
	ds_write_b16_d16_hi v59, v2 offset:256
	v_mul_f32_e32 v2, v20, v62
	v_bfe_u32 v3, v2, 16, 1
	v_add3_u32 v2, v2, v3, s9
	ds_write_b16_d16_hi v59, v2 offset:320
	v_mul_f32_e32 v2, v5, v63
	v_bfe_u32 v3, v2, 16, 1
	v_add3_u32 v2, v2, v3, s9
	ds_write_b16_d16_hi v59, v2 offset:384
	v_mul_f32_e32 v2, v21, v63
	v_bfe_u32 v3, v2, 16, 1
	v_add3_u32 v2, v2, v3, s9
	ds_write_b16_d16_hi v59, v2 offset:448
	v_mul_f32_e32 v2, v6, v64
	v_bfe_u32 v3, v2, 16, 1
	v_add3_u32 v2, v2, v3, s9
	ds_write_b16_d16_hi v59, v2 offset:1024
	v_mul_f32_e32 v2, v22, v64
	v_bfe_u32 v3, v2, 16, 1
	v_add3_u32 v2, v2, v3, s9
	ds_write_b16_d16_hi v59, v2 offset:1088
	v_mul_f32_e32 v2, v7, v65
	v_bfe_u32 v3, v2, 16, 1
	v_add3_u32 v2, v2, v3, s9
	ds_write_b16_d16_hi v59, v2 offset:1152
	v_mul_f32_e32 v2, v23, v65
	v_bfe_u32 v3, v2, 16, 1
	v_add3_u32 v2, v2, v3, s9
	ds_write_b16_d16_hi v59, v2 offset:1216
	v_mul_f32_e32 v2, v8, v66
	v_bfe_u32 v3, v2, 16, 1
	v_add3_u32 v2, v2, v3, s9
	ds_write_b16_d16_hi v59, v2 offset:1280
	v_mul_f32_e32 v2, v24, v66
	v_bfe_u32 v3, v2, 16, 1
	v_add3_u32 v2, v2, v3, s9
	ds_write_b16_d16_hi v59, v2 offset:1344
	v_mul_f32_e32 v2, v9, v67
	v_bfe_u32 v3, v2, 16, 1
	v_add3_u32 v2, v2, v3, s9
	ds_write_b16_d16_hi v59, v2 offset:1408
	v_mul_f32_e32 v2, v25, v67
	v_bfe_u32 v3, v2, 16, 1
	v_add3_u32 v2, v2, v3, s9
	ds_write_b16_d16_hi v59, v2 offset:1472
	v_mul_f32_e32 v2, v10, v51
	v_bfe_u32 v3, v2, 16, 1
	v_add3_u32 v2, v2, v3, s9
	ds_write_b16_d16_hi v59, v2 offset:2048
	v_mul_f32_e32 v2, v26, v51
	v_bfe_u32 v3, v2, 16, 1
	v_add3_u32 v2, v2, v3, s9
	ds_write_b16_d16_hi v59, v2 offset:2112
	v_mul_f32_e32 v2, v11, v52
	v_bfe_u32 v3, v2, 16, 1
	v_add3_u32 v2, v2, v3, s9
	ds_write_b16_d16_hi v59, v2 offset:2176
	v_mul_f32_e32 v2, v27, v52
	v_bfe_u32 v3, v2, 16, 1
	v_add3_u32 v2, v2, v3, s9
	ds_write_b16_d16_hi v59, v2 offset:2240
	v_mul_f32_e32 v2, v12, v53
	v_bfe_u32 v3, v2, 16, 1
	v_add3_u32 v2, v2, v3, s9
	ds_write_b16_d16_hi v59, v2 offset:2304
	v_mul_f32_e32 v2, v28, v53
	v_bfe_u32 v3, v2, 16, 1
	v_add3_u32 v2, v2, v3, s9
	ds_write_b16_d16_hi v59, v2 offset:2368
	v_mul_f32_e32 v2, v13, v54
	v_bfe_u32 v3, v2, 16, 1
	v_add3_u32 v2, v2, v3, s9
	ds_write_b16_d16_hi v59, v2 offset:2432
	v_mul_f32_e32 v2, v29, v54
	v_bfe_u32 v3, v2, 16, 1
	v_add3_u32 v2, v2, v3, s9
	ds_write_b16_d16_hi v59, v2 offset:2496
	v_mul_f32_e32 v2, v14, v55
	v_bfe_u32 v3, v2, 16, 1
	v_add3_u32 v2, v2, v3, s9
	ds_write_b16_d16_hi v59, v2 offset:3072
	v_mul_f32_e32 v2, v30, v55
	v_bfe_u32 v3, v2, 16, 1
	v_add3_u32 v2, v2, v3, s9
	ds_write_b16_d16_hi v59, v2 offset:3136
	v_mul_f32_e32 v2, v15, v56
	v_bfe_u32 v3, v2, 16, 1
	v_add3_u32 v2, v2, v3, s9
	ds_write_b16_d16_hi v59, v2 offset:3200
	v_mul_f32_e32 v2, v31, v56
	v_bfe_u32 v3, v2, 16, 1
	v_add3_u32 v2, v2, v3, s9
	ds_write_b16_d16_hi v59, v2 offset:3264
	v_mul_f32_e32 v2, v16, v57
	v_bfe_u32 v3, v2, 16, 1
	v_add3_u32 v2, v2, v3, s9
	ds_write_b16_d16_hi v59, v2 offset:3328
	v_mul_f32_e32 v2, v32, v57
	v_bfe_u32 v3, v2, 16, 1
	v_add3_u32 v2, v2, v3, s9
	ds_write_b16_d16_hi v59, v2 offset:3392
	v_mul_f32_e32 v2, v17, v58
	v_bfe_u32 v3, v2, 16, 1
	v_add3_u32 v2, v2, v3, s9
	ds_write_b16_d16_hi v59, v2 offset:3456
	v_mul_f32_e32 v2, v33, v58
	v_bfe_u32 v3, v2, 16, 1
	v_add3_u32 v2, v2, v3, s9
	ds_write_b16_d16_hi v59, v2 offset:3520
	v_add_u32_e32 v10, s24, v166
	s_waitcnt lgkmcnt(0)
	v_add_u32_e32 v2, v10, v242
	ds_read_b128 v[2:5], v2
	s_waitcnt vmcnt(0)
	v_lshlrev_b32_e32 v9, 16, v46
	v_lshl_add_u64 v[6:7], s[42:43], 0, v[166:167]
	v_mov_b32_e32 v199, v167
	v_mov_b32_e32 v201, v167
	s_waitcnt lgkmcnt(0)
	v_lshlrev_b32_e32 v8, 16, v2
	v_mul_f32_e32 v8, v8, v9
	v_and_b32_e32 v2, 0xffff0000, v2
	v_and_b32_e32 v9, 0xffff0000, v46
	v_mul_f32_e32 v2, v2, v9
	v_cvt_pk_bf16_f32 v2, v8, v2
	v_lshlrev_b32_e32 v8, 16, v3
	v_lshlrev_b32_e32 v9, 16, v47
	v_mul_f32_e32 v8, v8, v9
	v_and_b32_e32 v3, 0xffff0000, v3
	v_and_b32_e32 v9, 0xffff0000, v47
	v_mul_f32_e32 v3, v3, v9
	v_cvt_pk_bf16_f32 v3, v8, v3
	v_lshlrev_b32_e32 v8, 16, v4
	v_lshlrev_b32_e32 v9, 16, v48
	v_mul_f32_e32 v8, v8, v9
	v_and_b32_e32 v4, 0xffff0000, v4
	v_and_b32_e32 v9, 0xffff0000, v48
	v_mul_f32_e32 v4, v4, v9
	v_cvt_pk_bf16_f32 v4, v8, v4
	v_lshlrev_b32_e32 v8, 16, v5
	v_lshlrev_b32_e32 v9, 16, v49
	v_mul_f32_e32 v8, v8, v9
	v_and_b32_e32 v5, 0xffff0000, v5
	v_and_b32_e32 v9, 0xffff0000, v49
	v_mul_f32_e32 v5, v5, v9
	v_cvt_pk_bf16_f32 v5, v8, v5
	v_lshl_add_u64 v[8:9], v[6:7], 0, v[198:199]
	flat_store_dwordx4 v[8:9], v[2:5]
	v_lshlrev_b32_e32 v9, 16, v42
	v_mov_b32_e32 v203, v167
	v_add_u32_e32 v2, v10, v243
	ds_read_b128 v[2:5], v2
	v_mov_b32_e32 v205, v167
	s_waitcnt lgkmcnt(0)
	v_lshlrev_b32_e32 v8, 16, v2
	v_mul_f32_e32 v8, v8, v9
	v_and_b32_e32 v2, 0xffff0000, v2
	v_and_b32_e32 v9, 0xffff0000, v42
	v_mul_f32_e32 v2, v2, v9
	v_cvt_pk_bf16_f32 v2, v8, v2
	v_lshlrev_b32_e32 v8, 16, v3
	v_lshlrev_b32_e32 v9, 16, v43
	v_mul_f32_e32 v8, v8, v9
	v_and_b32_e32 v3, 0xffff0000, v3
	v_and_b32_e32 v9, 0xffff0000, v43
	v_mul_f32_e32 v3, v3, v9
	v_cvt_pk_bf16_f32 v3, v8, v3
	v_lshlrev_b32_e32 v8, 16, v4
	v_lshlrev_b32_e32 v9, 16, v44
	v_mul_f32_e32 v8, v8, v9
	v_and_b32_e32 v4, 0xffff0000, v4
	v_and_b32_e32 v9, 0xffff0000, v44
	v_mul_f32_e32 v4, v4, v9
	v_cvt_pk_bf16_f32 v4, v8, v4
	v_lshlrev_b32_e32 v8, 16, v5
	v_lshlrev_b32_e32 v9, 16, v45
	v_mul_f32_e32 v8, v8, v9
	v_and_b32_e32 v5, 0xffff0000, v5
	v_and_b32_e32 v9, 0xffff0000, v45
	v_mul_f32_e32 v5, v5, v9
	v_cvt_pk_bf16_f32 v5, v8, v5
	v_lshl_add_u64 v[8:9], v[6:7], 0, v[200:201]
	flat_store_dwordx4 v[8:9], v[2:5]
	v_lshlrev_b32_e32 v9, 16, v38
	s_nop 0
	v_add_u32_e32 v2, v10, v244
	ds_read_b128 v[2:5], v2
	s_waitcnt lgkmcnt(0)
	v_lshlrev_b32_e32 v8, 16, v2
	v_mul_f32_e32 v8, v8, v9
	v_and_b32_e32 v2, 0xffff0000, v2
	v_and_b32_e32 v9, 0xffff0000, v38
	v_mul_f32_e32 v2, v2, v9
	v_cvt_pk_bf16_f32 v2, v8, v2
	v_lshlrev_b32_e32 v8, 16, v3
	v_lshlrev_b32_e32 v9, 16, v39
	v_mul_f32_e32 v8, v8, v9
	v_and_b32_e32 v3, 0xffff0000, v3
	v_and_b32_e32 v9, 0xffff0000, v39
	v_mul_f32_e32 v3, v3, v9
	v_cvt_pk_bf16_f32 v3, v8, v3
	v_lshlrev_b32_e32 v8, 16, v4
	v_lshlrev_b32_e32 v9, 16, v40
	v_mul_f32_e32 v8, v8, v9
	v_and_b32_e32 v4, 0xffff0000, v4
	v_and_b32_e32 v9, 0xffff0000, v40
	v_mul_f32_e32 v4, v4, v9
	v_cvt_pk_bf16_f32 v4, v8, v4
	v_lshlrev_b32_e32 v8, 16, v5
	v_lshlrev_b32_e32 v9, 16, v41
	v_mul_f32_e32 v8, v8, v9
	v_and_b32_e32 v5, 0xffff0000, v5
	v_and_b32_e32 v9, 0xffff0000, v41
	v_mul_f32_e32 v5, v5, v9
	v_cvt_pk_bf16_f32 v5, v8, v5
	v_lshl_add_u64 v[8:9], v[6:7], 0, v[202:203]
	flat_store_dwordx4 v[8:9], v[2:5]
	v_lshlrev_b32_e32 v9, 16, v34
	v_lshl_add_u64 v[6:7], v[6:7], 0, v[204:205]
	v_add_u32_e32 v2, v10, v245
	ds_read_b128 v[2:5], v2
	s_waitcnt lgkmcnt(0)
	v_lshlrev_b32_e32 v8, 16, v2
	v_mul_f32_e32 v8, v8, v9
	v_and_b32_e32 v2, 0xffff0000, v2
	v_and_b32_e32 v9, 0xffff0000, v34
	v_mul_f32_e32 v2, v2, v9
	v_cvt_pk_bf16_f32 v2, v8, v2
	v_lshlrev_b32_e32 v8, 16, v3
	v_lshlrev_b32_e32 v9, 16, v35
	v_mul_f32_e32 v8, v8, v9
	v_and_b32_e32 v3, 0xffff0000, v3
	v_and_b32_e32 v9, 0xffff0000, v35
	v_mul_f32_e32 v3, v3, v9
	v_cvt_pk_bf16_f32 v3, v8, v3
	v_lshlrev_b32_e32 v8, 16, v4
	v_lshlrev_b32_e32 v9, 16, v36
	v_mul_f32_e32 v8, v8, v9
	v_and_b32_e32 v4, 0xffff0000, v4
	v_and_b32_e32 v9, 0xffff0000, v36
	v_mul_f32_e32 v4, v4, v9
	v_cvt_pk_bf16_f32 v4, v8, v4
	v_lshlrev_b32_e32 v8, 16, v5
	v_lshlrev_b32_e32 v9, 16, v37
	v_mul_f32_e32 v8, v8, v9
	v_and_b32_e32 v5, 0xffff0000, v5
	v_and_b32_e32 v9, 0xffff0000, v37
	v_mul_f32_e32 v5, v5, v9
	v_cvt_pk_bf16_f32 v5, v8, v5
	flat_store_dwordx4 v[6:7], v[2:5]
	s_and_saveexec_b64 s[42:43], s[38:39]
	s_cbranch_execz .LBB0_1260
	v_mov_b32_e32 v2, s89
	ds_write_b32 v2, v50
	s_branch .LBB0_1260

.LBB0_1673:
	v_bfe_u32 v8, v6, 4, 2
	s_add_u32 s36, s38, 0x16800000
	v_and_b32_e32 v7, 15, v6
	v_lshlrev_b32_e32 v9, 4, v8
	v_lshlrev_b32_e32 v6, 2, v6
	s_addc_u32 s37, s39, 0
	v_lshl_or_b32 v209, s40, 6, v7
	v_lshl_or_b32 v7, v7, 6, v9
	s_lshl_b32 s40, s40, 13
	v_and_b32_e32 v6, 32, v6
	v_bitop3_b32 v9, v7, s40, v6 bitop3:0xde
	s_lshl_b32 s40, s41, 5
	s_and_b32 s50, s40, 0x60
	s_add_i32 m0, s59, 0x18000
	v_lshl_add_u64 v[2:3], v[2:3], 0, s[56:57]
	s_lshl_b32 s40, s50, 7
	s_waitcnt vmcnt(2)
	s_barrier
	global_load_lds_dwordx4 v[2:3], off
	s_add_i32 m0, s59, 0x1a000
	v_bitop3_b32 v210, v7, s40, v6 bitop3:0xde
	s_add_u32 s40, s38, 0xe800080
	v_lshl_add_u64 v[2:3], v[4:5], 0, s[56:57]
	s_addc_u32 s41, s39, 0
	s_add_i32 s77, s59, 0x8000
	s_add_i32 s79, s59, 0xa000
	v_mov_b32_e32 v179, v167
	global_load_lds_dwordx4 v[2:3], off
	v_lshl_add_u64 v[2:3], s[40:41], 0, v[166:167]
	s_mov_b32 m0, s77
	s_add_u32 s38, s64, 0x20080
	global_load_lds_dwordx4 v[2:3], off
	v_lshl_add_u64 v[2:3], s[40:41], 0, v[178:179]
	s_mov_b32 m0, s79
	s_addc_u32 s39, s65, 0
	global_load_lds_dwordx4 v[2:3], off
	s_add_i32 m0, s59, 0x1c000
	v_lshl_add_u64 v[2:3], s[38:39], 0, v[162:163]
	global_load_lds_dwordx4 v[2:3], off
	v_lshl_add_u64 v[2:3], s[38:39], 0, v[164:165]
	s_add_i32 m0, s59, 0x1e000
	s_cmp_gt_i32 s11, 0
	global_load_lds_dwordx4 v[2:3], off
	s_cselect_b64 s[42:43], -1, 0
	s_add_i32 s88, s11, -2
	s_cmpk_lt_u32 s44, 0x100
	s_cselect_b64 s[44:45], -1, 0
	s_cmp_gt_i32 s1, -1
	s_waitcnt vmcnt(6)
	s_cselect_b64 s[46:47], -1, 0
	s_ashr_i32 s90, s8, 31
	s_mul_i32 s39, s8, 0x7fffffff
	s_mul_hi_i32 s38, s8, 0x7fffffff
	s_add_u32 s48, s39, s1
	s_mov_b32 s84, 0
	s_addc_u32 s49, s38, 0
	v_lshl_or_b32 v211, v8, 3, s50
	v_add_u32_e32 v212, 0, v9
	s_barrier
	v_mov_b32_e32 v34, 0
	v_mov_b32_e32 v35, 0
	v_mov_b32_e32 v36, 0
	v_mov_b32_e32 v37, 0
	v_mov_b32_e32 v38, 0
	v_mov_b32_e32 v39, 0
	v_mov_b32_e32 v40, 0
	v_mov_b32_e32 v41, 0
	v_mov_b32_e32 v42, 0
	v_mov_b32_e32 v43, 0
	v_mov_b32_e32 v44, 0
	v_mov_b32_e32 v45, 0
	v_mov_b32_e32 v46, 0
	v_mov_b32_e32 v47, 0
	v_mov_b32_e32 v48, 0
	v_mov_b32_e32 v49, 0
	v_mov_b32_e32 v50, 0
	v_mov_b32_e32 v51, 0
	v_mov_b32_e32 v52, 0
	v_mov_b32_e32 v53, 0
	v_mov_b32_e32 v54, 0
	v_mov_b32_e32 v55, 0
	v_mov_b32_e32 v56, 0
	v_mov_b32_e32 v57, 0
	v_mov_b32_e32 v58, 0
	v_mov_b32_e32 v59, 0
	v_mov_b32_e32 v60, 0
	v_mov_b32_e32 v61, 0
	v_mov_b32_e32 v62, 0
	v_mov_b32_e32 v63, 0
	v_mov_b32_e32 v64, 0
	v_mov_b32_e32 v65, 0
	v_mov_b32_e32 v66, 0
	v_mov_b32_e32 v67, 0
	v_mov_b32_e32 v68, 0
	v_mov_b32_e32 v69, 0
	v_mov_b32_e32 v70, 0
	v_mov_b32_e32 v71, 0
	v_mov_b32_e32 v72, 0
	v_mov_b32_e32 v73, 0
	v_mov_b32_e32 v74, 0
	v_mov_b32_e32 v75, 0
	v_mov_b32_e32 v76, 0
	v_mov_b32_e32 v77, 0
	v_mov_b32_e32 v78, 0
	v_mov_b32_e32 v79, 0
	v_mov_b32_e32 v80, 0
	v_mov_b32_e32 v81, 0
	v_mov_b32_e32 v82, 0
	v_mov_b32_e32 v83, 0
	v_mov_b32_e32 v84, 0
	v_mov_b32_e32 v85, 0
	v_mov_b32_e32 v86, 0
	v_mov_b32_e32 v87, 0
	v_mov_b32_e32 v88, 0
	v_mov_b32_e32 v89, 0
	v_mov_b32_e32 v90, 0
	v_mov_b32_e32 v91, 0
	v_mov_b32_e32 v92, 0
	v_mov_b32_e32 v93, 0
	v_mov_b32_e32 v94, 0
	v_mov_b32_e32 v95, 0
	v_mov_b32_e32 v96, 0
	v_mov_b32_e32 v97, 0
	v_mov_b32_e32 v98, 0
	v_mov_b32_e32 v99, 0
	v_mov_b32_e32 v100, 0
	v_mov_b32_e32 v101, 0
	v_mov_b32_e32 v102, 0
	v_mov_b32_e32 v103, 0
	v_mov_b32_e32 v104, 0
	v_mov_b32_e32 v105, 0
	v_mov_b32_e32 v106, 0
	v_mov_b32_e32 v107, 0
	v_mov_b32_e32 v108, 0
	v_mov_b32_e32 v109, 0
	v_mov_b32_e32 v110, 0
	v_mov_b32_e32 v111, 0
	v_mov_b32_e32 v112, 0
	v_mov_b32_e32 v113, 0
	v_mov_b32_e32 v114, 0
	v_mov_b32_e32 v115, 0
	v_mov_b32_e32 v116, 0
	v_mov_b32_e32 v117, 0
	v_mov_b32_e32 v118, 0
	v_mov_b32_e32 v119, 0
	v_mov_b32_e32 v120, 0
	v_mov_b32_e32 v121, 0
	v_mov_b32_e32 v122, 0
	v_mov_b32_e32 v123, 0
	v_mov_b32_e32 v124, 0
	v_mov_b32_e32 v125, 0
	v_mov_b32_e32 v126, 0
	v_mov_b32_e32 v127, 0
	v_mov_b32_e32 v128, 0
	v_mov_b32_e32 v129, 0
	v_mov_b32_e32 v130, 0
	v_mov_b32_e32 v131, 0
	v_mov_b32_e32 v132, 0
	v_mov_b32_e32 v133, 0
	v_mov_b32_e32 v134, 0
	v_mov_b32_e32 v135, 0
	v_mov_b32_e32 v136, 0
	v_mov_b32_e32 v137, 0
	v_mov_b32_e32 v138, 0
	v_mov_b32_e32 v139, 0
	v_mov_b32_e32 v140, 0
	v_mov_b32_e32 v141, 0
	v_mov_b32_e32 v142, 0
	v_mov_b32_e32 v143, 0
	v_mov_b32_e32 v144, 0
	v_mov_b32_e32 v145, 0
	v_mov_b32_e32 v146, 0
	v_mov_b32_e32 v147, 0
	v_mov_b32_e32 v148, 0
	v_mov_b32_e32 v149, 0
	v_mov_b32_e32 v150, 0
	v_mov_b32_e32 v151, 0
	v_mov_b32_e32 v152, 0
	v_mov_b32_e32 v153, 0
	v_mov_b32_e32 v154, 0
	v_mov_b32_e32 v155, 0
	v_mov_b32_e32 v156, 0
	v_mov_b32_e32 v157, 0
	v_mov_b32_e32 v158, 0
	v_mov_b32_e32 v159, 0
	v_mov_b32_e32 v160, 0
	v_mov_b32_e32 v161, 0
	s_branch .LBB0_1676

.LBB0_1689:
	s_andn2_b64 vcc, exec, s[42:43]
	s_cbranch_vccnz .LBB0_1700
	s_lshl_b32 s51, s52, 8
	v_add_u32_e32 v2, s51, v169
	v_add_u32_e32 v4, s51, v205
	s_bitset1_b32 s51, 7
	v_add_u32_e32 v6, s51, v169
	v_add_u32_e32 v8, s51, v205
	v_ashrrev_i32_e32 v3, 31, v2
	v_ashrrev_i32_e32 v5, 31, v4
	v_ashrrev_i32_e32 v7, 31, v6
	v_ashrrev_i32_e32 v9, 31, v8
	v_mov_b32_e32 v181, v167
	v_mov_b32_e32 v183, v167
	s_add_u32 s51, s64, 0x100
	v_lshl_add_u64 v[184:185], v[2:3], 2, s[30:31]
	v_lshl_add_u64 v[186:187], v[4:5], 2, s[30:31]
	v_lshl_add_u64 v[188:189], v[6:7], 2, s[30:31]
	v_lshl_add_u64 v[190:191], v[8:9], 2, s[30:31]
	s_addc_u32 s53, s65, 0
	s_and_b64 vcc, exec, s[62:63]
	s_cbranch_vccz .Lnolist_15
	global_load_dword v184, v[184:185], off
	global_load_dword v186, v[186:187], off
	global_load_dword v188, v[188:189], off
	global_load_dword v190, v[190:191], off
.Lnolist_15:
	v_lshl_add_u64 v[192:193], s[40:41], 0, v[182:183]
	v_lshl_add_u64 v[194:195], s[40:41], 0, v[180:181]
	s_mov_b32 s91, 0
	s_mov_b64 s[70:71], 0
.LBB0_1691:
	s_cmp_eq_u32 s88, s91
	s_cselect_b64 s[68:69], -1, 0
	s_and_b64 s[64:65], s[62:63], s[68:69]
	s_andn2_b64 vcc, exec, s[64:65]
	s_cbranch_vccnz .LBB0_1693
	v_readfirstlane_b32 s54, v1
	v_lshlrev_b32_e32 v2, 9, v184
	v_lshlrev_b32_e32 v3, 9, v186
	v_lshlrev_b32_e32 v4, 9, v188
	v_lshlrev_b32_e32 v5, 9, v190
	s_mul_hi_u32 s55, s54, 0x700000
	s_mul_i32 s54, s54, 0x700000
	s_add_u32 s54, s100, s54
	s_addc_u32 s55, s101, s55
	v_and_b32_e32 v2, 0x1fffe00, v2
	v_and_b32_e32 v3, 0x1fffe00, v3
	v_and_b32_e32 v4, 0x1fffe00, v4
	v_and_b32_e32 v5, 0x1fffe00, v5
	v_add_lshl_u32 v166, v2, v204, 1
	v_add_lshl_u32 v178, v3, v206, 1
	v_add_lshl_u32 v180, v4, v204, 1
	v_add_lshl_u32 v182, v5, v206, 1

.LBB0_1697:
	v_mov_b32_e32 v2, 0xbfb8aa3b
	v_mov_b32_e32 v3, 1.0
	v_mov_b32_e32 v4, 0x41000000
	v_lshl_add_u32 v251, s60, 8, v209
	v_lshl_or_b32 v250, s58, 7, v211
	v_mad_u32_u24 v249, v251, s33, v250
	v_mov_b32_e32 v8, 0
	v_mov_b32_e32 v9, 0
	v_mov_b32_e32 v10, 0
	v_mov_b32_e32 v11, 0
	v_pk_mul_f32 v[6:7], v[154:155], v[2:3] op_sel_hi:[1,0]
	v_pk_mul_f32 v[12:13], v[156:157], v[2:3] op_sel_hi:[1,0]
	v_pk_mul_f32 v[14:15], v[150:151], v[2:3] op_sel_hi:[1,0]
	v_exp_f32_e32 v6, v6
	v_pk_mul_f32 v[16:17], v[152:153], v[2:3] op_sel_hi:[1,0]
	v_exp_f32_e32 v12, v12
	v_pk_mul_f32 v[18:19], v[142:143], v[2:3] op_sel_hi:[1,0]
	v_exp_f32_e32 v14, v14
	v_pk_mul_f32 v[20:21], v[144:145], v[2:3] op_sel_hi:[1,0]
	v_exp_f32_e32 v16, v16
	v_pk_mul_f32 v[22:23], v[134:135], v[2:3] op_sel_hi:[1,0]
	v_exp_f32_e32 v7, v7
	v_pk_mul_f32 v[24:25], v[136:137], v[2:3] op_sel_hi:[1,0]
	v_exp_f32_e32 v13, v13
	v_pk_mul_f32 v[26:27], v[126:127], v[2:3] op_sel_hi:[1,0]
	v_exp_f32_e32 v15, v15
	v_pk_mul_f32 v[28:29], v[128:129], v[2:3] op_sel_hi:[1,0]
	v_exp_f32_e32 v17, v17
	v_pk_mul_f32 v[30:31], v[118:119], v[2:3] op_sel_hi:[1,0]
	v_exp_f32_e32 v18, v18
	v_pk_add_f32 v[6:7], v[6:7], v[2:3] op_sel:[0,1] op_sel_hi:[1,1]
	v_exp_f32_e32 v20, v20
	v_pk_add_f32 v[12:13], v[12:13], v[2:3] op_sel:[0,1] op_sel_hi:[1,1]
	v_exp_f32_e32 v22, v22
	v_pk_add_f32 v[14:15], v[14:15], v[2:3] op_sel:[0,1] op_sel_hi:[1,1]
	v_rcp_f32_e32 v6, v6
	v_pk_add_f32 v[16:17], v[16:17], v[2:3] op_sel:[0,1] op_sel_hi:[1,1]
	v_exp_f32_e32 v24, v24
	v_pk_mul_f32 v[32:33], v[120:121], v[2:3] op_sel_hi:[1,0]
	v_rcp_f32_e32 v12, v12
	v_pk_mul_f32 v[196:197], v[154:155], v[158:159]
	v_rcp_f32_e32 v14, v14
	v_pk_mul_f32 v[198:199], v[110:111], v[2:3] op_sel_hi:[1,0]
	v_exp_f32_e32 v19, v19
	v_pk_mul_f32 v[200:201], v[156:157], v[160:161]
	v_rcp_f32_e32 v16, v16
	v_pk_mul_f32 v[202:203], v[150:151], v[146:147]
	v_exp_f32_e32 v21, v21
	v_pk_mul_f32 v[214:215], v[112:113], v[2:3] op_sel_hi:[1,0]
	v_exp_f32_e32 v23, v23
	v_pk_mul_f32 v[216:217], v[102:103], v[2:3] op_sel_hi:[1,0]
	v_rcp_f32_e32 v7, v7
	v_pk_add_f32 v[18:19], v[18:19], v[2:3] op_sel:[0,1] op_sel_hi:[1,1]
	v_exp_f32_e32 v25, v25
	v_pk_mul_f32 v[218:219], v[152:153], v[148:149]
	v_exp_f32_e32 v26, v26
	v_pk_add_f32 v[20:21], v[20:21], v[2:3] op_sel:[0,1] op_sel_hi:[1,1]
	v_rcp_f32_e32 v13, v13
	v_pk_add_f32 v[22:23], v[22:23], v[2:3] op_sel:[0,1] op_sel_hi:[1,1]
	v_rcp_f32_e32 v15, v15
	v_pk_mul_f32 v[196:197], v[196:197], v[6:7]
	v_exp_f32_e32 v28, v28
	v_pk_add_f32 v[24:25], v[24:25], v[2:3] op_sel:[0,1] op_sel_hi:[1,1]
	v_exp_f32_e32 v30, v30
	v_pk_mul_f32 v[196:197], v[196:197], v[4:5] op_sel_hi:[1,0]
	v_rcp_f32_e32 v17, v17
	v_pk_mul_f32 v[200:201], v[200:201], v[12:13]
	v_rcp_f32_e32 v18, v18
	v_pk_mul_f32 v[202:203], v[202:203], v[14:15]
	v_exp_f32_e32 v32, v32
	v_med3_f32 v196, v196, s87, v227
	v_rcp_f32_e32 v20, v20
	v_pk_mul_f32 v[200:201], v[200:201], v[4:5] op_sel_hi:[1,0]
	v_rcp_f32_e32 v22, v22
	v_pk_mul_f32 v[202:203], v[202:203], v[4:5] op_sel_hi:[1,0]
	v_exp_f32_e32 v27, v27
	v_pk_mul_f32 v[218:219], v[218:219], v[16:17]
	v_rcp_f32_e32 v24, v24
	v_med3_f32 v197, v197, s87, v227
	v_exp_f32_e32 v29, v29
	v_med3_f32 v200, v200, s87, v227
	v_exp_f32_e32 v31, v31
	v_med3_f32 v202, v202, s87, v227
	v_rcp_f32_e32 v19, v19
	v_pk_mul_f32 v[218:219], v[218:219], v[4:5] op_sel_hi:[1,0]
	v_exp_f32_e32 v33, v33
	v_pk_add_f32 v[26:27], v[26:27], v[2:3] op_sel:[0,1] op_sel_hi:[1,1]
	v_exp_f32_e32 v198, v198
	v_pk_mul_f32 v[6:7], v[104:105], v[2:3] op_sel_hi:[1,0]
	v_rcp_f32_e32 v21, v21
	v_cvt_pk_fp8_f32 v12, v196, v197
	v_rcp_f32_e32 v23, v23
	v_med3_f32 v201, v201, s87, v227
	v_exp_f32_e32 v214, v214
	v_med3_f32 v203, v203, s87, v227
	v_exp_f32_e32 v216, v216
	v_med3_f32 v218, v218, s87, v227
	v_rcp_f32_e32 v25, v25
	v_pk_add_f32 v[28:29], v[28:29], v[2:3] op_sel:[0,1] op_sel_hi:[1,1]
	v_rcp_f32_e32 v26, v26
	v_pk_add_f32 v[30:31], v[30:31], v[2:3] op_sel:[0,1] op_sel_hi:[1,1]
	v_exp_f32_e32 v6, v6
	v_cvt_pk_fp8_f32 v12, v200, v201 op_sel:[0,0,1]
	v_cvt_pk_fp8_f32 v13, v202, v203
	v_med3_f32 v219, v219, s87, v227
	v_rcp_f32_e32 v28, v28
	v_pk_add_f32 v[32:33], v[32:33], v[2:3] op_sel:[0,1] op_sel_hi:[1,1]
	v_rcp_f32_e32 v30, v30
	v_pk_mul_f32 v[14:15], v[142:143], v[138:139]
	v_exp_f32_e32 v199, v199
	v_cvt_pk_fp8_f32 v13, v218, v219 op_sel:[0,0,1]
	v_pk_mul_f32 v[14:15], v[14:15], v[18:19]
	v_rcp_f32_e32 v32, v32
	v_pk_mul_f32 v[16:17], v[94:95], v[2:3] op_sel_hi:[1,0]
	v_pk_mul_f32 v[14:15], v[14:15], v[4:5] op_sel_hi:[1,0]
	v_exp_f32_e32 v215, v215
	v_pk_mul_f32 v[18:19], v[144:145], v[140:141]
	v_exp_f32_e32 v217, v217
	v_med3_f32 v14, v14, s87, v227
	v_pk_mul_f32 v[18:19], v[18:19], v[20:21]
	v_pk_mul_f32 v[20:21], v[134:135], v[130:131]
	v_rcp_f32_e32 v27, v27
	v_pk_mul_f32 v[18:19], v[18:19], v[4:5] op_sel_hi:[1,0]
	v_pk_mul_f32 v[20:21], v[20:21], v[22:23]
	global_store_dwordx2 v249, v[12:13], s[36:37]
	v_exp_f32_e32 v7, v7
	v_pk_mul_f32 v[20:21], v[20:21], v[4:5] op_sel_hi:[1,0]
	v_exp_f32_e32 v16, v16
	v_pk_mul_f32 v[12:13], v[96:97], v[2:3] op_sel_hi:[1,0]
	v_pk_mul_f32 v[22:23], v[86:87], v[2:3] op_sel_hi:[1,0]
	v_med3_f32 v15, v15, s87, v227
	v_med3_f32 v18, v18, s87, v227
	v_med3_f32 v20, v20, s87, v227
	v_pk_mul_f32 v[196:197], v[136:137], v[132:133]
	v_rcp_f32_e32 v29, v29
	v_pk_add_f32 v[198:199], v[198:199], v[2:3] op_sel:[0,1] op_sel_hi:[1,1]
	v_pk_mul_f32 v[196:197], v[196:197], v[24:25]
	v_rcp_f32_e32 v31, v31
	v_pk_mul_f32 v[24:25], v[88:89], v[2:3] op_sel_hi:[1,0]
	v_pk_mul_f32 v[196:197], v[196:197], v[4:5] op_sel_hi:[1,0]
	v_exp_f32_e32 v12, v12
	v_cvt_pk_fp8_f32 v14, v14, v15
	v_exp_f32_e32 v22, v22
	v_med3_f32 v19, v19, s87, v227
	v_med3_f32 v21, v21, s87, v227
	v_med3_f32 v196, v196, s87, v227
	v_rcp_f32_e32 v33, v33
	v_pk_add_f32 v[214:215], v[214:215], v[2:3] op_sel:[0,1] op_sel_hi:[1,1]
	v_rcp_f32_e32 v198, v198
	v_pk_add_f32 v[216:217], v[216:217], v[2:3] op_sel:[0,1] op_sel_hi:[1,1]
	v_exp_f32_e32 v24, v24
	v_cvt_pk_fp8_f32 v14, v18, v19 op_sel:[0,0,1]
	v_cvt_pk_fp8_f32 v15, v20, v21
	v_med3_f32 v197, v197, s87, v227
	v_rcp_f32_e32 v214, v214
	v_pk_add_f32 v[6:7], v[6:7], v[2:3] op_sel:[0,1] op_sel_hi:[1,1]
	v_rcp_f32_e32 v216, v216
	v_pk_mul_f32 v[18:19], v[126:127], v[122:123]
	v_exp_f32_e32 v17, v17
	v_cvt_pk_fp8_f32 v15, v196, v197 op_sel:[0,0,1]
	v_pk_mul_f32 v[18:19], v[18:19], v[26:27]
	v_rcp_f32_e32 v6, v6
	v_pk_mul_f32 v[20:21], v[78:79], v[2:3] op_sel_hi:[1,0]
	v_pk_mul_f32 v[18:19], v[18:19], v[4:5] op_sel_hi:[1,0]
	v_exp_f32_e32 v13, v13
	v_pk_mul_f32 v[26:27], v[128:129], v[124:125]
	v_exp_f32_e32 v23, v23
	v_med3_f32 v18, v18, s87, v227
	v_pk_mul_f32 v[26:27], v[26:27], v[28:29]
	v_pk_mul_f32 v[28:29], v[118:119], v[114:115]
	v_rcp_f32_e32 v199, v199
	v_pk_mul_f32 v[26:27], v[26:27], v[4:5] op_sel_hi:[1,0]
	v_pk_mul_f32 v[28:29], v[28:29], v[30:31]
	v_exp_f32_e32 v25, v25
	v_pk_mul_f32 v[30:31], v[80:81], v[2:3] op_sel_hi:[1,0]
	v_pk_mul_f32 v[28:29], v[28:29], v[4:5] op_sel_hi:[1,0]
	v_exp_f32_e32 v20, v20
	v_pk_mul_f32 v[196:197], v[70:71], v[2:3] op_sel_hi:[1,0]
	v_med3_f32 v19, v19, s87, v227
	v_med3_f32 v26, v26, s87, v227
	v_med3_f32 v28, v28, s87, v227
	v_pk_mul_f32 v[200:201], v[120:121], v[116:117]
	v_rcp_f32_e32 v215, v215
	v_pk_add_f32 v[16:17], v[16:17], v[2:3] op_sel:[0,1] op_sel_hi:[1,1]
	v_pk_mul_f32 v[200:201], v[200:201], v[32:33]
	v_rcp_f32_e32 v217, v217
	v_pk_mul_f32 v[32:33], v[72:73], v[2:3] op_sel_hi:[1,0]
	v_pk_mul_f32 v[200:201], v[200:201], v[4:5] op_sel_hi:[1,0]
	v_exp_f32_e32 v30, v30
	v_cvt_pk_fp8_f32 v18, v18, v19
	v_exp_f32_e32 v196, v196
	v_med3_f32 v27, v27, s87, v227
	v_med3_f32 v29, v29, s87, v227
	v_med3_f32 v200, v200, s87, v227
	v_rcp_f32_e32 v7, v7
	v_pk_add_f32 v[12:13], v[12:13], v[2:3] op_sel:[0,1] op_sel_hi:[1,1]
	v_rcp_f32_e32 v16, v16
	v_pk_add_f32 v[22:23], v[22:23], v[2:3] op_sel:[0,1] op_sel_hi:[1,1]
	v_exp_f32_e32 v32, v32
	v_cvt_pk_fp8_f32 v18, v26, v27 op_sel:[0,0,1]
	v_cvt_pk_fp8_f32 v19, v28, v29
	v_med3_f32 v201, v201, s87, v227
	v_rcp_f32_e32 v12, v12
	v_pk_add_f32 v[24:25], v[24:25], v[2:3] op_sel:[0,1] op_sel_hi:[1,1]
	v_rcp_f32_e32 v22, v22
	v_pk_mul_f32 v[26:27], v[110:111], v[106:107]
	v_exp_f32_e32 v21, v21
	v_cvt_pk_fp8_f32 v19, v200, v201 op_sel:[0,0,1]
	v_pk_mul_f32 v[26:27], v[26:27], v[198:199]
	v_rcp_f32_e32 v24, v24
	v_pk_mul_f32 v[28:29], v[62:63], v[2:3] op_sel_hi:[1,0]
	v_pk_mul_f32 v[26:27], v[26:27], v[4:5] op_sel_hi:[1,0]
	v_exp_f32_e32 v31, v31
	v_pk_mul_f32 v[198:199], v[112:113], v[108:109]
	v_exp_f32_e32 v197, v197
	v_med3_f32 v26, v26, s87, v227
	v_pk_mul_f32 v[198:199], v[198:199], v[214:215]
	v_pk_mul_f32 v[200:201], v[102:103], v[98:99]
	v_rcp_f32_e32 v17, v17
	v_pk_mul_f32 v[198:199], v[198:199], v[4:5] op_sel_hi:[1,0]
	v_pk_mul_f32 v[200:201], v[200:201], v[216:217]
	v_exp_f32_e32 v33, v33
	v_pk_mul_f32 v[202:203], v[64:65], v[2:3] op_sel_hi:[1,0]
	v_pk_mul_f32 v[200:201], v[200:201], v[4:5] op_sel_hi:[1,0]
	v_exp_f32_e32 v28, v28
	v_pk_mul_f32 v[214:215], v[54:55], v[2:3] op_sel_hi:[1,0]
	v_med3_f32 v27, v27, s87, v227
	v_med3_f32 v198, v198, s87, v227
	v_med3_f32 v200, v200, s87, v227
	v_pk_mul_f32 v[216:217], v[104:105], v[100:101]
	v_rcp_f32_e32 v13, v13
	v_pk_add_f32 v[20:21], v[20:21], v[2:3] op_sel:[0,1] op_sel_hi:[1,1]
	v_pk_mul_f32 v[216:217], v[216:217], v[6:7]
	v_rcp_f32_e32 v23, v23
	v_add_u32_e32 v6, 0xe000, v249
	v_pk_mul_f32 v[216:217], v[216:217], v[4:5] op_sel_hi:[1,0]
	v_exp_f32_e32 v202, v202
	global_store_dwordx2 v6, v[14:15], s[36:37]
	v_exp_f32_e32 v214, v214
	v_pk_mul_f32 v[6:7], v[56:57], v[2:3] op_sel_hi:[1,0]
	v_cvt_pk_fp8_f32 v14, v26, v27
	v_med3_f32 v199, v199, s87, v227
	v_med3_f32 v201, v201, s87, v227
	v_med3_f32 v216, v216, s87, v227
	v_rcp_f32_e32 v25, v25
	v_pk_add_f32 v[30:31], v[30:31], v[2:3] op_sel:[0,1] op_sel_hi:[1,1]
	v_rcp_f32_e32 v20, v20
	v_pk_add_f32 v[196:197], v[196:197], v[2:3] op_sel:[0,1] op_sel_hi:[1,1]
	v_exp_f32_e32 v6, v6
	v_cvt_pk_fp8_f32 v14, v198, v199 op_sel:[0,0,1]
	v_cvt_pk_fp8_f32 v15, v200, v201
	v_med3_f32 v217, v217, s87, v227
	v_rcp_f32_e32 v30, v30
	v_pk_add_f32 v[32:33], v[32:33], v[2:3] op_sel:[0,1] op_sel_hi:[1,1]
	v_rcp_f32_e32 v196, v196
	v_pk_mul_f32 v[26:27], v[94:95], v[90:91]
	v_exp_f32_e32 v29, v29
	v_cvt_pk_fp8_f32 v15, v216, v217 op_sel:[0,0,1]
	v_pk_mul_f32 v[26:27], v[26:27], v[16:17]
	v_rcp_f32_e32 v32, v32
	v_pk_mul_f32 v[16:17], v[46:47], v[2:3] op_sel_hi:[1,0]
	v_pk_mul_f32 v[26:27], v[26:27], v[4:5] op_sel_hi:[1,0]
	v_exp_f32_e32 v203, v203
	v_pk_mul_f32 v[198:199], v[96:97], v[92:93]
	v_exp_f32_e32 v215, v215
	v_med3_f32 v26, v26, s87, v227
	v_pk_mul_f32 v[198:199], v[198:199], v[12:13]
	v_pk_mul_f32 v[12:13], v[86:87], v[82:83]
	v_rcp_f32_e32 v21, v21
	v_pk_mul_f32 v[198:199], v[198:199], v[4:5] op_sel_hi:[1,0]
	v_pk_mul_f32 v[12:13], v[12:13], v[22:23]
	v_exp_f32_e32 v7, v7
	v_pk_mul_f32 v[22:23], v[48:49], v[2:3] op_sel_hi:[1,0]
	v_pk_mul_f32 v[12:13], v[12:13], v[4:5] op_sel_hi:[1,0]
	v_exp_f32_e32 v16, v16
	v_pk_mul_f32 v[200:201], v[38:39], v[2:3] op_sel_hi:[1,0]
	v_med3_f32 v27, v27, s87, v227
	v_med3_f32 v198, v198, s87, v227
	v_med3_f32 v12, v12, s87, v227
	v_pk_mul_f32 v[216:217], v[88:89], v[84:85]
	v_rcp_f32_e32 v31, v31
	v_pk_add_f32 v[28:29], v[28:29], v[2:3] op_sel:[0,1] op_sel_hi:[1,1]
	v_pk_mul_f32 v[216:217], v[216:217], v[24:25]
	v_rcp_f32_e32 v197, v197
	v_add_u32_e32 v24, 0x1c000, v249
	v_pk_mul_f32 v[216:217], v[216:217], v[4:5] op_sel_hi:[1,0]
	v_exp_f32_e32 v22, v22
	global_store_dwordx2 v24, v[18:19], s[36:37]
	v_exp_f32_e32 v200, v200
	v_pk_mul_f32 v[18:19], v[40:41], v[2:3] op_sel_hi:[1,0]
	v_cvt_pk_fp8_f32 v24, v26, v27
	v_med3_f32 v199, v199, s87, v227
	v_med3_f32 v13, v13, s87, v227
	v_med3_f32 v216, v216, s87, v227
	v_rcp_f32_e32 v33, v33
	v_pk_add_f32 v[202:203], v[202:203], v[2:3] op_sel:[0,1] op_sel_hi:[1,1]
	v_rcp_f32_e32 v28, v28
	v_pk_add_f32 v[214:215], v[214:215], v[2:3] op_sel:[0,1] op_sel_hi:[1,1]
	v_exp_f32_e32 v18, v18
	v_cvt_pk_fp8_f32 v24, v198, v199 op_sel:[0,0,1]
	v_cvt_pk_fp8_f32 v25, v12, v13
	v_med3_f32 v217, v217, s87, v227
	v_rcp_f32_e32 v202, v202
	v_pk_add_f32 v[6:7], v[6:7], v[2:3] op_sel:[0,1] op_sel_hi:[1,1]
	v_rcp_f32_e32 v214, v214
	v_pk_mul_f32 v[12:13], v[78:79], v[74:75]
	v_exp_f32_e32 v17, v17
	v_cvt_pk_fp8_f32 v25, v216, v217 op_sel:[0,0,1]
	v_pk_mul_f32 v[12:13], v[12:13], v[20:21]
	v_rcp_f32_e32 v6, v6
	v_pk_mul_f32 v[20:21], v[80:81], v[76:77]
	v_pk_mul_f32 v[12:13], v[12:13], v[4:5] op_sel_hi:[1,0]
	v_exp_f32_e32 v23, v23
	v_pk_mul_f32 v[20:21], v[20:21], v[30:31]
	v_exp_f32_e32 v201, v201
	v_med3_f32 v12, v12, s87, v227
	v_pk_mul_f32 v[20:21], v[20:21], v[4:5] op_sel_hi:[1,0]
	v_pk_mul_f32 v[26:27], v[70:71], v[66:67]
	v_rcp_f32_e32 v29, v29
	v_med3_f32 v13, v13, s87, v227
	v_pk_mul_f32 v[26:27], v[26:27], v[196:197]
	v_exp_f32_e32 v19, v19
	v_med3_f32 v20, v20, s87, v227
	v_pk_mul_f32 v[26:27], v[26:27], v[4:5] op_sel_hi:[1,0]
	v_pk_mul_f32 v[30:31], v[72:73], v[68:69]
	v_rcp_f32_e32 v203, v203
	v_med3_f32 v26, v26, s87, v227
	v_pk_mul_f32 v[30:31], v[30:31], v[32:33]
	v_rcp_f32_e32 v215, v215
	v_pk_add_f32 v[16:17], v[16:17], v[2:3] op_sel:[0,1] op_sel_hi:[1,1]
	v_pk_mul_f32 v[30:31], v[30:31], v[4:5] op_sel_hi:[1,0]
	v_add_u32_e32 v32, 0x2a000, v249
	v_cvt_pk_fp8_f32 v12, v12, v13
	v_med3_f32 v21, v21, s87, v227
	global_store_dwordx2 v32, v[14:15], s[36:37]
	v_med3_f32 v27, v27, s87, v227
	v_med3_f32 v30, v30, s87, v227
	v_rcp_f32_e32 v7, v7
	v_pk_add_f32 v[22:23], v[22:23], v[2:3] op_sel:[0,1] op_sel_hi:[1,1]
	v_rcp_f32_e32 v16, v16
	v_pk_add_f32 v[200:201], v[200:201], v[2:3] op_sel:[0,1] op_sel_hi:[1,1]
	v_cvt_pk_fp8_f32 v12, v20, v21 op_sel:[0,0,1]
	v_cvt_pk_fp8_f32 v13, v26, v27
	v_med3_f32 v31, v31, s87, v227
	v_rcp_f32_e32 v22, v22
	v_pk_add_f32 v[18:19], v[18:19], v[2:3] op_sel:[0,1] op_sel_hi:[1,1]
	v_rcp_f32_e32 v200, v200
	v_pk_mul_f32 v[14:15], v[62:63], v[58:59]
	v_cvt_pk_fp8_f32 v13, v30, v31 op_sel:[0,0,1]
	v_rcp_f32_e32 v18, v18
	v_pk_mul_f32 v[14:15], v[14:15], v[28:29]
	v_pk_mul_f32 v[20:21], v[64:65], v[60:61]
	v_pk_mul_f32 v[26:27], v[54:55], v[50:51]
	v_pk_mul_f32 v[14:15], v[14:15], v[4:5] op_sel_hi:[1,0]
	v_pk_mul_f32 v[20:21], v[20:21], v[202:203]
	v_pk_mul_f32 v[26:27], v[26:27], v[214:215]
	v_med3_f32 v14, v14, s87, v227
	v_pk_mul_f32 v[20:21], v[20:21], v[4:5] op_sel_hi:[1,0]
	v_pk_mul_f32 v[26:27], v[26:27], v[4:5] op_sel_hi:[1,0]
	v_rcp_f32_e32 v17, v17
	v_med3_f32 v15, v15, s87, v227
	v_med3_f32 v20, v20, s87, v227
	v_med3_f32 v26, v26, s87, v227
	v_pk_mul_f32 v[28:29], v[56:57], v[52:53]
	v_rcp_f32_e32 v23, v23
	v_add_u32_e32 v30, 0x70000, v249
	v_pk_mul_f32 v[28:29], v[28:29], v[6:7]
	v_rcp_f32_e32 v201, v201
	global_store_dwordx2 v30, v[24:25], s[36:37]
	v_pk_mul_f32 v[28:29], v[28:29], v[4:5] op_sel_hi:[1,0]
	v_cvt_pk_fp8_f32 v6, v14, v15
	v_med3_f32 v21, v21, s87, v227
	v_med3_f32 v27, v27, s87, v227
	v_med3_f32 v28, v28, s87, v227
	v_rcp_f32_e32 v19, v19
	v_cvt_pk_fp8_f32 v6, v20, v21 op_sel:[0,0,1]
	v_cvt_pk_fp8_f32 v7, v26, v27
	v_med3_f32 v29, v29, s87, v227
	v_pk_mul_f32 v[14:15], v[46:47], v[42:43]
	v_pk_mul_f32 v[20:21], v[48:49], v[44:45]
	v_cvt_pk_fp8_f32 v7, v28, v29 op_sel:[0,0,1]
	v_pk_mul_f32 v[14:15], v[14:15], v[16:17]
	v_pk_mul_f32 v[20:21], v[20:21], v[22:23]
	v_pk_mul_f32 v[16:17], v[38:39], v[34:35]
	v_pk_mul_f32 v[14:15], v[14:15], v[4:5] op_sel_hi:[1,0]
	v_pk_mul_f32 v[20:21], v[20:21], v[4:5] op_sel_hi:[1,0]
	v_pk_mul_f32 v[16:17], v[16:17], v[200:201]
	v_med3_f32 v14, v14, s87, v227
	v_med3_f32 v20, v20, s87, v227
	v_pk_mul_f32 v[16:17], v[16:17], v[4:5] op_sel_hi:[1,0]
	v_med3_f32 v15, v15, s87, v227
	v_pk_mul_f32 v[22:23], v[40:41], v[36:37]
	v_med3_f32 v16, v16, s87, v227
	v_add_u32_e32 v24, 0x7e000, v249
	v_pk_mul_f32 v[22:23], v[22:23], v[18:19]
	v_cvt_pk_fp8_f32 v14, v14, v15
	global_store_dwordx2 v24, v[12:13], s[36:37]
	v_pk_mul_f32 v[22:23], v[22:23], v[4:5] op_sel_hi:[1,0]
	v_med3_f32 v21, v21, s87, v227
	v_med3_f32 v17, v17, s87, v227
	v_med3_f32 v22, v22, s87, v227
	v_cvt_pk_fp8_f32 v14, v20, v21 op_sel:[0,0,1]
	v_cvt_pk_fp8_f32 v15, v16, v17
	v_med3_f32 v23, v23, s87, v227
	v_add_u32_e32 v12, 0x8c000, v249
	v_add_u32_e32 v13, 0x9a000, v249
	v_cvt_pk_fp8_f32 v15, v22, v23 op_sel:[0,0,1]
	global_store_dwordx2 v12, v[6:7], s[36:37]
	v_mfma_f32_32x32x16_bf16 v[34:49], v[8:11], v[8:11], 0
	global_store_dwordx2 v13, v[14:15], s[36:37]
	v_mfma_f32_32x32x16_bf16 v[50:65], v[8:11], v[8:11], 0
	v_mfma_f32_32x32x16_bf16 v[66:81], v[8:11], v[8:11], 0
	v_mfma_f32_32x32x16_bf16 v[82:97], v[8:11], v[8:11], 0
	v_mfma_f32_32x32x16_bf16 v[98:113], v[8:11], v[8:11], 0
	v_mfma_f32_32x32x16_bf16 v[114:129], v[8:11], v[8:11], 0
	v_mfma_f32_32x32x16_bf16 v[130:145], v[8:11], v[8:11], 0
	v_mfma_f32_32x32x16_bf16 v[146:161], v[8:11], v[8:11], 0
	s_nop 15
	s_and_b64 vcc, exec, s[38:39]
	s_mov_b64 s[38:39], -1
	s_cbranch_vccnz .LBB0_1675
	s_andn2_b64 vcc, exec, s[34:35]
	s_cbranch_vccnz .LBB0_1674
	s_barrier
	s_branch .LBB0_1674

.LBB0_1816:
	v_bfe_u32 v8, v6, 4, 2
	s_add_u32 s36, s38, 0x24f00000
	v_and_b32_e32 v7, 15, v6
	v_lshlrev_b32_e32 v9, 4, v8
	v_lshlrev_b32_e32 v6, 2, v6
	s_addc_u32 s37, s39, 0
	v_lshl_or_b32 v209, s40, 6, v7
	v_lshl_or_b32 v7, v7, 6, v9
	s_lshl_b32 s40, s40, 13
	v_and_b32_e32 v6, 32, v6
	v_bitop3_b32 v9, v7, s40, v6 bitop3:0xde
	s_lshl_b32 s40, s41, 5
	s_and_b32 s47, s40, 0x60
	s_add_i32 m0, s59, 0x18000
	v_lshl_add_u64 v[2:3], v[2:3], 0, s[56:57]
	s_lshl_b32 s40, s47, 7
	s_waitcnt vmcnt(2)
	s_barrier
	global_load_lds_dwordx4 v[2:3], off
	s_add_i32 m0, s59, 0x1a000
	s_add_u32 s38, s38, 0xe800080
	v_lshl_add_u64 v[2:3], v[4:5], 0, s[56:57]
	s_addc_u32 s39, s39, 0
	s_add_i32 s74, s59, 0x8000
	s_add_i32 s75, s59, 0xa000
	v_mov_b32_e32 v179, v167
	v_bitop3_b32 v210, v7, s40, v6 bitop3:0xde
	global_load_lds_dwordx4 v[2:3], off
	v_lshl_add_u64 v[2:3], s[38:39], 0, v[166:167]
	s_mov_b32 m0, s74
	s_add_u32 s40, s60, 0x20080
	global_load_lds_dwordx4 v[2:3], off
	v_lshl_add_u64 v[2:3], s[38:39], 0, v[178:179]
	s_mov_b32 m0, s75
	s_addc_u32 s41, s61, 0
	global_load_lds_dwordx4 v[2:3], off
	s_add_i32 m0, s59, 0x1c000
	v_lshl_add_u64 v[2:3], s[40:41], 0, v[162:163]
	global_load_lds_dwordx4 v[2:3], off
	v_lshl_add_u64 v[2:3], s[40:41], 0, v[164:165]
	s_add_i32 m0, s59, 0x1e000
	s_cmp_gt_i32 s11, 0
	global_load_lds_dwordx4 v[2:3], off
	s_cselect_b64 s[40:41], -1, 0
	s_add_i32 s77, s11, -2
	s_cmpk_lt_u32 s42, 0x100
	s_cselect_b64 s[42:43], -1, 0
	s_cmp_ge_i32 s0, s46
	s_waitcnt vmcnt(6)
	s_cselect_b64 s[44:45], -1, 0
	s_ashr_i32 s79, s1, 31
	s_mul_i32 s49, s10, s1
	s_sub_i32 s84, s1, s46
	s_sub_i32 s46, s0, s46
	s_mul_hi_i32 s48, s10, s1
	s_add_u32 s88, s49, s46
	s_mov_b32 s76, 0
	s_addc_u32 s90, s48, 0
	v_lshl_or_b32 v211, v8, 3, s47
	v_add_u32_e32 v212, 0, v9
	s_barrier
	v_mov_b32_e32 v34, 0
	v_mov_b32_e32 v35, 0
	v_mov_b32_e32 v36, 0
	v_mov_b32_e32 v37, 0
	v_mov_b32_e32 v38, 0
	v_mov_b32_e32 v39, 0
	v_mov_b32_e32 v40, 0
	v_mov_b32_e32 v41, 0
	v_mov_b32_e32 v42, 0
	v_mov_b32_e32 v43, 0
	v_mov_b32_e32 v44, 0
	v_mov_b32_e32 v45, 0
	v_mov_b32_e32 v46, 0
	v_mov_b32_e32 v47, 0
	v_mov_b32_e32 v48, 0
	v_mov_b32_e32 v49, 0
	v_mov_b32_e32 v50, 0
	v_mov_b32_e32 v51, 0
	v_mov_b32_e32 v52, 0
	v_mov_b32_e32 v53, 0
	v_mov_b32_e32 v54, 0
	v_mov_b32_e32 v55, 0
	v_mov_b32_e32 v56, 0
	v_mov_b32_e32 v57, 0
	v_mov_b32_e32 v58, 0
	v_mov_b32_e32 v59, 0
	v_mov_b32_e32 v60, 0
	v_mov_b32_e32 v61, 0
	v_mov_b32_e32 v62, 0
	v_mov_b32_e32 v63, 0
	v_mov_b32_e32 v64, 0
	v_mov_b32_e32 v65, 0
	v_mov_b32_e32 v66, 0
	v_mov_b32_e32 v67, 0
	v_mov_b32_e32 v68, 0
	v_mov_b32_e32 v69, 0
	v_mov_b32_e32 v70, 0
	v_mov_b32_e32 v71, 0
	v_mov_b32_e32 v72, 0
	v_mov_b32_e32 v73, 0
	v_mov_b32_e32 v74, 0
	v_mov_b32_e32 v75, 0
	v_mov_b32_e32 v76, 0
	v_mov_b32_e32 v77, 0
	v_mov_b32_e32 v78, 0
	v_mov_b32_e32 v79, 0
	v_mov_b32_e32 v80, 0
	v_mov_b32_e32 v81, 0
	v_mov_b32_e32 v82, 0
	v_mov_b32_e32 v83, 0
	v_mov_b32_e32 v84, 0
	v_mov_b32_e32 v85, 0
	v_mov_b32_e32 v86, 0
	v_mov_b32_e32 v87, 0
	v_mov_b32_e32 v88, 0
	v_mov_b32_e32 v89, 0
	v_mov_b32_e32 v90, 0
	v_mov_b32_e32 v91, 0
	v_mov_b32_e32 v92, 0
	v_mov_b32_e32 v93, 0
	v_mov_b32_e32 v94, 0
	v_mov_b32_e32 v95, 0
	v_mov_b32_e32 v96, 0
	v_mov_b32_e32 v97, 0
	v_mov_b32_e32 v98, 0
	v_mov_b32_e32 v99, 0
	v_mov_b32_e32 v100, 0
	v_mov_b32_e32 v101, 0
	v_mov_b32_e32 v102, 0
	v_mov_b32_e32 v103, 0
	v_mov_b32_e32 v104, 0
	v_mov_b32_e32 v105, 0
	v_mov_b32_e32 v106, 0
	v_mov_b32_e32 v107, 0
	v_mov_b32_e32 v108, 0
	v_mov_b32_e32 v109, 0
	v_mov_b32_e32 v110, 0
	v_mov_b32_e32 v111, 0
	v_mov_b32_e32 v112, 0
	v_mov_b32_e32 v113, 0
	v_mov_b32_e32 v114, 0
	v_mov_b32_e32 v115, 0
	v_mov_b32_e32 v116, 0
	v_mov_b32_e32 v117, 0
	v_mov_b32_e32 v118, 0
	v_mov_b32_e32 v119, 0
	v_mov_b32_e32 v120, 0
	v_mov_b32_e32 v121, 0
	v_mov_b32_e32 v122, 0
	v_mov_b32_e32 v123, 0
	v_mov_b32_e32 v124, 0
	v_mov_b32_e32 v125, 0
	v_mov_b32_e32 v126, 0
	v_mov_b32_e32 v127, 0
	v_mov_b32_e32 v128, 0
	v_mov_b32_e32 v129, 0
	v_mov_b32_e32 v130, 0
	v_mov_b32_e32 v131, 0
	v_mov_b32_e32 v132, 0
	v_mov_b32_e32 v133, 0
	v_mov_b32_e32 v134, 0
	v_mov_b32_e32 v135, 0
	v_mov_b32_e32 v136, 0
	v_mov_b32_e32 v137, 0
	v_mov_b32_e32 v138, 0
	v_mov_b32_e32 v139, 0
	v_mov_b32_e32 v140, 0
	v_mov_b32_e32 v141, 0
	v_mov_b32_e32 v142, 0
	v_mov_b32_e32 v143, 0
	v_mov_b32_e32 v144, 0
	v_mov_b32_e32 v145, 0
	v_mov_b32_e32 v146, 0
	v_mov_b32_e32 v147, 0
	v_mov_b32_e32 v148, 0
	v_mov_b32_e32 v149, 0
	v_mov_b32_e32 v150, 0
	v_mov_b32_e32 v151, 0
	v_mov_b32_e32 v152, 0
	v_mov_b32_e32 v153, 0
	v_mov_b32_e32 v154, 0
	v_mov_b32_e32 v155, 0
	v_mov_b32_e32 v156, 0
	v_mov_b32_e32 v157, 0
	v_mov_b32_e32 v158, 0
	v_mov_b32_e32 v159, 0
	v_mov_b32_e32 v160, 0
	v_mov_b32_e32 v161, 0
	s_branch .LBB0_1819

.LBB0_1834:
	s_andn2_b64 vcc, exec, s[40:41]
	s_cbranch_vccnz .LBB0_1840
	s_lshl_b32 s47, s48, 8
	v_add_u32_e32 v2, s47, v169
	v_add_u32_e32 v4, s47, v205
	s_bitset1_b32 s47, 7
	v_add_u32_e32 v6, s47, v169
	v_add_u32_e32 v8, s47, v205
	v_ashrrev_i32_e32 v3, 31, v2
	v_ashrrev_i32_e32 v5, 31, v4
	v_ashrrev_i32_e32 v7, 31, v6
	v_ashrrev_i32_e32 v9, 31, v8
	v_mov_b32_e32 v181, v167
	v_mov_b32_e32 v183, v167
	s_add_u32 s47, s60, 0x100
	v_lshl_add_u64 v[184:185], v[2:3], 2, s[28:29]
	v_lshl_add_u64 v[186:187], v[4:5], 2, s[28:29]
	v_lshl_add_u64 v[188:189], v[6:7], 2, s[28:29]
	v_lshl_add_u64 v[190:191], v[8:9], 2, s[28:29]
	s_addc_u32 s49, s61, 0
	s_and_b64 vcc, exec, s[50:51]
	s_cbranch_vccz .Lnolist_17
	global_load_dword v184, v[184:185], off
	global_load_dword v186, v[186:187], off
	global_load_dword v188, v[188:189], off
	global_load_dword v190, v[190:191], off
.Lnolist_17:
	v_lshl_add_u64 v[192:193], s[38:39], 0, v[182:183]
	v_lshl_add_u64 v[194:195], s[38:39], 0, v[180:181]
	s_mov_b32 s55, 0
	s_mov_b64 s[64:65], 0
.LBB0_1836:
	s_cmp_eq_u32 s77, s55
	s_cselect_b64 s[62:63], -1, 0
	s_and_b64 s[60:61], s[50:51], s[62:63]
	s_andn2_b64 vcc, exec, s[60:61]
	s_cbranch_vccnz .LBB0_1838
	v_readfirstlane_b32 s52, v1
	v_lshlrev_b32_e32 v2, 9, v184
	v_lshlrev_b32_e32 v3, 9, v186
	v_lshlrev_b32_e32 v4, 9, v188
	v_lshlrev_b32_e32 v5, 9, v190
	s_mul_hi_u32 s53, s52, 0x700000
	s_mul_i32 s52, s52, 0x700000
	s_add_u32 s52, s100, s52
	s_addc_u32 s53, s101, s53
	v_and_b32_e32 v2, 0x1fffe00, v2
	v_and_b32_e32 v3, 0x1fffe00, v3
	v_and_b32_e32 v4, 0x1fffe00, v4
	v_and_b32_e32 v5, 0x1fffe00, v5
	v_add_lshl_u32 v166, v2, v204, 1
	v_add_lshl_u32 v178, v3, v206, 1
	v_add_lshl_u32 v180, v4, v204, 1
	v_add_lshl_u32 v182, v5, v206, 1

.LBB0_1843:
	v_mov_b32_e32 v2, 0xbfb8aa3b
	v_mov_b32_e32 v3, 1.0
	v_mov_b32_e32 v4, 0x41000000
	v_lshl_add_u32 v251, s58, 8, v209
	v_lshl_or_b32 v250, s54, 7, v211
	v_mad_u32_u24 v249, v251, s33, v250
	v_mov_b32_e32 v8, 0
	v_mov_b32_e32 v9, 0
	v_mov_b32_e32 v10, 0
	v_mov_b32_e32 v11, 0
	v_pk_mul_f32 v[6:7], v[154:155], v[2:3] op_sel_hi:[1,0]
	v_pk_mul_f32 v[12:13], v[156:157], v[2:3] op_sel_hi:[1,0]
	v_pk_mul_f32 v[14:15], v[150:151], v[2:3] op_sel_hi:[1,0]
	v_exp_f32_e32 v6, v6
	v_pk_mul_f32 v[16:17], v[152:153], v[2:3] op_sel_hi:[1,0]
	v_exp_f32_e32 v12, v12
	v_pk_mul_f32 v[18:19], v[142:143], v[2:3] op_sel_hi:[1,0]
	v_exp_f32_e32 v14, v14
	v_pk_mul_f32 v[20:21], v[144:145], v[2:3] op_sel_hi:[1,0]
	v_exp_f32_e32 v16, v16
	v_pk_mul_f32 v[22:23], v[134:135], v[2:3] op_sel_hi:[1,0]
	v_exp_f32_e32 v7, v7
	v_pk_mul_f32 v[24:25], v[136:137], v[2:3] op_sel_hi:[1,0]
	v_exp_f32_e32 v13, v13
	v_pk_mul_f32 v[26:27], v[126:127], v[2:3] op_sel_hi:[1,0]
	v_exp_f32_e32 v15, v15
	v_pk_mul_f32 v[28:29], v[128:129], v[2:3] op_sel_hi:[1,0]
	v_exp_f32_e32 v17, v17
	v_pk_mul_f32 v[30:31], v[118:119], v[2:3] op_sel_hi:[1,0]
	v_exp_f32_e32 v18, v18
	v_pk_add_f32 v[6:7], v[6:7], v[2:3] op_sel:[0,1] op_sel_hi:[1,1]
	v_exp_f32_e32 v20, v20
	v_pk_add_f32 v[12:13], v[12:13], v[2:3] op_sel:[0,1] op_sel_hi:[1,1]
	v_exp_f32_e32 v22, v22
	v_pk_add_f32 v[14:15], v[14:15], v[2:3] op_sel:[0,1] op_sel_hi:[1,1]
	v_rcp_f32_e32 v6, v6
	v_pk_add_f32 v[16:17], v[16:17], v[2:3] op_sel:[0,1] op_sel_hi:[1,1]
	v_exp_f32_e32 v24, v24
	v_pk_mul_f32 v[32:33], v[120:121], v[2:3] op_sel_hi:[1,0]
	v_rcp_f32_e32 v12, v12
	v_pk_mul_f32 v[196:197], v[154:155], v[158:159]
	v_rcp_f32_e32 v14, v14
	v_pk_mul_f32 v[198:199], v[110:111], v[2:3] op_sel_hi:[1,0]
	v_exp_f32_e32 v19, v19
	v_pk_mul_f32 v[200:201], v[156:157], v[160:161]
	v_rcp_f32_e32 v16, v16
	v_pk_mul_f32 v[202:203], v[150:151], v[146:147]
	v_exp_f32_e32 v21, v21
	v_pk_mul_f32 v[214:215], v[112:113], v[2:3] op_sel_hi:[1,0]
	v_exp_f32_e32 v23, v23
	v_pk_mul_f32 v[216:217], v[102:103], v[2:3] op_sel_hi:[1,0]
	v_rcp_f32_e32 v7, v7
	v_pk_add_f32 v[18:19], v[18:19], v[2:3] op_sel:[0,1] op_sel_hi:[1,1]
	v_exp_f32_e32 v25, v25
	v_pk_mul_f32 v[218:219], v[152:153], v[148:149]
	v_exp_f32_e32 v26, v26
	v_pk_add_f32 v[20:21], v[20:21], v[2:3] op_sel:[0,1] op_sel_hi:[1,1]
	v_rcp_f32_e32 v13, v13
	v_pk_add_f32 v[22:23], v[22:23], v[2:3] op_sel:[0,1] op_sel_hi:[1,1]
	v_rcp_f32_e32 v15, v15
	v_pk_mul_f32 v[196:197], v[196:197], v[6:7]
	v_exp_f32_e32 v28, v28
	v_pk_add_f32 v[24:25], v[24:25], v[2:3] op_sel:[0,1] op_sel_hi:[1,1]
	v_exp_f32_e32 v30, v30
	v_pk_mul_f32 v[196:197], v[196:197], v[4:5] op_sel_hi:[1,0]
	v_rcp_f32_e32 v17, v17
	v_pk_mul_f32 v[200:201], v[200:201], v[12:13]
	v_rcp_f32_e32 v18, v18
	v_pk_mul_f32 v[202:203], v[202:203], v[14:15]
	v_exp_f32_e32 v32, v32
	v_med3_f32 v196, v196, s87, v227
	v_rcp_f32_e32 v20, v20
	v_pk_mul_f32 v[200:201], v[200:201], v[4:5] op_sel_hi:[1,0]
	v_rcp_f32_e32 v22, v22
	v_pk_mul_f32 v[202:203], v[202:203], v[4:5] op_sel_hi:[1,0]
	v_exp_f32_e32 v27, v27
	v_pk_mul_f32 v[218:219], v[218:219], v[16:17]
	v_rcp_f32_e32 v24, v24
	v_med3_f32 v197, v197, s87, v227
	v_exp_f32_e32 v29, v29
	v_med3_f32 v200, v200, s87, v227
	v_exp_f32_e32 v31, v31
	v_med3_f32 v202, v202, s87, v227
	v_rcp_f32_e32 v19, v19
	v_pk_mul_f32 v[218:219], v[218:219], v[4:5] op_sel_hi:[1,0]
	v_exp_f32_e32 v33, v33
	v_pk_add_f32 v[26:27], v[26:27], v[2:3] op_sel:[0,1] op_sel_hi:[1,1]
	v_exp_f32_e32 v198, v198
	v_pk_mul_f32 v[6:7], v[104:105], v[2:3] op_sel_hi:[1,0]
	v_rcp_f32_e32 v21, v21
	v_cvt_pk_fp8_f32 v12, v196, v197
	v_rcp_f32_e32 v23, v23
	v_med3_f32 v201, v201, s87, v227
	v_exp_f32_e32 v214, v214
	v_med3_f32 v203, v203, s87, v227
	v_exp_f32_e32 v216, v216
	v_med3_f32 v218, v218, s87, v227
	v_rcp_f32_e32 v25, v25
	v_pk_add_f32 v[28:29], v[28:29], v[2:3] op_sel:[0,1] op_sel_hi:[1,1]
	v_rcp_f32_e32 v26, v26
	v_pk_add_f32 v[30:31], v[30:31], v[2:3] op_sel:[0,1] op_sel_hi:[1,1]
	v_exp_f32_e32 v6, v6
	v_cvt_pk_fp8_f32 v12, v200, v201 op_sel:[0,0,1]
	v_cvt_pk_fp8_f32 v13, v202, v203
	v_med3_f32 v219, v219, s87, v227
	v_rcp_f32_e32 v28, v28
	v_pk_add_f32 v[32:33], v[32:33], v[2:3] op_sel:[0,1] op_sel_hi:[1,1]
	v_rcp_f32_e32 v30, v30
	v_pk_mul_f32 v[14:15], v[142:143], v[138:139]
	v_exp_f32_e32 v199, v199
	v_cvt_pk_fp8_f32 v13, v218, v219 op_sel:[0,0,1]
	v_pk_mul_f32 v[14:15], v[14:15], v[18:19]
	v_rcp_f32_e32 v32, v32
	v_pk_mul_f32 v[16:17], v[94:95], v[2:3] op_sel_hi:[1,0]
	v_pk_mul_f32 v[14:15], v[14:15], v[4:5] op_sel_hi:[1,0]
	v_exp_f32_e32 v215, v215
	v_pk_mul_f32 v[18:19], v[144:145], v[140:141]
	v_exp_f32_e32 v217, v217
	v_med3_f32 v14, v14, s87, v227
	v_pk_mul_f32 v[18:19], v[18:19], v[20:21]
	v_pk_mul_f32 v[20:21], v[134:135], v[130:131]
	v_rcp_f32_e32 v27, v27
	v_pk_mul_f32 v[18:19], v[18:19], v[4:5] op_sel_hi:[1,0]
	v_pk_mul_f32 v[20:21], v[20:21], v[22:23]
	global_store_dwordx2 v249, v[12:13], s[36:37]
	v_exp_f32_e32 v7, v7
	v_pk_mul_f32 v[20:21], v[20:21], v[4:5] op_sel_hi:[1,0]
	v_exp_f32_e32 v16, v16
	v_pk_mul_f32 v[12:13], v[96:97], v[2:3] op_sel_hi:[1,0]
	v_pk_mul_f32 v[22:23], v[86:87], v[2:3] op_sel_hi:[1,0]
	v_med3_f32 v15, v15, s87, v227
	v_med3_f32 v18, v18, s87, v227
	v_med3_f32 v20, v20, s87, v227
	v_pk_mul_f32 v[196:197], v[136:137], v[132:133]
	v_rcp_f32_e32 v29, v29
	v_pk_add_f32 v[198:199], v[198:199], v[2:3] op_sel:[0,1] op_sel_hi:[1,1]
	v_pk_mul_f32 v[196:197], v[196:197], v[24:25]
	v_rcp_f32_e32 v31, v31
	v_pk_mul_f32 v[24:25], v[88:89], v[2:3] op_sel_hi:[1,0]
	v_pk_mul_f32 v[196:197], v[196:197], v[4:5] op_sel_hi:[1,0]
	v_exp_f32_e32 v12, v12
	v_cvt_pk_fp8_f32 v14, v14, v15
	v_exp_f32_e32 v22, v22
	v_med3_f32 v19, v19, s87, v227
	v_med3_f32 v21, v21, s87, v227
	v_med3_f32 v196, v196, s87, v227
	v_rcp_f32_e32 v33, v33
	v_pk_add_f32 v[214:215], v[214:215], v[2:3] op_sel:[0,1] op_sel_hi:[1,1]
	v_rcp_f32_e32 v198, v198
	v_pk_add_f32 v[216:217], v[216:217], v[2:3] op_sel:[0,1] op_sel_hi:[1,1]
	v_exp_f32_e32 v24, v24
	v_cvt_pk_fp8_f32 v14, v18, v19 op_sel:[0,0,1]
	v_cvt_pk_fp8_f32 v15, v20, v21
	v_med3_f32 v197, v197, s87, v227
	v_rcp_f32_e32 v214, v214
	v_pk_add_f32 v[6:7], v[6:7], v[2:3] op_sel:[0,1] op_sel_hi:[1,1]
	v_rcp_f32_e32 v216, v216
	v_pk_mul_f32 v[18:19], v[126:127], v[122:123]
	v_exp_f32_e32 v17, v17
	v_cvt_pk_fp8_f32 v15, v196, v197 op_sel:[0,0,1]
	v_pk_mul_f32 v[18:19], v[18:19], v[26:27]
	v_rcp_f32_e32 v6, v6
	v_pk_mul_f32 v[20:21], v[78:79], v[2:3] op_sel_hi:[1,0]
	v_pk_mul_f32 v[18:19], v[18:19], v[4:5] op_sel_hi:[1,0]
	v_exp_f32_e32 v13, v13
	v_pk_mul_f32 v[26:27], v[128:129], v[124:125]
	v_exp_f32_e32 v23, v23
	v_med3_f32 v18, v18, s87, v227
	v_pk_mul_f32 v[26:27], v[26:27], v[28:29]
	v_pk_mul_f32 v[28:29], v[118:119], v[114:115]
	v_rcp_f32_e32 v199, v199
	v_pk_mul_f32 v[26:27], v[26:27], v[4:5] op_sel_hi:[1,0]
	v_pk_mul_f32 v[28:29], v[28:29], v[30:31]
	v_exp_f32_e32 v25, v25
	v_pk_mul_f32 v[30:31], v[80:81], v[2:3] op_sel_hi:[1,0]
	v_pk_mul_f32 v[28:29], v[28:29], v[4:5] op_sel_hi:[1,0]
	v_exp_f32_e32 v20, v20
	v_pk_mul_f32 v[196:197], v[70:71], v[2:3] op_sel_hi:[1,0]
	v_med3_f32 v19, v19, s87, v227
	v_med3_f32 v26, v26, s87, v227
	v_med3_f32 v28, v28, s87, v227
	v_pk_mul_f32 v[200:201], v[120:121], v[116:117]
	v_rcp_f32_e32 v215, v215
	v_pk_add_f32 v[16:17], v[16:17], v[2:3] op_sel:[0,1] op_sel_hi:[1,1]
	v_pk_mul_f32 v[200:201], v[200:201], v[32:33]
	v_rcp_f32_e32 v217, v217
	v_pk_mul_f32 v[32:33], v[72:73], v[2:3] op_sel_hi:[1,0]
	v_pk_mul_f32 v[200:201], v[200:201], v[4:5] op_sel_hi:[1,0]
	v_exp_f32_e32 v30, v30
	v_cvt_pk_fp8_f32 v18, v18, v19
	v_exp_f32_e32 v196, v196
	v_med3_f32 v27, v27, s87, v227
	v_med3_f32 v29, v29, s87, v227
	v_med3_f32 v200, v200, s87, v227
	v_rcp_f32_e32 v7, v7
	v_pk_add_f32 v[12:13], v[12:13], v[2:3] op_sel:[0,1] op_sel_hi:[1,1]
	v_rcp_f32_e32 v16, v16
	v_pk_add_f32 v[22:23], v[22:23], v[2:3] op_sel:[0,1] op_sel_hi:[1,1]
	v_exp_f32_e32 v32, v32
	v_cvt_pk_fp8_f32 v18, v26, v27 op_sel:[0,0,1]
	v_cvt_pk_fp8_f32 v19, v28, v29
	v_med3_f32 v201, v201, s87, v227
	v_rcp_f32_e32 v12, v12
	v_pk_add_f32 v[24:25], v[24:25], v[2:3] op_sel:[0,1] op_sel_hi:[1,1]
	v_rcp_f32_e32 v22, v22
	v_pk_mul_f32 v[26:27], v[110:111], v[106:107]
	v_exp_f32_e32 v21, v21
	v_cvt_pk_fp8_f32 v19, v200, v201 op_sel:[0,0,1]
	v_pk_mul_f32 v[26:27], v[26:27], v[198:199]
	v_rcp_f32_e32 v24, v24
	v_pk_mul_f32 v[28:29], v[62:63], v[2:3] op_sel_hi:[1,0]
	v_pk_mul_f32 v[26:27], v[26:27], v[4:5] op_sel_hi:[1,0]
	v_exp_f32_e32 v31, v31
	v_pk_mul_f32 v[198:199], v[112:113], v[108:109]
	v_exp_f32_e32 v197, v197
	v_med3_f32 v26, v26, s87, v227
	v_pk_mul_f32 v[198:199], v[198:199], v[214:215]
	v_pk_mul_f32 v[200:201], v[102:103], v[98:99]
	v_rcp_f32_e32 v17, v17
	v_pk_mul_f32 v[198:199], v[198:199], v[4:5] op_sel_hi:[1,0]
	v_pk_mul_f32 v[200:201], v[200:201], v[216:217]
	v_exp_f32_e32 v33, v33
	v_pk_mul_f32 v[202:203], v[64:65], v[2:3] op_sel_hi:[1,0]
	v_pk_mul_f32 v[200:201], v[200:201], v[4:5] op_sel_hi:[1,0]
	v_exp_f32_e32 v28, v28
	v_pk_mul_f32 v[214:215], v[54:55], v[2:3] op_sel_hi:[1,0]
	v_med3_f32 v27, v27, s87, v227
	v_med3_f32 v198, v198, s87, v227
	v_med3_f32 v200, v200, s87, v227
	v_pk_mul_f32 v[216:217], v[104:105], v[100:101]
	v_rcp_f32_e32 v13, v13
	v_pk_add_f32 v[20:21], v[20:21], v[2:3] op_sel:[0,1] op_sel_hi:[1,1]
	v_pk_mul_f32 v[216:217], v[216:217], v[6:7]
	v_rcp_f32_e32 v23, v23
	v_add_u32_e32 v6, 0xe000, v249
	v_pk_mul_f32 v[216:217], v[216:217], v[4:5] op_sel_hi:[1,0]
	v_exp_f32_e32 v202, v202
	global_store_dwordx2 v6, v[14:15], s[36:37]
	v_exp_f32_e32 v214, v214
	v_pk_mul_f32 v[6:7], v[56:57], v[2:3] op_sel_hi:[1,0]
	v_cvt_pk_fp8_f32 v14, v26, v27
	v_med3_f32 v199, v199, s87, v227
	v_med3_f32 v201, v201, s87, v227
	v_med3_f32 v216, v216, s87, v227
	v_rcp_f32_e32 v25, v25
	v_pk_add_f32 v[30:31], v[30:31], v[2:3] op_sel:[0,1] op_sel_hi:[1,1]
	v_rcp_f32_e32 v20, v20
	v_pk_add_f32 v[196:197], v[196:197], v[2:3] op_sel:[0,1] op_sel_hi:[1,1]
	v_exp_f32_e32 v6, v6
	v_cvt_pk_fp8_f32 v14, v198, v199 op_sel:[0,0,1]
	v_cvt_pk_fp8_f32 v15, v200, v201
	v_med3_f32 v217, v217, s87, v227
	v_rcp_f32_e32 v30, v30
	v_pk_add_f32 v[32:33], v[32:33], v[2:3] op_sel:[0,1] op_sel_hi:[1,1]
	v_rcp_f32_e32 v196, v196
	v_pk_mul_f32 v[26:27], v[94:95], v[90:91]
	v_exp_f32_e32 v29, v29
	v_cvt_pk_fp8_f32 v15, v216, v217 op_sel:[0,0,1]
	v_pk_mul_f32 v[26:27], v[26:27], v[16:17]
	v_rcp_f32_e32 v32, v32
	v_pk_mul_f32 v[16:17], v[46:47], v[2:3] op_sel_hi:[1,0]
	v_pk_mul_f32 v[26:27], v[26:27], v[4:5] op_sel_hi:[1,0]
	v_exp_f32_e32 v203, v203
	v_pk_mul_f32 v[198:199], v[96:97], v[92:93]
	v_exp_f32_e32 v215, v215
	v_med3_f32 v26, v26, s87, v227
	v_pk_mul_f32 v[198:199], v[198:199], v[12:13]
	v_pk_mul_f32 v[12:13], v[86:87], v[82:83]
	v_rcp_f32_e32 v21, v21
	v_pk_mul_f32 v[198:199], v[198:199], v[4:5] op_sel_hi:[1,0]
	v_pk_mul_f32 v[12:13], v[12:13], v[22:23]
	v_exp_f32_e32 v7, v7
	v_pk_mul_f32 v[22:23], v[48:49], v[2:3] op_sel_hi:[1,0]
	v_pk_mul_f32 v[12:13], v[12:13], v[4:5] op_sel_hi:[1,0]
	v_exp_f32_e32 v16, v16
	v_pk_mul_f32 v[200:201], v[38:39], v[2:3] op_sel_hi:[1,0]
	v_med3_f32 v27, v27, s87, v227
	v_med3_f32 v198, v198, s87, v227
	v_med3_f32 v12, v12, s87, v227
	v_pk_mul_f32 v[216:217], v[88:89], v[84:85]
	v_rcp_f32_e32 v31, v31
	v_pk_add_f32 v[28:29], v[28:29], v[2:3] op_sel:[0,1] op_sel_hi:[1,1]
	v_pk_mul_f32 v[216:217], v[216:217], v[24:25]
	v_rcp_f32_e32 v197, v197
	v_add_u32_e32 v24, 0x1c000, v249
	v_pk_mul_f32 v[216:217], v[216:217], v[4:5] op_sel_hi:[1,0]
	v_exp_f32_e32 v22, v22
	global_store_dwordx2 v24, v[18:19], s[36:37]
	v_exp_f32_e32 v200, v200
	v_pk_mul_f32 v[18:19], v[40:41], v[2:3] op_sel_hi:[1,0]
	v_cvt_pk_fp8_f32 v24, v26, v27
	v_med3_f32 v199, v199, s87, v227
	v_med3_f32 v13, v13, s87, v227
	v_med3_f32 v216, v216, s87, v227
	v_rcp_f32_e32 v33, v33
	v_pk_add_f32 v[202:203], v[202:203], v[2:3] op_sel:[0,1] op_sel_hi:[1,1]
	v_rcp_f32_e32 v28, v28
	v_pk_add_f32 v[214:215], v[214:215], v[2:3] op_sel:[0,1] op_sel_hi:[1,1]
	v_exp_f32_e32 v18, v18
	v_cvt_pk_fp8_f32 v24, v198, v199 op_sel:[0,0,1]
	v_cvt_pk_fp8_f32 v25, v12, v13
	v_med3_f32 v217, v217, s87, v227
	v_rcp_f32_e32 v202, v202
	v_pk_add_f32 v[6:7], v[6:7], v[2:3] op_sel:[0,1] op_sel_hi:[1,1]
	v_rcp_f32_e32 v214, v214
	v_pk_mul_f32 v[12:13], v[78:79], v[74:75]
	v_exp_f32_e32 v17, v17
	v_cvt_pk_fp8_f32 v25, v216, v217 op_sel:[0,0,1]
	v_pk_mul_f32 v[12:13], v[12:13], v[20:21]
	v_rcp_f32_e32 v6, v6
	v_pk_mul_f32 v[20:21], v[80:81], v[76:77]
	v_pk_mul_f32 v[12:13], v[12:13], v[4:5] op_sel_hi:[1,0]
	v_exp_f32_e32 v23, v23
	v_pk_mul_f32 v[20:21], v[20:21], v[30:31]
	v_exp_f32_e32 v201, v201
	v_med3_f32 v12, v12, s87, v227
	v_pk_mul_f32 v[20:21], v[20:21], v[4:5] op_sel_hi:[1,0]
	v_pk_mul_f32 v[26:27], v[70:71], v[66:67]
	v_rcp_f32_e32 v29, v29
	v_med3_f32 v13, v13, s87, v227
	v_pk_mul_f32 v[26:27], v[26:27], v[196:197]
	v_exp_f32_e32 v19, v19
	v_med3_f32 v20, v20, s87, v227
	v_pk_mul_f32 v[26:27], v[26:27], v[4:5] op_sel_hi:[1,0]
	v_pk_mul_f32 v[30:31], v[72:73], v[68:69]
	v_rcp_f32_e32 v203, v203
	v_med3_f32 v26, v26, s87, v227
	v_pk_mul_f32 v[30:31], v[30:31], v[32:33]
	v_rcp_f32_e32 v215, v215
	v_pk_add_f32 v[16:17], v[16:17], v[2:3] op_sel:[0,1] op_sel_hi:[1,1]
	v_pk_mul_f32 v[30:31], v[30:31], v[4:5] op_sel_hi:[1,0]
	v_add_u32_e32 v32, 0x2a000, v249
	v_cvt_pk_fp8_f32 v12, v12, v13
	v_med3_f32 v21, v21, s87, v227
	global_store_dwordx2 v32, v[14:15], s[36:37]
	v_med3_f32 v27, v27, s87, v227
	v_med3_f32 v30, v30, s87, v227
	v_rcp_f32_e32 v7, v7
	v_pk_add_f32 v[22:23], v[22:23], v[2:3] op_sel:[0,1] op_sel_hi:[1,1]
	v_rcp_f32_e32 v16, v16
	v_pk_add_f32 v[200:201], v[200:201], v[2:3] op_sel:[0,1] op_sel_hi:[1,1]
	v_cvt_pk_fp8_f32 v12, v20, v21 op_sel:[0,0,1]
	v_cvt_pk_fp8_f32 v13, v26, v27
	v_med3_f32 v31, v31, s87, v227
	v_rcp_f32_e32 v22, v22
	v_pk_add_f32 v[18:19], v[18:19], v[2:3] op_sel:[0,1] op_sel_hi:[1,1]
	v_rcp_f32_e32 v200, v200
	v_pk_mul_f32 v[14:15], v[62:63], v[58:59]
	v_cvt_pk_fp8_f32 v13, v30, v31 op_sel:[0,0,1]
	v_rcp_f32_e32 v18, v18
	v_pk_mul_f32 v[14:15], v[14:15], v[28:29]
	v_pk_mul_f32 v[20:21], v[64:65], v[60:61]
	v_pk_mul_f32 v[26:27], v[54:55], v[50:51]
	v_pk_mul_f32 v[14:15], v[14:15], v[4:5] op_sel_hi:[1,0]
	v_pk_mul_f32 v[20:21], v[20:21], v[202:203]
	v_pk_mul_f32 v[26:27], v[26:27], v[214:215]
	v_med3_f32 v14, v14, s87, v227
	v_pk_mul_f32 v[20:21], v[20:21], v[4:5] op_sel_hi:[1,0]
	v_pk_mul_f32 v[26:27], v[26:27], v[4:5] op_sel_hi:[1,0]
	v_rcp_f32_e32 v17, v17
	v_med3_f32 v15, v15, s87, v227
	v_med3_f32 v20, v20, s87, v227
	v_med3_f32 v26, v26, s87, v227
	v_pk_mul_f32 v[28:29], v[56:57], v[52:53]
	v_rcp_f32_e32 v23, v23
	v_add_u32_e32 v30, 0x70000, v249
	v_pk_mul_f32 v[28:29], v[28:29], v[6:7]
	v_rcp_f32_e32 v201, v201
	global_store_dwordx2 v30, v[24:25], s[36:37]
	v_pk_mul_f32 v[28:29], v[28:29], v[4:5] op_sel_hi:[1,0]
	v_cvt_pk_fp8_f32 v6, v14, v15
	v_med3_f32 v21, v21, s87, v227
	v_med3_f32 v27, v27, s87, v227
	v_med3_f32 v28, v28, s87, v227
	v_rcp_f32_e32 v19, v19
	v_cvt_pk_fp8_f32 v6, v20, v21 op_sel:[0,0,1]
	v_cvt_pk_fp8_f32 v7, v26, v27
	v_med3_f32 v29, v29, s87, v227
	v_pk_mul_f32 v[14:15], v[46:47], v[42:43]
	v_pk_mul_f32 v[20:21], v[48:49], v[44:45]
	v_cvt_pk_fp8_f32 v7, v28, v29 op_sel:[0,0,1]
	v_pk_mul_f32 v[14:15], v[14:15], v[16:17]
	v_pk_mul_f32 v[20:21], v[20:21], v[22:23]
	v_pk_mul_f32 v[16:17], v[38:39], v[34:35]
	v_pk_mul_f32 v[14:15], v[14:15], v[4:5] op_sel_hi:[1,0]
	v_pk_mul_f32 v[20:21], v[20:21], v[4:5] op_sel_hi:[1,0]
	v_pk_mul_f32 v[16:17], v[16:17], v[200:201]
	v_med3_f32 v14, v14, s87, v227
	v_med3_f32 v20, v20, s87, v227
	v_pk_mul_f32 v[16:17], v[16:17], v[4:5] op_sel_hi:[1,0]
	v_med3_f32 v15, v15, s87, v227
	v_pk_mul_f32 v[22:23], v[40:41], v[36:37]
	v_med3_f32 v16, v16, s87, v227
	v_add_u32_e32 v24, 0x7e000, v249
	v_pk_mul_f32 v[22:23], v[22:23], v[18:19]
	v_cvt_pk_fp8_f32 v14, v14, v15
	global_store_dwordx2 v24, v[12:13], s[36:37]
	v_pk_mul_f32 v[22:23], v[22:23], v[4:5] op_sel_hi:[1,0]
	v_med3_f32 v21, v21, s87, v227
	v_med3_f32 v17, v17, s87, v227
	v_med3_f32 v22, v22, s87, v227
	v_cvt_pk_fp8_f32 v14, v20, v21 op_sel:[0,0,1]
	v_cvt_pk_fp8_f32 v15, v16, v17
	v_med3_f32 v23, v23, s87, v227
	v_add_u32_e32 v12, 0x8c000, v249
	v_add_u32_e32 v13, 0x9a000, v249
	v_cvt_pk_fp8_f32 v15, v22, v23 op_sel:[0,0,1]
	global_store_dwordx2 v12, v[6:7], s[36:37]
	v_mfma_f32_32x32x16_bf16 v[34:49], v[8:11], v[8:11], 0
	global_store_dwordx2 v13, v[14:15], s[36:37]
	v_mfma_f32_32x32x16_bf16 v[50:65], v[8:11], v[8:11], 0
	v_mfma_f32_32x32x16_bf16 v[66:81], v[8:11], v[8:11], 0
	v_mfma_f32_32x32x16_bf16 v[82:97], v[8:11], v[8:11], 0
	v_mfma_f32_32x32x16_bf16 v[98:113], v[8:11], v[8:11], 0
	v_mfma_f32_32x32x16_bf16 v[114:129], v[8:11], v[8:11], 0
	v_mfma_f32_32x32x16_bf16 v[130:145], v[8:11], v[8:11], 0
	v_mfma_f32_32x32x16_bf16 v[146:161], v[8:11], v[8:11], 0
	s_nop 15
	s_mov_b64 s[54:55], -1
	s_and_b64 vcc, exec, s[50:51]
	s_cbranch_vccz .LBB0_1818
	s_andn2_b64 vcc, exec, s[34:35]
	s_cbranch_vccnz .LBB0_1817
	s_barrier
	s_branch .LBB0_1817
